# speedup vs baseline: 1.0053x; 1.0053x over previous
.Lmy_noperm_in:
	v_mfma_f32_16x16x32_f16 v[210:213], v[70:73], v[150:153], v[98:101]
	v_mfma_f32_16x16x32_f16 v[214:217], v[74:77], v[150:153], v[102:105]
	v_mfma_f32_16x16x32_f16 v[210:213], v[66:69], v[154:157], v[210:213]
	v_mfma_f32_16x16x32_f16 v[214:217], v[78:81], v[154:157], v[214:217]
	s_add_u32 s48, s20, 0x600000
	s_addc_u32 s49, s21, 0
	s_sub_u32 s50, s22, 0x600000
	s_mov_b32 s51, s23
	s_add_u32 s68, s16, 0xc000
	s_addc_u32 s69, s17, 0
	s_sub_u32 s70, s18, 0xc000
	s_mov_b32 s71, s19
	s_add_u32 s52, s20, 0x700000
	s_addc_u32 s53, s21, 0
	s_sub_u32 s54, s22, 0x700000
	s_mov_b32 s55, s23
	s_add_u32 s72, s16, 0x10000
	s_addc_u32 s73, s17, 0
	s_sub_u32 s74, s18, 0x10000
	s_mov_b32 s75, s19
	s_add_u32 s56, s20, 0x800000
	s_addc_u32 s57, s21, 0
	s_sub_u32 s58, s22, 0x800000
	s_mov_b32 s59, s23
	s_add_u32 s76, s16, 0x14000
	s_addc_u32 s77, s17, 0
	s_sub_u32 s78, s18, 0x14000
	s_mov_b32 s79, s19
	s_add_u32 s60, s20, 0x900000
	s_addc_u32 s61, s21, 0
	s_sub_u32 s62, s22, 0x900000
	s_mov_b32 s63, s23
	s_add_u32 s80, s16, 0x18000
	s_addc_u32 s81, s17, 0
	s_sub_u32 s82, s18, 0x18000
	s_mov_b32 s83, s19
	ds_read_b128 v[158:161], v248 offset:0
	ds_read_b128 v[162:165], v248 offset:1024
	ds_read_b128 v[166:169], v249 offset:2048
	ds_read_b128 v[170:173], v249 offset:3072
	v_mfma_f32_16x16x32_f16 v[218:221], v[82:85], v[150:153], v[106:109]
	v_mfma_f32_16x16x32_f16 v[222:225], v[90:93], v[150:153], v[110:113]
	v_mfma_f32_16x16x32_f16 v[218:221], v[86:89], v[154:157], v[218:221]
	v_mfma_f32_16x16x32_f16 v[222:225], v[94:97], v[154:157], v[222:225]
	s_waitcnt lgkmcnt(2)
	v_mfma_f32_16x16x32_f16 v[210:213], v[54:57], v[158:161], v[210:213]
	v_mfma_f32_16x16x32_f16 v[210:213], v[58:61], v[162:165], v[210:213]
	s_waitcnt lgkmcnt(0)
	v_mfma_f32_16x16x32_f16 v[210:213], v[62:65], v[166:169], v[210:213]
	v_mfma_f32_16x16x32_f16 v[210:213], v[50:53], v[170:173], v[210:213]
	s_waitcnt vmcnt(9)
	v_cvt_pk_f16_f32 v251, v196, v197
	ds_write_b32 v1, v251 offset:4096
	ds_read_b128 v[150:153], v186 offset:2048
	ds_read_b128 v[154:157], v186 offset:3072
	s_add_i32 s45, s45, 0x100000
	s_add_i32 s46, s46, 0x4000
	s_movk_i32 s47, 0x0
	s_add_i32 s43, s40, -12
	s_lshl_b32 s43, s43, 12
	s_cmp_lt_u32 s40, 14
	s_cselect_b32 s43, s47, s43
	v_exp_f32_e32 v226, v210
	v_exp_f32_e32 v227, v211
	v_mfma_f32_16x16x32_f16 v[214:217], v[34:37], v[158:161], v[214:217]
	v_min_f32_e32 v228, s42, v212
	v_exp_f32_e32 v229, v213
	v_mfma_f32_16x16x32_f16 v[214:217], v[38:41], v[162:165], v[214:217]
	v_exp_f32_e32 v228, v228
	v_add_f32_e32 v227, 1.0, v227
	v_mfma_f32_16x16x32_f16 v[214:217], v[42:45], v[166:169], v[214:217]
	v_fma_f32 v230, v228, s41, s41
	v_rcp_f32_e32 v227, v227
	v_mfma_f32_16x16x32_f16 v[214:217], v[46:49], v[170:173], v[214:217]
	v_fma_f32 v230, v226, v230, v230
	v_rcp_f32_e32 v230, v230
	v_mfma_f32_16x16x32_f16 v[218:221], v[18:21], v[158:161], v[218:221]
	v_fma_f32 v226, -v228, v230, v230
	v_fma_f32 v200, v200, v227, v226
	v_mfma_f32_16x16x32_f16 v[218:221], v[14:17], v[162:165], v[218:221]
	v_exp_f32_e32 v226, v200
	s_nop 0
	v_add_f32_e32 v227, 1.0, v226
	v_mfma_f32_16x16x32_f16 v[218:221], v[10:13], v[166:169], v[218:221]
	v_fma_f32 v227, v229, v227, v227
	v_rcp_f32_e32 v227, v227
	v_mfma_f32_16x16x32_f16 v[218:221], v[26:29], v[170:173], v[218:221]
	v_fma_f32 v226, -v226, v227, v227
	v_exp_f32_e32 v231, v214
	v_mfma_f32_16x16x32_f16 v[222:225], v[2:5], v[158:161], v[222:225]
	v_exp_f32_e32 v232, v215
	v_min_f32_e32 v233, s42, v216
	v_mfma_f32_16x16x32_f16 v[222:225], v[6:9], v[162:165], v[222:225]
	v_exp_f32_e32 v234, v217
	v_exp_f32_e32 v233, v233
	v_mfma_f32_16x16x32_f16 v[222:225], v[22:25], v[166:169], v[222:225]
	v_exp_f32_e32 v236, v218
	v_add_f32_e32 v232, 1.0, v232
	v_mfma_f32_16x16x32_f16 v[222:225], v[30:33], v[170:173], v[222:225]
	v_fma_f32 v235, v233, s41, s41
	v_exp_f32_e32 v227, v219
	v_rcp_f32_e32 v232, v232
	v_fma_f32 v235, v231, v235, v235
	v_min_f32_e32 v228, s42, v220
	v_rcp_f32_e32 v235, v235
	s_nop 0
	v_fma_f32 v231, -v233, v235, v235
	v_exp_f32_e32 v229, v221
	v_fma_f32 v201, v201, v232, v231
	v_exp_f32_e32 v231, v201
	v_exp_f32_e32 v228, v228
	v_add_f32_e32 v232, 1.0, v231
	v_fma_f32 v232, v234, v232, v232
	v_add_f32_e32 v227, 1.0, v227
	v_rcp_f32_e32 v232, v232
	v_mfma_f32_16x16x32_f16 v[146:149], v[138:141], v[158:161], v[146:149]
	v_fma_f32 v231, -v231, v232, v232
	v_fma_f32 v230, v228, s41, s41
	v_cvt_pk_f16_f32 v246, v226, v231
	v_mfma_f32_16x16x32_f16 v[146:149], v[142:145], v[162:165], v[146:149]
	v_exp_f32_e32 v231, v222
	v_rcp_f32_e32 v227, v227
	v_exp_f32_e32 v232, v223
	buffer_load_dwordx4 v[138:141], v189, s[16:19], s46 offen
	buffer_load_dwordx4 v[142:145], v208, s[16:19], s46 offen
	v_min_f32_e32 v233, s42, v224
	v_fma_f32 v230, v236, v230, v230
	v_exp_f32_e32 v234, v225
	s_waitcnt lgkmcnt(0)
	v_mfma_f32_16x16x32_f16 v[210:213], v[70:73], v[150:153], v[98:101]
	v_exp_f32_e32 v233, v233
	v_rcp_f32_e32 v230, v230
	v_add_f32_e32 v232, 1.0, v232
	v_mfma_f32_16x16x32_f16 v[214:217], v[74:77], v[150:153], v[102:105]
	v_fma_f32 v235, v233, s41, s41
	v_fma_f32 v236, -v228, v230, v230
	v_rcp_f32_e32 v232, v232
	v_fma_f32 v235, v231, v235, v235
	v_fma_f32 v198, v198, v227, v236
	v_rcp_f32_e32 v235, v235
	s_nop 0
	v_fma_f32 v231, -v233, v235, v235
	v_exp_f32_e32 v236, v198
	v_fma_f32 v199, v199, v232, v231
	v_exp_f32_e32 v231, v199
	v_add_f32_e32 v227, 1.0, v236
	v_add_f32_e32 v232, 1.0, v231
	v_add_u32_e32 v250, s43, v206
	v_fma_f32 v232, v234, v232, v232
	v_fma_f32 v227, v229, v227, v227
	v_add_u32_e32 v248, s43, v252
	v_rcp_f32_e32 v232, v232
	s_nop 0
	v_fma_f32 v231, -v231, v232, v232
	v_add_u32_e32 v249, s43, v253
	v_rcp_f32_e32 v227, v227
	s_nop 0
	v_fma_f32 v236, -v236, v227, v227
	v_cvt_pk_f16_f32 v247, v236, v231
	ds_write_b64 v250, v[246:247] offset:8192
	v_mfma_f32_16x16x32_f16 v[210:213], v[66:69], v[154:157], v[210:213]
	v_mfma_f32_16x16x32_f16 v[214:217], v[78:81], v[154:157], v[214:217]
	v_mov_b32_e32 v174, v246
	v_mov_b32_e32 v175, v247
	buffer_load_dwordx2 v[196:197], v209, s[20:23], s45 offen
	s_add_i32 s40, s40, 1
	s_add_i32 s44, s44, 0x1000
	s_waitcnt lgkmcnt(0)
	s_barrier
	ds_read_b128 v[158:161], v248 offset:0
	ds_read_b128 v[162:165], v248 offset:1024
	ds_read_b128 v[166:169], v249 offset:2048
	ds_read_b128 v[170:173], v249 offset:3072
	v_mfma_f32_16x16x32_f16 v[218:221], v[82:85], v[150:153], v[106:109]
	v_mfma_f32_16x16x32_f16 v[222:225], v[90:93], v[150:153], v[110:113]
	v_mfma_f32_16x16x32_f16 v[218:221], v[86:89], v[154:157], v[218:221]
	v_mfma_f32_16x16x32_f16 v[222:225], v[94:97], v[154:157], v[222:225]
	s_waitcnt lgkmcnt(2)
	v_mfma_f32_16x16x32_f16 v[210:213], v[54:57], v[158:161], v[210:213]
	v_mfma_f32_16x16x32_f16 v[210:213], v[58:61], v[162:165], v[210:213]
	s_waitcnt lgkmcnt(0)
	v_mfma_f32_16x16x32_f16 v[210:213], v[62:65], v[166:169], v[210:213]
	v_mfma_f32_16x16x32_f16 v[210:213], v[50:53], v[170:173], v[210:213]
	s_waitcnt vmcnt(9)
	v_cvt_pk_f16_f32 v251, v194, v195
	ds_write_b32 v1, v251 offset:6144
	ds_read_b128 v[150:153], v186 offset:4096
	ds_read_b128 v[154:157], v186 offset:5120
	s_add_i32 s45, s45, 0x100000
	s_add_i32 s46, s46, 0x4000
	s_movk_i32 s47, 0x1000
	s_add_i32 s43, s40, -12
	s_lshl_b32 s43, s43, 12
	s_cmp_lt_u32 s40, 14
	s_cselect_b32 s43, s47, s43
	v_exp_f32_e32 v226, v210
	v_exp_f32_e32 v227, v211
	v_mfma_f32_16x16x32_f16 v[214:217], v[34:37], v[158:161], v[214:217]
	v_min_f32_e32 v228, s42, v212
	v_exp_f32_e32 v229, v213
	v_mfma_f32_16x16x32_f16 v[214:217], v[38:41], v[162:165], v[214:217]
	v_exp_f32_e32 v228, v228
	v_add_f32_e32 v227, 1.0, v227
	v_mfma_f32_16x16x32_f16 v[214:217], v[42:45], v[166:169], v[214:217]
	v_fma_f32 v230, v228, s41, s41
	v_rcp_f32_e32 v227, v227
	v_mfma_f32_16x16x32_f16 v[214:217], v[46:49], v[170:173], v[214:217]
	v_fma_f32 v230, v226, v230, v230
	v_rcp_f32_e32 v230, v230
	v_mfma_f32_16x16x32_f16 v[218:221], v[18:21], v[158:161], v[218:221]
	v_fma_f32 v226, -v228, v230, v230
	v_fma_f32 v200, v200, v227, v226
	v_mfma_f32_16x16x32_f16 v[218:221], v[14:17], v[162:165], v[218:221]
	v_exp_f32_e32 v226, v200
	s_nop 0
	v_add_f32_e32 v227, 1.0, v226
	v_mfma_f32_16x16x32_f16 v[218:221], v[10:13], v[166:169], v[218:221]
	v_fma_f32 v227, v229, v227, v227
	v_rcp_f32_e32 v227, v227
	v_mfma_f32_16x16x32_f16 v[218:221], v[26:29], v[170:173], v[218:221]
	v_fma_f32 v226, -v226, v227, v227
	v_exp_f32_e32 v231, v214
	v_mfma_f32_16x16x32_f16 v[222:225], v[2:5], v[158:161], v[222:225]
	v_exp_f32_e32 v232, v215
	v_min_f32_e32 v233, s42, v216
	v_mfma_f32_16x16x32_f16 v[222:225], v[6:9], v[162:165], v[222:225]
	v_exp_f32_e32 v234, v217
	v_exp_f32_e32 v233, v233
	v_mfma_f32_16x16x32_f16 v[222:225], v[22:25], v[166:169], v[222:225]
	v_exp_f32_e32 v236, v218
	v_add_f32_e32 v232, 1.0, v232
	v_mfma_f32_16x16x32_f16 v[222:225], v[30:33], v[170:173], v[222:225]
	v_fma_f32 v235, v233, s41, s41
	v_exp_f32_e32 v227, v219
	v_rcp_f32_e32 v232, v232
	v_fma_f32 v235, v231, v235, v235
	v_min_f32_e32 v228, s42, v220
	v_rcp_f32_e32 v235, v235
	s_nop 0
	v_fma_f32 v231, -v233, v235, v235
	v_exp_f32_e32 v229, v221
	v_fma_f32 v201, v201, v232, v231
	v_exp_f32_e32 v231, v201
	v_exp_f32_e32 v228, v228
	v_add_f32_e32 v232, 1.0, v231
	v_fma_f32 v232, v234, v232, v232
	v_add_f32_e32 v227, 1.0, v227
	v_rcp_f32_e32 v232, v232
	v_mfma_f32_16x16x32_f16 v[146:149], v[130:133], v[158:161], v[146:149]
	v_fma_f32 v231, -v231, v232, v232
	v_fma_f32 v230, v228, s41, s41
	v_cvt_pk_f16_f32 v246, v226, v231
	v_mfma_f32_16x16x32_f16 v[146:149], v[134:137], v[162:165], v[146:149]
	v_exp_f32_e32 v231, v222
	v_rcp_f32_e32 v227, v227
	v_exp_f32_e32 v232, v223
	buffer_load_dwordx4 v[130:133], v189, s[16:19], s46 offen
	buffer_load_dwordx4 v[134:137], v208, s[16:19], s46 offen
	v_min_f32_e32 v233, s42, v224
	v_fma_f32 v230, v236, v230, v230
	v_exp_f32_e32 v234, v225
	s_waitcnt lgkmcnt(0)
	v_mfma_f32_16x16x32_f16 v[210:213], v[70:73], v[150:153], v[98:101]
	v_exp_f32_e32 v233, v233
	v_rcp_f32_e32 v230, v230
	v_add_f32_e32 v232, 1.0, v232
	v_mfma_f32_16x16x32_f16 v[214:217], v[74:77], v[150:153], v[102:105]
	v_fma_f32 v235, v233, s41, s41
	v_fma_f32 v236, -v228, v230, v230
	v_rcp_f32_e32 v232, v232
	v_fma_f32 v235, v231, v235, v235
	v_fma_f32 v198, v198, v227, v236
	v_rcp_f32_e32 v235, v235
	s_nop 0
	v_fma_f32 v231, -v233, v235, v235
	v_exp_f32_e32 v236, v198
	v_fma_f32 v199, v199, v232, v231
	v_exp_f32_e32 v231, v199
	v_add_f32_e32 v227, 1.0, v236
	v_add_f32_e32 v232, 1.0, v231
	v_add_u32_e32 v250, s43, v206
	v_fma_f32 v232, v234, v232, v232
	v_fma_f32 v227, v229, v227, v227
	v_add_u32_e32 v248, s43, v252
	v_rcp_f32_e32 v232, v232
	s_nop 0
	v_fma_f32 v231, -v231, v232, v232
	v_add_u32_e32 v249, s43, v253
	v_rcp_f32_e32 v227, v227
	s_nop 0
	v_fma_f32 v236, -v236, v227, v227
	v_cvt_pk_f16_f32 v247, v236, v231
	ds_write_b64 v250, v[246:247] offset:8192
	v_mfma_f32_16x16x32_f16 v[210:213], v[66:69], v[154:157], v[210:213]
	v_mfma_f32_16x16x32_f16 v[214:217], v[78:81], v[154:157], v[214:217]
	v_mov_b32_e32 v176, v246
	v_mov_b32_e32 v177, v247
	buffer_load_dwordx2 v[194:195], v209, s[20:23], s45 offen
	s_add_i32 s40, s40, 1
	s_add_i32 s44, s44, 0x1000
	s_waitcnt lgkmcnt(0)
	s_barrier
	ds_read_b128 v[158:161], v248 offset:0
	ds_read_b128 v[162:165], v248 offset:1024
	ds_read_b128 v[166:169], v249 offset:2048
	ds_read_b128 v[170:173], v249 offset:3072
	v_mfma_f32_16x16x32_f16 v[218:221], v[82:85], v[150:153], v[106:109]
	v_mfma_f32_16x16x32_f16 v[222:225], v[90:93], v[150:153], v[110:113]
	v_mfma_f32_16x16x32_f16 v[218:221], v[86:89], v[154:157], v[218:221]
	v_mfma_f32_16x16x32_f16 v[222:225], v[94:97], v[154:157], v[222:225]
	s_waitcnt lgkmcnt(2)
	v_mfma_f32_16x16x32_f16 v[210:213], v[54:57], v[158:161], v[210:213]
	v_mfma_f32_16x16x32_f16 v[210:213], v[58:61], v[162:165], v[210:213]
	s_waitcnt lgkmcnt(0)
	v_mfma_f32_16x16x32_f16 v[210:213], v[62:65], v[166:169], v[210:213]
	v_mfma_f32_16x16x32_f16 v[210:213], v[50:53], v[170:173], v[210:213]
	s_waitcnt vmcnt(9)
	v_cvt_pk_f16_f32 v251, v192, v193
	ds_write_b32 v1, v251 offset:0
	ds_read_b128 v[150:153], v186 offset:6144
	ds_read_b128 v[154:157], v186 offset:7168
	s_add_i32 s45, s45, 0x100000
	s_add_i32 s46, s46, 0x4000
	s_movk_i32 s47, 0x0
	s_add_i32 s43, s40, -12
	s_lshl_b32 s43, s43, 12
	s_cmp_lt_u32 s40, 14
	s_cselect_b32 s43, s47, s43
	v_exp_f32_e32 v226, v210
	v_exp_f32_e32 v227, v211
	v_mfma_f32_16x16x32_f16 v[214:217], v[34:37], v[158:161], v[214:217]
	v_min_f32_e32 v228, s42, v212
	v_exp_f32_e32 v229, v213
	v_mfma_f32_16x16x32_f16 v[214:217], v[38:41], v[162:165], v[214:217]
	v_exp_f32_e32 v228, v228
	v_add_f32_e32 v227, 1.0, v227
	v_mfma_f32_16x16x32_f16 v[214:217], v[42:45], v[166:169], v[214:217]
	v_fma_f32 v230, v228, s41, s41
	v_rcp_f32_e32 v227, v227
	v_mfma_f32_16x16x32_f16 v[214:217], v[46:49], v[170:173], v[214:217]
	v_fma_f32 v230, v226, v230, v230
	v_rcp_f32_e32 v230, v230
	v_mfma_f32_16x16x32_f16 v[218:221], v[18:21], v[158:161], v[218:221]
	v_fma_f32 v226, -v228, v230, v230
	v_fma_f32 v200, v200, v227, v226
	v_mfma_f32_16x16x32_f16 v[218:221], v[14:17], v[162:165], v[218:221]
	v_exp_f32_e32 v226, v200
	s_nop 0
	v_add_f32_e32 v227, 1.0, v226
	v_mfma_f32_16x16x32_f16 v[218:221], v[10:13], v[166:169], v[218:221]
	v_fma_f32 v227, v229, v227, v227
	v_rcp_f32_e32 v227, v227
	v_mfma_f32_16x16x32_f16 v[218:221], v[26:29], v[170:173], v[218:221]
	v_fma_f32 v226, -v226, v227, v227
	v_exp_f32_e32 v231, v214
	v_mfma_f32_16x16x32_f16 v[222:225], v[2:5], v[158:161], v[222:225]
	v_exp_f32_e32 v232, v215
	v_min_f32_e32 v233, s42, v216
	v_mfma_f32_16x16x32_f16 v[222:225], v[6:9], v[162:165], v[222:225]
	v_exp_f32_e32 v234, v217
	v_exp_f32_e32 v233, v233
	v_mfma_f32_16x16x32_f16 v[222:225], v[22:25], v[166:169], v[222:225]
	v_exp_f32_e32 v236, v218
	v_add_f32_e32 v232, 1.0, v232
	v_mfma_f32_16x16x32_f16 v[222:225], v[30:33], v[170:173], v[222:225]
	v_fma_f32 v235, v233, s41, s41
	v_exp_f32_e32 v227, v219
	v_rcp_f32_e32 v232, v232
	v_fma_f32 v235, v231, v235, v235
	v_min_f32_e32 v228, s42, v220
	v_rcp_f32_e32 v235, v235
	s_nop 0
	v_fma_f32 v231, -v233, v235, v235
	v_exp_f32_e32 v229, v221
	v_fma_f32 v201, v201, v232, v231
	v_exp_f32_e32 v231, v201
	v_exp_f32_e32 v228, v228
	v_add_f32_e32 v232, 1.0, v231
	v_fma_f32 v232, v234, v232, v232
	v_add_f32_e32 v227, 1.0, v227
	v_rcp_f32_e32 v232, v232
	v_mfma_f32_16x16x32_f16 v[146:149], v[122:125], v[158:161], v[146:149]
	v_fma_f32 v231, -v231, v232, v232
	v_fma_f32 v230, v228, s41, s41
	v_cvt_pk_f16_f32 v246, v226, v231
	v_mfma_f32_16x16x32_f16 v[146:149], v[126:129], v[162:165], v[146:149]
	v_exp_f32_e32 v231, v222
	v_rcp_f32_e32 v227, v227
	v_exp_f32_e32 v232, v223
	buffer_load_dwordx4 v[122:125], v189, s[16:19], s46 offen
	buffer_load_dwordx4 v[126:129], v208, s[16:19], s46 offen
	v_min_f32_e32 v233, s42, v224
	v_fma_f32 v230, v236, v230, v230
	v_exp_f32_e32 v234, v225
	s_waitcnt lgkmcnt(0)
	v_mfma_f32_16x16x32_f16 v[210:213], v[70:73], v[150:153], v[98:101]
	v_exp_f32_e32 v233, v233
	v_rcp_f32_e32 v230, v230
	v_add_f32_e32 v232, 1.0, v232
	v_mfma_f32_16x16x32_f16 v[214:217], v[74:77], v[150:153], v[102:105]
	v_fma_f32 v235, v233, s41, s41
	v_fma_f32 v236, -v228, v230, v230
	v_rcp_f32_e32 v232, v232
	v_fma_f32 v235, v231, v235, v235
	v_fma_f32 v198, v198, v227, v236
	v_rcp_f32_e32 v235, v235
	s_nop 0
	v_fma_f32 v231, -v233, v235, v235
	v_exp_f32_e32 v236, v198
	v_fma_f32 v199, v199, v232, v231
	v_exp_f32_e32 v231, v199
	v_add_f32_e32 v227, 1.0, v236
	v_add_f32_e32 v232, 1.0, v231
	v_add_u32_e32 v250, s43, v206
	v_fma_f32 v232, v234, v232, v232
	v_fma_f32 v227, v229, v227, v227
	v_add_u32_e32 v248, s43, v252
	v_rcp_f32_e32 v232, v232
	s_nop 0
	v_fma_f32 v231, -v231, v232, v232
	v_add_u32_e32 v249, s43, v253
	v_rcp_f32_e32 v227, v227
	s_nop 0
	v_fma_f32 v236, -v236, v227, v227
	v_cvt_pk_f16_f32 v247, v236, v231
	ds_write_b64 v250, v[246:247] offset:8192
	v_mfma_f32_16x16x32_f16 v[210:213], v[66:69], v[154:157], v[210:213]
	v_mfma_f32_16x16x32_f16 v[214:217], v[78:81], v[154:157], v[214:217]
	v_mov_b32_e32 v178, v246
	v_mov_b32_e32 v179, v247
	buffer_load_dwordx2 v[192:193], v209, s[20:23], s45 offen
	s_add_i32 s40, s40, 1
	s_add_i32 s44, s44, 0x1000
	s_waitcnt lgkmcnt(0)
	s_barrier
	ds_read_b128 v[158:161], v248 offset:0
	ds_read_b128 v[162:165], v248 offset:1024
	ds_read_b128 v[166:169], v249 offset:2048
	ds_read_b128 v[170:173], v249 offset:3072
	v_mfma_f32_16x16x32_f16 v[218:221], v[82:85], v[150:153], v[106:109]
	v_mfma_f32_16x16x32_f16 v[222:225], v[90:93], v[150:153], v[110:113]
	v_mfma_f32_16x16x32_f16 v[218:221], v[86:89], v[154:157], v[218:221]
	v_mfma_f32_16x16x32_f16 v[222:225], v[94:97], v[154:157], v[222:225]
	s_waitcnt lgkmcnt(2)
	v_mfma_f32_16x16x32_f16 v[210:213], v[54:57], v[158:161], v[210:213]
	v_mfma_f32_16x16x32_f16 v[210:213], v[58:61], v[162:165], v[210:213]
	s_waitcnt lgkmcnt(0)
	v_mfma_f32_16x16x32_f16 v[210:213], v[62:65], v[166:169], v[210:213]
	v_mfma_f32_16x16x32_f16 v[210:213], v[50:53], v[170:173], v[210:213]
	s_waitcnt vmcnt(9)
	v_cvt_pk_f16_f32 v251, v190, v191
	ds_write_b32 v1, v251 offset:2048
	ds_read_b128 v[150:153], v186 offset:0
	ds_read_b128 v[154:157], v186 offset:1024
	s_add_i32 s45, s45, 0x100000
	s_add_i32 s46, s46, 0x4000
	s_movk_i32 s47, 0x1000
	s_add_i32 s43, s40, -12
	s_lshl_b32 s43, s43, 12
	s_cmp_lt_u32 s40, 14
	s_cselect_b32 s43, s47, s43
	v_exp_f32_e32 v226, v210
	v_exp_f32_e32 v227, v211
	v_mfma_f32_16x16x32_f16 v[214:217], v[34:37], v[158:161], v[214:217]
	v_min_f32_e32 v228, s42, v212
	v_exp_f32_e32 v229, v213
	v_mfma_f32_16x16x32_f16 v[214:217], v[38:41], v[162:165], v[214:217]
	v_exp_f32_e32 v228, v228
	v_add_f32_e32 v227, 1.0, v227
	v_mfma_f32_16x16x32_f16 v[214:217], v[42:45], v[166:169], v[214:217]
	v_fma_f32 v230, v228, s41, s41
	v_rcp_f32_e32 v227, v227
	v_mfma_f32_16x16x32_f16 v[214:217], v[46:49], v[170:173], v[214:217]
	v_fma_f32 v230, v226, v230, v230
	v_rcp_f32_e32 v230, v230
	v_mfma_f32_16x16x32_f16 v[218:221], v[18:21], v[158:161], v[218:221]
	v_fma_f32 v226, -v228, v230, v230
	v_fma_f32 v200, v200, v227, v226
	v_mfma_f32_16x16x32_f16 v[218:221], v[14:17], v[162:165], v[218:221]
	v_exp_f32_e32 v226, v200
	s_nop 0
	v_add_f32_e32 v227, 1.0, v226
	v_mfma_f32_16x16x32_f16 v[218:221], v[10:13], v[166:169], v[218:221]
	v_fma_f32 v227, v229, v227, v227
	v_rcp_f32_e32 v227, v227
	v_mfma_f32_16x16x32_f16 v[218:221], v[26:29], v[170:173], v[218:221]
	v_fma_f32 v226, -v226, v227, v227
	v_exp_f32_e32 v231, v214
	v_mfma_f32_16x16x32_f16 v[222:225], v[2:5], v[158:161], v[222:225]
	v_exp_f32_e32 v232, v215
	v_min_f32_e32 v233, s42, v216
	v_mfma_f32_16x16x32_f16 v[222:225], v[6:9], v[162:165], v[222:225]
	v_exp_f32_e32 v234, v217
	v_exp_f32_e32 v233, v233
	v_mfma_f32_16x16x32_f16 v[222:225], v[22:25], v[166:169], v[222:225]
	v_exp_f32_e32 v236, v218
	v_add_f32_e32 v232, 1.0, v232
	v_mfma_f32_16x16x32_f16 v[222:225], v[30:33], v[170:173], v[222:225]
	v_fma_f32 v235, v233, s41, s41
	v_exp_f32_e32 v227, v219
	v_rcp_f32_e32 v232, v232
	v_fma_f32 v235, v231, v235, v235
	v_min_f32_e32 v228, s42, v220
	v_rcp_f32_e32 v235, v235
	s_nop 0
	v_fma_f32 v231, -v233, v235, v235
	v_exp_f32_e32 v229, v221
	v_fma_f32 v201, v201, v232, v231
	v_exp_f32_e32 v231, v201
	v_exp_f32_e32 v228, v228
	v_add_f32_e32 v232, 1.0, v231
	v_fma_f32 v232, v234, v232, v232
	v_add_f32_e32 v227, 1.0, v227
	v_rcp_f32_e32 v232, v232
	v_mfma_f32_16x16x32_f16 v[146:149], v[114:117], v[158:161], v[146:149]
	v_fma_f32 v231, -v231, v232, v232
	v_fma_f32 v230, v228, s41, s41
	v_cvt_pk_f16_f32 v246, v226, v231
	v_mfma_f32_16x16x32_f16 v[146:149], v[118:121], v[162:165], v[146:149]
	v_exp_f32_e32 v231, v222
	v_rcp_f32_e32 v227, v227
	v_exp_f32_e32 v232, v223
	buffer_load_dwordx4 v[114:117], v189, s[16:19], s46 offen
	buffer_load_dwordx4 v[118:121], v208, s[16:19], s46 offen
	v_min_f32_e32 v233, s42, v224
	v_fma_f32 v230, v236, v230, v230
	v_exp_f32_e32 v234, v225
	s_waitcnt lgkmcnt(0)
	v_mfma_f32_16x16x32_f16 v[210:213], v[70:73], v[150:153], v[98:101]
	v_exp_f32_e32 v233, v233
	v_rcp_f32_e32 v230, v230
	v_add_f32_e32 v232, 1.0, v232
	v_mfma_f32_16x16x32_f16 v[214:217], v[74:77], v[150:153], v[102:105]
	v_fma_f32 v235, v233, s41, s41
	v_fma_f32 v236, -v228, v230, v230
	v_rcp_f32_e32 v232, v232
	v_fma_f32 v235, v231, v235, v235
	v_fma_f32 v198, v198, v227, v236
	v_rcp_f32_e32 v235, v235
	s_nop 0
	v_fma_f32 v231, -v233, v235, v235
	v_exp_f32_e32 v236, v198
	v_fma_f32 v199, v199, v232, v231
	v_exp_f32_e32 v231, v199
	v_add_f32_e32 v227, 1.0, v236
	v_add_f32_e32 v232, 1.0, v231
	v_add_u32_e32 v250, s43, v206
	v_fma_f32 v232, v234, v232, v232
	v_fma_f32 v227, v229, v227, v227
	v_add_u32_e32 v248, s43, v252
	v_rcp_f32_e32 v232, v232
	s_nop 0
	v_fma_f32 v231, -v231, v232, v232
	v_add_u32_e32 v249, s43, v253
	v_rcp_f32_e32 v227, v227
	s_nop 0
	v_fma_f32 v236, -v236, v227, v227
	v_cvt_pk_f16_f32 v247, v236, v231
	ds_write_b64 v250, v[246:247] offset:8192
	v_mfma_f32_16x16x32_f16 v[210:213], v[66:69], v[154:157], v[210:213]
	v_mfma_f32_16x16x32_f16 v[214:217], v[78:81], v[154:157], v[214:217]
	v_mov_b32_e32 v180, v246
	v_mov_b32_e32 v181, v247
	buffer_load_dwordx2 v[190:191], v209, s[20:23], s45 offen
	s_add_i32 s40, s40, 1
	s_add_i32 s44, s44, 0x1000
	s_waitcnt lgkmcnt(0)
	s_barrier
	ds_read_b128 v[158:161], v248 offset:0
	ds_read_b128 v[162:165], v248 offset:1024
	ds_read_b128 v[166:169], v249 offset:2048
	ds_read_b128 v[170:173], v249 offset:3072
	v_mfma_f32_16x16x32_f16 v[218:221], v[82:85], v[150:153], v[106:109]
	v_mfma_f32_16x16x32_f16 v[222:225], v[90:93], v[150:153], v[110:113]
	v_mfma_f32_16x16x32_f16 v[218:221], v[86:89], v[154:157], v[218:221]
	v_mfma_f32_16x16x32_f16 v[222:225], v[94:97], v[154:157], v[222:225]
	s_waitcnt lgkmcnt(2)
	v_mfma_f32_16x16x32_f16 v[210:213], v[54:57], v[158:161], v[210:213]
	v_mfma_f32_16x16x32_f16 v[210:213], v[58:61], v[162:165], v[210:213]
	s_waitcnt lgkmcnt(0)
	v_mfma_f32_16x16x32_f16 v[210:213], v[62:65], v[166:169], v[210:213]
	v_mfma_f32_16x16x32_f16 v[210:213], v[50:53], v[170:173], v[210:213]
	s_waitcnt vmcnt(9)
	v_cvt_pk_f16_f32 v251, v196, v197
	ds_write_b32 v1, v251 offset:4096
	ds_read_b128 v[150:153], v186 offset:2048
	ds_read_b128 v[154:157], v186 offset:3072
	s_add_i32 s45, s45, 0x100000
	s_add_i32 s46, s46, 0x4000
	s_movk_i32 s47, 0x0
	s_add_i32 s43, s40, -12
	s_lshl_b32 s43, s43, 12
	s_cmp_lt_u32 s40, 14
	s_cselect_b32 s43, s47, s43
	v_exp_f32_e32 v226, v210
	v_exp_f32_e32 v227, v211
	v_mfma_f32_16x16x32_f16 v[214:217], v[34:37], v[158:161], v[214:217]
	v_min_f32_e32 v228, s42, v212
	v_exp_f32_e32 v229, v213
	v_mfma_f32_16x16x32_f16 v[214:217], v[38:41], v[162:165], v[214:217]
	v_exp_f32_e32 v228, v228
	v_add_f32_e32 v227, 1.0, v227
	v_mfma_f32_16x16x32_f16 v[214:217], v[42:45], v[166:169], v[214:217]
	v_fma_f32 v230, v228, s41, s41
	v_rcp_f32_e32 v227, v227
	v_mfma_f32_16x16x32_f16 v[214:217], v[46:49], v[170:173], v[214:217]
	v_fma_f32 v230, v226, v230, v230
	v_rcp_f32_e32 v230, v230
	v_mfma_f32_16x16x32_f16 v[218:221], v[18:21], v[158:161], v[218:221]
	v_fma_f32 v226, -v228, v230, v230
	v_fma_f32 v200, v200, v227, v226
	v_mfma_f32_16x16x32_f16 v[218:221], v[14:17], v[162:165], v[218:221]
	v_exp_f32_e32 v226, v200
	s_nop 0
	v_add_f32_e32 v227, 1.0, v226
	v_mfma_f32_16x16x32_f16 v[218:221], v[10:13], v[166:169], v[218:221]
	v_fma_f32 v227, v229, v227, v227
	v_rcp_f32_e32 v227, v227
	v_mfma_f32_16x16x32_f16 v[218:221], v[26:29], v[170:173], v[218:221]
	v_fma_f32 v226, -v226, v227, v227
	v_exp_f32_e32 v231, v214
	v_mfma_f32_16x16x32_f16 v[222:225], v[2:5], v[158:161], v[222:225]
	v_exp_f32_e32 v232, v215
	v_min_f32_e32 v233, s42, v216
	v_mfma_f32_16x16x32_f16 v[222:225], v[6:9], v[162:165], v[222:225]
	v_exp_f32_e32 v234, v217
	v_exp_f32_e32 v233, v233
	v_mfma_f32_16x16x32_f16 v[222:225], v[22:25], v[166:169], v[222:225]
	v_exp_f32_e32 v236, v218
	v_add_f32_e32 v232, 1.0, v232
	v_mfma_f32_16x16x32_f16 v[222:225], v[30:33], v[170:173], v[222:225]
	v_fma_f32 v235, v233, s41, s41
	v_exp_f32_e32 v227, v219
	v_rcp_f32_e32 v232, v232
	v_fma_f32 v235, v231, v235, v235
	v_min_f32_e32 v228, s42, v220
	v_rcp_f32_e32 v235, v235
	s_nop 0
	v_fma_f32 v231, -v233, v235, v235
	v_exp_f32_e32 v229, v221
	v_fma_f32 v201, v201, v232, v231
	v_exp_f32_e32 v231, v201
	v_exp_f32_e32 v228, v228
	v_add_f32_e32 v232, 1.0, v231
	v_fma_f32 v232, v234, v232, v232
	v_add_f32_e32 v227, 1.0, v227
	v_rcp_f32_e32 v232, v232
	v_mfma_f32_16x16x32_f16 v[146:149], v[138:141], v[158:161], v[146:149]
	v_fma_f32 v231, -v231, v232, v232
	v_fma_f32 v230, v228, s41, s41
	v_cvt_pk_f16_f32 v246, v226, v231
	v_mfma_f32_16x16x32_f16 v[146:149], v[142:145], v[162:165], v[146:149]
	v_exp_f32_e32 v231, v222
	v_rcp_f32_e32 v227, v227
	v_exp_f32_e32 v232, v223
	buffer_load_dwordx4 v[138:141], v189, s[16:19], s46 offen
	buffer_load_dwordx4 v[142:145], v208, s[16:19], s46 offen
	v_min_f32_e32 v233, s42, v224
	v_fma_f32 v230, v236, v230, v230
	v_exp_f32_e32 v234, v225
	s_waitcnt lgkmcnt(0)
	v_mfma_f32_16x16x32_f16 v[210:213], v[70:73], v[150:153], v[98:101]
	v_exp_f32_e32 v233, v233
	v_rcp_f32_e32 v230, v230
	v_add_f32_e32 v232, 1.0, v232
	v_mfma_f32_16x16x32_f16 v[214:217], v[74:77], v[150:153], v[102:105]
	v_fma_f32 v235, v233, s41, s41
	v_fma_f32 v236, -v228, v230, v230
	v_rcp_f32_e32 v232, v232
	v_fma_f32 v235, v231, v235, v235
	v_fma_f32 v198, v198, v227, v236
	v_rcp_f32_e32 v235, v235
	s_nop 0
	v_fma_f32 v231, -v233, v235, v235
	v_exp_f32_e32 v236, v198
	v_fma_f32 v199, v199, v232, v231
	v_exp_f32_e32 v231, v199
	v_add_f32_e32 v227, 1.0, v236
	v_add_f32_e32 v232, 1.0, v231
	v_add_u32_e32 v250, s43, v206
	v_fma_f32 v232, v234, v232, v232
	v_fma_f32 v227, v229, v227, v227
	v_add_u32_e32 v248, s43, v252
	v_rcp_f32_e32 v232, v232
	s_nop 0
	v_fma_f32 v231, -v231, v232, v232
	v_add_u32_e32 v249, s43, v253
	v_rcp_f32_e32 v227, v227
	s_nop 0
	v_fma_f32 v236, -v236, v227, v227
	v_cvt_pk_f16_f32 v247, v236, v231
	ds_write_b64 v250, v[246:247] offset:8192
	v_mfma_f32_16x16x32_f16 v[210:213], v[66:69], v[154:157], v[210:213]
	v_mfma_f32_16x16x32_f16 v[214:217], v[78:81], v[154:157], v[214:217]
	v_mov_b32_e32 v182, v246
	v_mov_b32_e32 v183, v247
	buffer_load_dwordx2 v[196:197], v209, s[20:23], s45 offen
	s_add_i32 s40, s40, 1
	s_add_i32 s44, s44, 0x1000
	s_waitcnt lgkmcnt(0)
	s_barrier
	ds_read_b128 v[158:161], v248 offset:0
	ds_read_b128 v[162:165], v248 offset:1024
	ds_read_b128 v[166:169], v249 offset:2048
	ds_read_b128 v[170:173], v249 offset:3072
	v_mfma_f32_16x16x32_f16 v[218:221], v[82:85], v[150:153], v[106:109]
	v_mfma_f32_16x16x32_f16 v[222:225], v[90:93], v[150:153], v[110:113]
	v_mfma_f32_16x16x32_f16 v[218:221], v[86:89], v[154:157], v[218:221]
	v_mfma_f32_16x16x32_f16 v[222:225], v[94:97], v[154:157], v[222:225]
	s_waitcnt lgkmcnt(2)
	v_mfma_f32_16x16x32_f16 v[210:213], v[54:57], v[158:161], v[210:213]
	v_mfma_f32_16x16x32_f16 v[210:213], v[58:61], v[162:165], v[210:213]
	s_waitcnt lgkmcnt(0)
	v_mfma_f32_16x16x32_f16 v[210:213], v[62:65], v[166:169], v[210:213]
	v_mfma_f32_16x16x32_f16 v[210:213], v[50:53], v[170:173], v[210:213]
	s_waitcnt vmcnt(9)
	v_cvt_pk_f16_f32 v251, v194, v195
	ds_write_b32 v1, v251 offset:6144
	ds_read_b128 v[150:153], v186 offset:4096
	ds_read_b128 v[154:157], v186 offset:5120
	s_add_i32 s45, s45, 0x100000
	s_add_i32 s46, s46, 0x4000
	s_movk_i32 s47, 0x1000
	s_add_i32 s43, s40, -12
	s_lshl_b32 s43, s43, 12
	s_cmp_lt_u32 s40, 14
	s_cselect_b32 s43, s47, s43
	v_exp_f32_e32 v226, v210
	v_exp_f32_e32 v227, v211
	v_mfma_f32_16x16x32_f16 v[214:217], v[34:37], v[158:161], v[214:217]
	v_min_f32_e32 v228, s42, v212
	v_exp_f32_e32 v229, v213
	v_mfma_f32_16x16x32_f16 v[214:217], v[38:41], v[162:165], v[214:217]
	v_exp_f32_e32 v228, v228
	v_add_f32_e32 v227, 1.0, v227
	v_mfma_f32_16x16x32_f16 v[214:217], v[42:45], v[166:169], v[214:217]
	v_fma_f32 v230, v228, s41, s41
	v_rcp_f32_e32 v227, v227
	v_mfma_f32_16x16x32_f16 v[214:217], v[46:49], v[170:173], v[214:217]
	v_fma_f32 v230, v226, v230, v230
	v_rcp_f32_e32 v230, v230
	v_mfma_f32_16x16x32_f16 v[218:221], v[18:21], v[158:161], v[218:221]
	v_fma_f32 v226, -v228, v230, v230
	v_fma_f32 v200, v200, v227, v226
	v_mfma_f32_16x16x32_f16 v[218:221], v[14:17], v[162:165], v[218:221]
	v_exp_f32_e32 v226, v200
	s_nop 0
	v_add_f32_e32 v227, 1.0, v226
	v_mfma_f32_16x16x32_f16 v[218:221], v[10:13], v[166:169], v[218:221]
	v_fma_f32 v227, v229, v227, v227
	v_rcp_f32_e32 v227, v227
	v_mfma_f32_16x16x32_f16 v[218:221], v[26:29], v[170:173], v[218:221]
	v_fma_f32 v226, -v226, v227, v227
	v_exp_f32_e32 v231, v214
	v_mfma_f32_16x16x32_f16 v[222:225], v[2:5], v[158:161], v[222:225]
	v_exp_f32_e32 v232, v215
	v_min_f32_e32 v233, s42, v216
	v_mfma_f32_16x16x32_f16 v[222:225], v[6:9], v[162:165], v[222:225]
	v_exp_f32_e32 v234, v217
	v_exp_f32_e32 v233, v233
	v_mfma_f32_16x16x32_f16 v[222:225], v[22:25], v[166:169], v[222:225]
	v_exp_f32_e32 v236, v218
	v_add_f32_e32 v232, 1.0, v232
	v_mfma_f32_16x16x32_f16 v[222:225], v[30:33], v[170:173], v[222:225]
	v_fma_f32 v235, v233, s41, s41
	v_exp_f32_e32 v227, v219
	v_rcp_f32_e32 v232, v232
	v_fma_f32 v235, v231, v235, v235
	v_min_f32_e32 v228, s42, v220
	v_rcp_f32_e32 v235, v235
	s_nop 0
	v_fma_f32 v231, -v233, v235, v235
	v_exp_f32_e32 v229, v221
	v_fma_f32 v201, v201, v232, v231
	v_exp_f32_e32 v231, v201
	v_exp_f32_e32 v228, v228
	v_add_f32_e32 v232, 1.0, v231
	v_fma_f32 v232, v234, v232, v232
	v_add_f32_e32 v227, 1.0, v227
	v_rcp_f32_e32 v232, v232
	v_mfma_f32_16x16x32_f16 v[146:149], v[130:133], v[158:161], v[146:149]
	v_fma_f32 v231, -v231, v232, v232
	v_fma_f32 v230, v228, s41, s41
	v_cvt_pk_f16_f32 v246, v226, v231
	v_mfma_f32_16x16x32_f16 v[146:149], v[134:137], v[162:165], v[146:149]
	v_exp_f32_e32 v231, v222
	v_rcp_f32_e32 v227, v227
	v_exp_f32_e32 v232, v223
	buffer_load_dwordx4 v[130:133], v189, s[16:19], s46 offen
	buffer_load_dwordx4 v[134:137], v208, s[16:19], s46 offen
	v_min_f32_e32 v233, s42, v224
	v_fma_f32 v230, v236, v230, v230
	v_exp_f32_e32 v234, v225
	s_waitcnt lgkmcnt(0)
	v_mfma_f32_16x16x32_f16 v[210:213], v[70:73], v[150:153], v[98:101]
	v_exp_f32_e32 v233, v233
	v_rcp_f32_e32 v230, v230
	v_add_f32_e32 v232, 1.0, v232
	v_mfma_f32_16x16x32_f16 v[214:217], v[74:77], v[150:153], v[102:105]
	v_fma_f32 v235, v233, s41, s41
	v_fma_f32 v236, -v228, v230, v230
	v_rcp_f32_e32 v232, v232
	v_fma_f32 v235, v231, v235, v235
	v_fma_f32 v198, v198, v227, v236
	v_rcp_f32_e32 v235, v235
	s_nop 0
	v_fma_f32 v231, -v233, v235, v235
	v_exp_f32_e32 v236, v198
	v_fma_f32 v199, v199, v232, v231
	v_exp_f32_e32 v231, v199
	v_add_f32_e32 v227, 1.0, v236
	v_add_f32_e32 v232, 1.0, v231
	v_add_u32_e32 v250, s43, v206
	v_fma_f32 v232, v234, v232, v232
	v_fma_f32 v227, v229, v227, v227
	v_add_u32_e32 v248, s43, v252
	v_rcp_f32_e32 v232, v232
	s_nop 0
	v_fma_f32 v231, -v231, v232, v232
	v_add_u32_e32 v249, s43, v253
	v_rcp_f32_e32 v227, v227
	s_nop 0
	v_fma_f32 v236, -v236, v227, v227
	v_cvt_pk_f16_f32 v247, v236, v231
	ds_write_b64 v250, v[246:247] offset:8192
	v_mfma_f32_16x16x32_f16 v[210:213], v[66:69], v[154:157], v[210:213]
	v_mfma_f32_16x16x32_f16 v[214:217], v[78:81], v[154:157], v[214:217]
	v_mov_b32_e32 v184, v246
	v_mov_b32_e32 v185, v247
	buffer_load_dwordx2 v[194:195], v209, s[20:23], s45 offen
	s_add_i32 s40, s40, 1
	s_add_i32 s44, s44, 0x1000
	s_waitcnt lgkmcnt(0)
	s_barrier
	ds_read_b128 v[158:161], v248 offset:0
	ds_read_b128 v[162:165], v248 offset:1024
	ds_read_b128 v[166:169], v249 offset:2048
	ds_read_b128 v[170:173], v249 offset:3072
	v_mfma_f32_16x16x32_f16 v[218:221], v[82:85], v[150:153], v[106:109]
	v_mfma_f32_16x16x32_f16 v[222:225], v[90:93], v[150:153], v[110:113]
	v_mfma_f32_16x16x32_f16 v[218:221], v[86:89], v[154:157], v[218:221]
	v_mfma_f32_16x16x32_f16 v[222:225], v[94:97], v[154:157], v[222:225]
	s_waitcnt lgkmcnt(2)
	v_mfma_f32_16x16x32_f16 v[210:213], v[54:57], v[158:161], v[210:213]
	v_mfma_f32_16x16x32_f16 v[210:213], v[58:61], v[162:165], v[210:213]
	s_waitcnt lgkmcnt(0)
	v_mfma_f32_16x16x32_f16 v[210:213], v[62:65], v[166:169], v[210:213]
	v_mfma_f32_16x16x32_f16 v[210:213], v[50:53], v[170:173], v[210:213]
	s_waitcnt vmcnt(9)
	v_cvt_pk_f16_f32 v251, v192, v193
	ds_write_b32 v1, v251 offset:0
	ds_read_b128 v[150:153], v186 offset:6144
	ds_read_b128 v[154:157], v186 offset:7168
	s_add_i32 s45, s45, 0x100000
	s_add_i32 s46, s46, 0x4000
	s_movk_i32 s47, 0x0
	s_add_i32 s43, s40, -12
	s_lshl_b32 s43, s43, 12
	s_cmp_lt_u32 s40, 14
	s_cselect_b32 s43, s47, s43
	v_exp_f32_e32 v226, v210
	v_exp_f32_e32 v227, v211
	v_mfma_f32_16x16x32_f16 v[214:217], v[34:37], v[158:161], v[214:217]
	v_min_f32_e32 v228, s42, v212
	v_exp_f32_e32 v229, v213
	v_mfma_f32_16x16x32_f16 v[214:217], v[38:41], v[162:165], v[214:217]
	v_exp_f32_e32 v228, v228
	v_add_f32_e32 v227, 1.0, v227
	v_mfma_f32_16x16x32_f16 v[214:217], v[42:45], v[166:169], v[214:217]
	v_fma_f32 v230, v228, s41, s41
	v_rcp_f32_e32 v227, v227
	v_mfma_f32_16x16x32_f16 v[214:217], v[46:49], v[170:173], v[214:217]
	v_fma_f32 v230, v226, v230, v230
	v_rcp_f32_e32 v230, v230
	v_mfma_f32_16x16x32_f16 v[218:221], v[18:21], v[158:161], v[218:221]
	v_fma_f32 v226, -v228, v230, v230
	v_fma_f32 v200, v200, v227, v226
	v_mfma_f32_16x16x32_f16 v[218:221], v[14:17], v[162:165], v[218:221]
	v_exp_f32_e32 v226, v200
	s_nop 0
	v_add_f32_e32 v227, 1.0, v226
	v_mfma_f32_16x16x32_f16 v[218:221], v[10:13], v[166:169], v[218:221]
	v_fma_f32 v227, v229, v227, v227
	v_rcp_f32_e32 v227, v227
	v_mfma_f32_16x16x32_f16 v[218:221], v[26:29], v[170:173], v[218:221]
	v_fma_f32 v226, -v226, v227, v227
	v_exp_f32_e32 v231, v214
	v_mfma_f32_16x16x32_f16 v[222:225], v[2:5], v[158:161], v[222:225]
	v_exp_f32_e32 v232, v215
	v_min_f32_e32 v233, s42, v216
	v_mfma_f32_16x16x32_f16 v[222:225], v[6:9], v[162:165], v[222:225]
	v_exp_f32_e32 v234, v217
	v_exp_f32_e32 v233, v233
	v_mfma_f32_16x16x32_f16 v[222:225], v[22:25], v[166:169], v[222:225]
	v_exp_f32_e32 v236, v218
	v_add_f32_e32 v232, 1.0, v232
	v_mfma_f32_16x16x32_f16 v[222:225], v[30:33], v[170:173], v[222:225]
	v_fma_f32 v235, v233, s41, s41
	v_exp_f32_e32 v227, v219
	v_rcp_f32_e32 v232, v232
	v_fma_f32 v235, v231, v235, v235
	v_min_f32_e32 v228, s42, v220
	v_rcp_f32_e32 v235, v235
	s_nop 0
	v_fma_f32 v231, -v233, v235, v235
	v_exp_f32_e32 v229, v221
	v_fma_f32 v201, v201, v232, v231
	v_exp_f32_e32 v231, v201
	v_exp_f32_e32 v228, v228
	v_add_f32_e32 v232, 1.0, v231
	v_fma_f32 v232, v234, v232, v232
	v_add_f32_e32 v227, 1.0, v227
	v_rcp_f32_e32 v232, v232
	v_mfma_f32_16x16x32_f16 v[146:149], v[122:125], v[158:161], v[146:149]
	v_fma_f32 v231, -v231, v232, v232
	v_fma_f32 v230, v228, s41, s41
	v_cvt_pk_f16_f32 v246, v226, v231
	v_mfma_f32_16x16x32_f16 v[146:149], v[126:129], v[162:165], v[146:149]
	v_exp_f32_e32 v231, v222
	v_rcp_f32_e32 v227, v227
	v_exp_f32_e32 v232, v223
	buffer_load_dwordx4 v[122:125], v189, s[16:19], s46 offen
	buffer_load_dwordx4 v[126:129], v208, s[16:19], s46 offen
	v_min_f32_e32 v233, s42, v224
	v_fma_f32 v230, v236, v230, v230
	v_exp_f32_e32 v234, v225
	s_waitcnt lgkmcnt(0)
	v_mfma_f32_16x16x32_f16 v[210:213], v[70:73], v[150:153], v[98:101]
	v_exp_f32_e32 v233, v233
	v_rcp_f32_e32 v230, v230
	v_add_f32_e32 v232, 1.0, v232
	v_mfma_f32_16x16x32_f16 v[214:217], v[74:77], v[150:153], v[102:105]
	v_fma_f32 v235, v233, s41, s41
	v_fma_f32 v236, -v228, v230, v230
	v_rcp_f32_e32 v232, v232
	v_fma_f32 v235, v231, v235, v235
	v_fma_f32 v198, v198, v227, v236
	v_rcp_f32_e32 v235, v235
	s_nop 0
	v_fma_f32 v231, -v233, v235, v235
	v_exp_f32_e32 v236, v198
	v_fma_f32 v199, v199, v232, v231
	v_exp_f32_e32 v231, v199
	v_add_f32_e32 v227, 1.0, v236
	v_add_f32_e32 v232, 1.0, v231
	v_add_u32_e32 v250, s43, v206
	v_fma_f32 v232, v234, v232, v232
	v_fma_f32 v227, v229, v227, v227
	v_add_u32_e32 v248, s43, v252
	v_rcp_f32_e32 v232, v232
	s_nop 0
	v_fma_f32 v231, -v231, v232, v232
	v_add_u32_e32 v249, s43, v253
	v_rcp_f32_e32 v227, v227
	s_nop 0
	v_fma_f32 v236, -v236, v227, v227
	v_cvt_pk_f16_f32 v247, v236, v231
	ds_write_b64 v250, v[246:247] offset:8192
	v_mfma_f32_16x16x32_f16 v[210:213], v[66:69], v[154:157], v[210:213]
	v_mfma_f32_16x16x32_f16 v[214:217], v[78:81], v[154:157], v[214:217]
	v_mov_b32_e32 v237, v246
	v_mov_b32_e32 v238, v247
	buffer_load_dwordx2 v[192:193], v209, s[20:23], s45 offen
	s_add_i32 s40, s40, 1
	s_add_i32 s44, s44, 0x1000
	s_waitcnt lgkmcnt(0)
	s_barrier
	ds_read_b128 v[158:161], v248 offset:0
	ds_read_b128 v[162:165], v248 offset:1024
	ds_read_b128 v[166:169], v249 offset:2048
	ds_read_b128 v[170:173], v249 offset:3072
	v_mfma_f32_16x16x32_f16 v[218:221], v[82:85], v[150:153], v[106:109]
	v_mfma_f32_16x16x32_f16 v[222:225], v[90:93], v[150:153], v[110:113]
	v_mfma_f32_16x16x32_f16 v[218:221], v[86:89], v[154:157], v[218:221]
	v_mfma_f32_16x16x32_f16 v[222:225], v[94:97], v[154:157], v[222:225]
	s_waitcnt lgkmcnt(2)
	v_mfma_f32_16x16x32_f16 v[210:213], v[54:57], v[158:161], v[210:213]
	v_mfma_f32_16x16x32_f16 v[210:213], v[58:61], v[162:165], v[210:213]
	s_waitcnt lgkmcnt(0)
	v_mfma_f32_16x16x32_f16 v[210:213], v[62:65], v[166:169], v[210:213]
	v_mfma_f32_16x16x32_f16 v[210:213], v[50:53], v[170:173], v[210:213]
	s_waitcnt vmcnt(9)
	v_cvt_pk_f16_f32 v251, v190, v191
	ds_write_b32 v1, v251 offset:2048
	ds_read_b128 v[150:153], v186 offset:0
	ds_read_b128 v[154:157], v186 offset:1024
	s_add_i32 s45, s45, 0x100000
	s_add_i32 s46, s46, 0x4000
	s_movk_i32 s47, 0x1000
	s_add_i32 s43, s40, -12
	s_lshl_b32 s43, s43, 12
	s_cmp_lt_u32 s40, 14
	s_cselect_b32 s43, s47, s43
	v_exp_f32_e32 v226, v210
	v_exp_f32_e32 v227, v211
	v_mfma_f32_16x16x32_f16 v[214:217], v[34:37], v[158:161], v[214:217]
	v_min_f32_e32 v228, s42, v212
	v_exp_f32_e32 v229, v213
	v_mfma_f32_16x16x32_f16 v[214:217], v[38:41], v[162:165], v[214:217]
	v_exp_f32_e32 v228, v228
	v_add_f32_e32 v227, 1.0, v227
	v_mfma_f32_16x16x32_f16 v[214:217], v[42:45], v[166:169], v[214:217]
	v_fma_f32 v230, v228, s41, s41
	v_rcp_f32_e32 v227, v227
	v_mfma_f32_16x16x32_f16 v[214:217], v[46:49], v[170:173], v[214:217]
	v_fma_f32 v230, v226, v230, v230
	v_rcp_f32_e32 v230, v230
	v_mfma_f32_16x16x32_f16 v[218:221], v[18:21], v[158:161], v[218:221]
	v_fma_f32 v226, -v228, v230, v230
	v_fma_f32 v200, v200, v227, v226
	v_mfma_f32_16x16x32_f16 v[218:221], v[14:17], v[162:165], v[218:221]
	v_exp_f32_e32 v226, v200
	s_nop 0
	v_add_f32_e32 v227, 1.0, v226
	v_mfma_f32_16x16x32_f16 v[218:221], v[10:13], v[166:169], v[218:221]
	v_fma_f32 v227, v229, v227, v227
	v_rcp_f32_e32 v227, v227
	v_mfma_f32_16x16x32_f16 v[218:221], v[26:29], v[170:173], v[218:221]
	v_fma_f32 v226, -v226, v227, v227
	v_exp_f32_e32 v231, v214
	v_mfma_f32_16x16x32_f16 v[222:225], v[2:5], v[158:161], v[222:225]
	v_exp_f32_e32 v232, v215
	v_min_f32_e32 v233, s42, v216
	v_mfma_f32_16x16x32_f16 v[222:225], v[6:9], v[162:165], v[222:225]
	v_exp_f32_e32 v234, v217
	v_exp_f32_e32 v233, v233
	v_mfma_f32_16x16x32_f16 v[222:225], v[22:25], v[166:169], v[222:225]
	v_exp_f32_e32 v236, v218
	v_add_f32_e32 v232, 1.0, v232
	v_mfma_f32_16x16x32_f16 v[222:225], v[30:33], v[170:173], v[222:225]
	v_fma_f32 v235, v233, s41, s41
	v_exp_f32_e32 v227, v219
	v_rcp_f32_e32 v232, v232
	v_fma_f32 v235, v231, v235, v235
	v_min_f32_e32 v228, s42, v220
	v_rcp_f32_e32 v235, v235
	s_nop 0
	v_fma_f32 v231, -v233, v235, v235
	v_exp_f32_e32 v229, v221
	v_fma_f32 v201, v201, v232, v231
	v_exp_f32_e32 v231, v201
	v_exp_f32_e32 v228, v228
	v_add_f32_e32 v232, 1.0, v231
	v_fma_f32 v232, v234, v232, v232
	v_add_f32_e32 v227, 1.0, v227
	v_rcp_f32_e32 v232, v232
	v_mfma_f32_16x16x32_f16 v[146:149], v[114:117], v[158:161], v[146:149]
	v_fma_f32 v231, -v231, v232, v232
	v_fma_f32 v230, v228, s41, s41
	v_cvt_pk_f16_f32 v246, v226, v231
	v_mfma_f32_16x16x32_f16 v[146:149], v[118:121], v[162:165], v[146:149]
	v_exp_f32_e32 v231, v222
	v_rcp_f32_e32 v227, v227
	v_exp_f32_e32 v232, v223
	buffer_load_dwordx4 v[114:117], v189, s[16:19], s46 offen
	buffer_load_dwordx4 v[118:121], v208, s[16:19], s46 offen
	v_min_f32_e32 v233, s42, v224
	v_fma_f32 v230, v236, v230, v230
	v_exp_f32_e32 v234, v225
	s_waitcnt lgkmcnt(0)
	v_mfma_f32_16x16x32_f16 v[210:213], v[70:73], v[150:153], v[98:101]
	v_exp_f32_e32 v233, v233
	v_rcp_f32_e32 v230, v230
	v_add_f32_e32 v232, 1.0, v232
	v_mfma_f32_16x16x32_f16 v[214:217], v[74:77], v[150:153], v[102:105]
	v_fma_f32 v235, v233, s41, s41
	v_fma_f32 v236, -v228, v230, v230
	v_rcp_f32_e32 v232, v232
	v_fma_f32 v235, v231, v235, v235
	v_fma_f32 v198, v198, v227, v236
	v_rcp_f32_e32 v235, v235
	s_nop 0
	v_fma_f32 v231, -v233, v235, v235
	v_exp_f32_e32 v236, v198
	v_fma_f32 v199, v199, v232, v231
	v_exp_f32_e32 v231, v199
	v_add_f32_e32 v227, 1.0, v236
	v_add_f32_e32 v232, 1.0, v231
	v_add_u32_e32 v250, s43, v206
	v_fma_f32 v232, v234, v232, v232
	v_fma_f32 v227, v229, v227, v227
	v_add_u32_e32 v248, s43, v252
	v_rcp_f32_e32 v232, v232
	s_nop 0
	v_fma_f32 v231, -v231, v232, v232
	v_add_u32_e32 v249, s43, v253
	v_rcp_f32_e32 v227, v227
	s_nop 0
	v_fma_f32 v236, -v236, v227, v227
	v_cvt_pk_f16_f32 v247, v236, v231
	ds_write_b64 v250, v[246:247] offset:8192
	v_mfma_f32_16x16x32_f16 v[210:213], v[66:69], v[154:157], v[210:213]
	v_mfma_f32_16x16x32_f16 v[214:217], v[78:81], v[154:157], v[214:217]
	v_mov_b32_e32 v239, v246
	v_mov_b32_e32 v240, v247
	buffer_load_dwordx2 v[190:191], v209, s[20:23], s45 offen
	s_add_i32 s40, s40, 1
	s_add_i32 s44, s44, 0x1000
	s_waitcnt lgkmcnt(0)
	s_barrier
	ds_read_b128 v[158:161], v248 offset:0
	ds_read_b128 v[162:165], v248 offset:1024
	ds_read_b128 v[166:169], v249 offset:2048
	ds_read_b128 v[170:173], v249 offset:3072
	v_mfma_f32_16x16x32_f16 v[218:221], v[82:85], v[150:153], v[106:109]
	v_mfma_f32_16x16x32_f16 v[222:225], v[90:93], v[150:153], v[110:113]
	v_mfma_f32_16x16x32_f16 v[218:221], v[86:89], v[154:157], v[218:221]
	v_mfma_f32_16x16x32_f16 v[222:225], v[94:97], v[154:157], v[222:225]
	s_waitcnt lgkmcnt(2)
	v_mfma_f32_16x16x32_f16 v[210:213], v[54:57], v[158:161], v[210:213]
	v_mfma_f32_16x16x32_f16 v[210:213], v[58:61], v[162:165], v[210:213]
	s_waitcnt lgkmcnt(0)
	v_mfma_f32_16x16x32_f16 v[210:213], v[62:65], v[166:169], v[210:213]
	v_mfma_f32_16x16x32_f16 v[210:213], v[50:53], v[170:173], v[210:213]
	s_waitcnt vmcnt(9)
	v_cvt_pk_f16_f32 v251, v196, v197
	ds_write_b32 v1, v251 offset:4096
	ds_read_b128 v[150:153], v186 offset:2048
	ds_read_b128 v[154:157], v186 offset:3072
	s_add_i32 s45, s45, 0x100000
	s_add_i32 s46, s46, 0x4000
	s_movk_i32 s47, 0x0
	s_add_i32 s43, s40, -12
	s_lshl_b32 s43, s43, 12
	s_cmp_lt_u32 s40, 14
	s_cselect_b32 s43, s47, s43
	v_exp_f32_e32 v226, v210
	v_exp_f32_e32 v227, v211
	v_mfma_f32_16x16x32_f16 v[214:217], v[34:37], v[158:161], v[214:217]
	v_min_f32_e32 v228, s42, v212
	v_exp_f32_e32 v229, v213
	v_mfma_f32_16x16x32_f16 v[214:217], v[38:41], v[162:165], v[214:217]
	v_exp_f32_e32 v228, v228
	v_add_f32_e32 v227, 1.0, v227
	v_mfma_f32_16x16x32_f16 v[214:217], v[42:45], v[166:169], v[214:217]
	v_fma_f32 v230, v228, s41, s41
	v_rcp_f32_e32 v227, v227
	v_mfma_f32_16x16x32_f16 v[214:217], v[46:49], v[170:173], v[214:217]
	v_fma_f32 v230, v226, v230, v230
	v_rcp_f32_e32 v230, v230
	v_mfma_f32_16x16x32_f16 v[218:221], v[18:21], v[158:161], v[218:221]
	v_fma_f32 v226, -v228, v230, v230
	v_fma_f32 v200, v200, v227, v226
	v_mfma_f32_16x16x32_f16 v[218:221], v[14:17], v[162:165], v[218:221]
	v_exp_f32_e32 v226, v200
	s_nop 0
	v_add_f32_e32 v227, 1.0, v226
	v_mfma_f32_16x16x32_f16 v[218:221], v[10:13], v[166:169], v[218:221]
	v_fma_f32 v227, v229, v227, v227
	v_rcp_f32_e32 v227, v227
	v_mfma_f32_16x16x32_f16 v[218:221], v[26:29], v[170:173], v[218:221]
	v_fma_f32 v226, -v226, v227, v227
	v_exp_f32_e32 v231, v214
	v_mfma_f32_16x16x32_f16 v[222:225], v[2:5], v[158:161], v[222:225]
	v_exp_f32_e32 v232, v215
	v_min_f32_e32 v233, s42, v216
	v_mfma_f32_16x16x32_f16 v[222:225], v[6:9], v[162:165], v[222:225]
	v_exp_f32_e32 v234, v217
	v_exp_f32_e32 v233, v233
	v_mfma_f32_16x16x32_f16 v[222:225], v[22:25], v[166:169], v[222:225]
	v_exp_f32_e32 v236, v218
	v_add_f32_e32 v232, 1.0, v232
	v_mfma_f32_16x16x32_f16 v[222:225], v[30:33], v[170:173], v[222:225]
	v_fma_f32 v235, v233, s41, s41
	v_exp_f32_e32 v227, v219
	v_rcp_f32_e32 v232, v232
	v_fma_f32 v235, v231, v235, v235
	v_min_f32_e32 v228, s42, v220
	v_rcp_f32_e32 v235, v235
	s_nop 0
	v_fma_f32 v231, -v233, v235, v235
	v_exp_f32_e32 v229, v221
	v_fma_f32 v201, v201, v232, v231
	v_exp_f32_e32 v231, v201
	v_exp_f32_e32 v228, v228
	v_add_f32_e32 v232, 1.0, v231
	v_fma_f32 v232, v234, v232, v232
	v_add_f32_e32 v227, 1.0, v227
	v_rcp_f32_e32 v232, v232
	v_mfma_f32_16x16x32_f16 v[146:149], v[138:141], v[158:161], v[146:149]
	v_fma_f32 v231, -v231, v232, v232
	v_fma_f32 v230, v228, s41, s41
	v_cvt_pk_f16_f32 v246, v226, v231
	v_mfma_f32_16x16x32_f16 v[146:149], v[142:145], v[162:165], v[146:149]
	v_exp_f32_e32 v231, v222
	v_rcp_f32_e32 v227, v227
	v_exp_f32_e32 v232, v223
	buffer_load_dwordx4 v[138:141], v189, s[16:19], s46 offen
	buffer_load_dwordx4 v[142:145], v208, s[16:19], s46 offen
	v_min_f32_e32 v233, s42, v224
	v_fma_f32 v230, v236, v230, v230
	v_exp_f32_e32 v234, v225
	s_waitcnt lgkmcnt(0)
	v_mfma_f32_16x16x32_f16 v[210:213], v[70:73], v[150:153], v[98:101]
	v_exp_f32_e32 v233, v233
	v_rcp_f32_e32 v230, v230
	v_add_f32_e32 v232, 1.0, v232
	v_mfma_f32_16x16x32_f16 v[214:217], v[74:77], v[150:153], v[102:105]
	v_fma_f32 v235, v233, s41, s41
	v_fma_f32 v236, -v228, v230, v230
	v_rcp_f32_e32 v232, v232
	v_fma_f32 v235, v231, v235, v235
	v_fma_f32 v198, v198, v227, v236
	v_rcp_f32_e32 v235, v235
	s_nop 0
	v_fma_f32 v231, -v233, v235, v235
	v_exp_f32_e32 v236, v198
	v_fma_f32 v199, v199, v232, v231
	v_exp_f32_e32 v231, v199
	v_add_f32_e32 v227, 1.0, v236
	v_add_f32_e32 v232, 1.0, v231
	v_add_u32_e32 v250, s43, v206
	v_fma_f32 v232, v234, v232, v232
	v_fma_f32 v227, v229, v227, v227
	v_add_u32_e32 v248, s43, v252
	v_rcp_f32_e32 v232, v232
	s_nop 0
	v_fma_f32 v231, -v231, v232, v232
	v_add_u32_e32 v249, s43, v253
	v_rcp_f32_e32 v227, v227
	s_nop 0
	v_fma_f32 v236, -v236, v227, v227
	v_cvt_pk_f16_f32 v247, v236, v231
	ds_write_b64 v250, v[246:247] offset:8192
	v_mfma_f32_16x16x32_f16 v[210:213], v[66:69], v[154:157], v[210:213]
	v_mfma_f32_16x16x32_f16 v[214:217], v[78:81], v[154:157], v[214:217]
	v_mov_b32_e32 v241, v246
	v_mov_b32_e32 v242, v247
	buffer_load_dwordx2 v[196:197], v209, s[20:23], s45 offen
	s_add_i32 s40, s40, 1
	s_add_i32 s44, s44, 0x1000
	s_waitcnt lgkmcnt(0)
	s_barrier
	ds_read_b128 v[158:161], v248 offset:0
	ds_read_b128 v[162:165], v248 offset:1024
	ds_read_b128 v[166:169], v249 offset:2048
	ds_read_b128 v[170:173], v249 offset:3072
	v_mfma_f32_16x16x32_f16 v[218:221], v[82:85], v[150:153], v[106:109]
	v_mfma_f32_16x16x32_f16 v[222:225], v[90:93], v[150:153], v[110:113]
	v_mfma_f32_16x16x32_f16 v[218:221], v[86:89], v[154:157], v[218:221]
	v_mfma_f32_16x16x32_f16 v[222:225], v[94:97], v[154:157], v[222:225]
	s_waitcnt lgkmcnt(2)
	v_mfma_f32_16x16x32_f16 v[210:213], v[54:57], v[158:161], v[210:213]
	v_mfma_f32_16x16x32_f16 v[210:213], v[58:61], v[162:165], v[210:213]
	s_waitcnt lgkmcnt(0)
	v_mfma_f32_16x16x32_f16 v[210:213], v[62:65], v[166:169], v[210:213]
	v_mfma_f32_16x16x32_f16 v[210:213], v[50:53], v[170:173], v[210:213]
	s_waitcnt vmcnt(9)
	v_cvt_pk_f16_f32 v251, v194, v195
	ds_write_b32 v1, v251 offset:6144
	ds_read_b128 v[150:153], v186 offset:4096
	ds_read_b128 v[154:157], v186 offset:5120
	s_add_i32 s45, s45, 0x100000
	s_add_i32 s46, s46, 0x4000
	s_movk_i32 s47, 0x1000
	s_add_i32 s43, s40, -12
	s_lshl_b32 s43, s43, 12
	s_cmp_lt_u32 s40, 14
	s_cselect_b32 s43, s47, s43
	v_exp_f32_e32 v226, v210
	v_exp_f32_e32 v227, v211
	v_mfma_f32_16x16x32_f16 v[214:217], v[34:37], v[158:161], v[214:217]
	v_min_f32_e32 v228, s42, v212
	v_exp_f32_e32 v229, v213
	v_mfma_f32_16x16x32_f16 v[214:217], v[38:41], v[162:165], v[214:217]
	v_exp_f32_e32 v228, v228
	v_add_f32_e32 v227, 1.0, v227
	v_mfma_f32_16x16x32_f16 v[214:217], v[42:45], v[166:169], v[214:217]
	v_fma_f32 v230, v228, s41, s41
	v_rcp_f32_e32 v227, v227
	v_mfma_f32_16x16x32_f16 v[214:217], v[46:49], v[170:173], v[214:217]
	v_fma_f32 v230, v226, v230, v230
	v_rcp_f32_e32 v230, v230
	v_mfma_f32_16x16x32_f16 v[218:221], v[18:21], v[158:161], v[218:221]
	v_fma_f32 v226, -v228, v230, v230
	v_fma_f32 v200, v200, v227, v226
	v_mfma_f32_16x16x32_f16 v[218:221], v[14:17], v[162:165], v[218:221]
	v_exp_f32_e32 v226, v200
	s_nop 0
	v_add_f32_e32 v227, 1.0, v226
	v_mfma_f32_16x16x32_f16 v[218:221], v[10:13], v[166:169], v[218:221]
	v_fma_f32 v227, v229, v227, v227
	v_rcp_f32_e32 v227, v227
	v_mfma_f32_16x16x32_f16 v[218:221], v[26:29], v[170:173], v[218:221]
	v_fma_f32 v226, -v226, v227, v227
	v_exp_f32_e32 v231, v214
	v_mfma_f32_16x16x32_f16 v[222:225], v[2:5], v[158:161], v[222:225]
	v_exp_f32_e32 v232, v215
	v_min_f32_e32 v233, s42, v216
	v_mfma_f32_16x16x32_f16 v[222:225], v[6:9], v[162:165], v[222:225]
	v_exp_f32_e32 v234, v217
	v_exp_f32_e32 v233, v233
	v_mfma_f32_16x16x32_f16 v[222:225], v[22:25], v[166:169], v[222:225]
	v_exp_f32_e32 v236, v218
	v_add_f32_e32 v232, 1.0, v232
	v_mfma_f32_16x16x32_f16 v[222:225], v[30:33], v[170:173], v[222:225]
	v_fma_f32 v235, v233, s41, s41
	v_exp_f32_e32 v227, v219
	v_rcp_f32_e32 v232, v232
	v_fma_f32 v235, v231, v235, v235
	v_min_f32_e32 v228, s42, v220
	v_rcp_f32_e32 v235, v235
	s_nop 0
	v_fma_f32 v231, -v233, v235, v235
	v_exp_f32_e32 v229, v221
	v_fma_f32 v201, v201, v232, v231
	v_exp_f32_e32 v231, v201
	v_exp_f32_e32 v228, v228
	v_add_f32_e32 v232, 1.0, v231
	v_fma_f32 v232, v234, v232, v232
	v_add_f32_e32 v227, 1.0, v227
	v_rcp_f32_e32 v232, v232
	v_mfma_f32_16x16x32_f16 v[146:149], v[130:133], v[158:161], v[146:149]
	v_fma_f32 v231, -v231, v232, v232
	v_fma_f32 v230, v228, s41, s41
	v_cvt_pk_f16_f32 v246, v226, v231
	v_mfma_f32_16x16x32_f16 v[146:149], v[134:137], v[162:165], v[146:149]
	v_exp_f32_e32 v231, v222
	v_rcp_f32_e32 v227, v227
	v_exp_f32_e32 v232, v223
	buffer_load_dwordx4 v[130:133], v189, s[16:19], s46 offen
	buffer_load_dwordx4 v[134:137], v208, s[16:19], s46 offen
	v_min_f32_e32 v233, s42, v224
	v_fma_f32 v230, v236, v230, v230
	v_exp_f32_e32 v234, v225
	s_waitcnt lgkmcnt(0)
	v_mfma_f32_16x16x32_f16 v[210:213], v[70:73], v[150:153], v[98:101]
	v_exp_f32_e32 v233, v233
	v_rcp_f32_e32 v230, v230
	v_add_f32_e32 v232, 1.0, v232
	v_mfma_f32_16x16x32_f16 v[214:217], v[74:77], v[150:153], v[102:105]
	v_fma_f32 v235, v233, s41, s41
	v_fma_f32 v236, -v228, v230, v230
	v_rcp_f32_e32 v232, v232
	v_fma_f32 v235, v231, v235, v235
	v_fma_f32 v198, v198, v227, v236
	v_rcp_f32_e32 v235, v235
	s_nop 0
	v_fma_f32 v231, -v233, v235, v235
	v_exp_f32_e32 v236, v198
	v_fma_f32 v199, v199, v232, v231
	v_exp_f32_e32 v231, v199
	v_add_f32_e32 v227, 1.0, v236
	v_add_f32_e32 v232, 1.0, v231
	v_add_u32_e32 v250, s43, v206
	v_fma_f32 v232, v234, v232, v232
	v_fma_f32 v227, v229, v227, v227
	v_add_u32_e32 v248, s43, v252
	v_rcp_f32_e32 v232, v232
	s_nop 0
	v_fma_f32 v231, -v231, v232, v232
	v_add_u32_e32 v249, s43, v253
	v_rcp_f32_e32 v227, v227
	s_nop 0
	v_fma_f32 v236, -v236, v227, v227
	v_cvt_pk_f16_f32 v247, v236, v231
	ds_write_b64 v250, v[246:247] offset:8192
	v_mfma_f32_16x16x32_f16 v[210:213], v[66:69], v[154:157], v[210:213]
	v_mfma_f32_16x16x32_f16 v[214:217], v[78:81], v[154:157], v[214:217]
	v_mov_b32_e32 v243, v246
	v_mov_b32_e32 v244, v247
	buffer_load_dwordx2 v[194:195], v209, s[20:23], s45 offen
	s_add_i32 s40, s40, 1
	s_add_i32 s44, s44, 0x1000
	s_waitcnt lgkmcnt(0)
	s_barrier
	ds_read_b128 v[158:161], v248 offset:0
	ds_read_b128 v[162:165], v248 offset:1024
	ds_read_b128 v[166:169], v249 offset:2048
	ds_read_b128 v[170:173], v249 offset:3072
	v_mfma_f32_16x16x32_f16 v[218:221], v[82:85], v[150:153], v[106:109]
	v_mfma_f32_16x16x32_f16 v[222:225], v[90:93], v[150:153], v[110:113]
	v_mfma_f32_16x16x32_f16 v[218:221], v[86:89], v[154:157], v[218:221]
	v_mfma_f32_16x16x32_f16 v[222:225], v[94:97], v[154:157], v[222:225]
	s_waitcnt lgkmcnt(2)
	v_mfma_f32_16x16x32_f16 v[210:213], v[54:57], v[158:161], v[210:213]
	v_mfma_f32_16x16x32_f16 v[210:213], v[58:61], v[162:165], v[210:213]
	s_waitcnt lgkmcnt(0)
	v_mfma_f32_16x16x32_f16 v[210:213], v[62:65], v[166:169], v[210:213]
	v_mfma_f32_16x16x32_f16 v[210:213], v[50:53], v[170:173], v[210:213]
	s_waitcnt vmcnt(9)
	v_cvt_pk_f16_f32 v251, v192, v193
	ds_write_b32 v1, v251 offset:0
	ds_read_b128 v[150:153], v186 offset:6144
	ds_read_b128 v[154:157], v186 offset:7168
	s_add_i32 s45, s45, 0x100000
	s_add_i32 s46, s46, 0x4000
	s_movk_i32 s47, 0x0
	s_add_i32 s43, s40, -12
	s_lshl_b32 s43, s43, 12
	s_cmp_lt_u32 s40, 14
	s_cselect_b32 s43, s47, s43
	v_exp_f32_e32 v226, v210
	v_exp_f32_e32 v227, v211
	v_mfma_f32_16x16x32_f16 v[214:217], v[34:37], v[158:161], v[214:217]
	v_min_f32_e32 v228, s42, v212
	v_exp_f32_e32 v229, v213
	v_mfma_f32_16x16x32_f16 v[214:217], v[38:41], v[162:165], v[214:217]
	v_exp_f32_e32 v228, v228
	v_add_f32_e32 v227, 1.0, v227
	v_mfma_f32_16x16x32_f16 v[214:217], v[42:45], v[166:169], v[214:217]
	v_fma_f32 v230, v228, s41, s41
	v_rcp_f32_e32 v227, v227
	v_mfma_f32_16x16x32_f16 v[214:217], v[46:49], v[170:173], v[214:217]
	v_fma_f32 v230, v226, v230, v230
	v_rcp_f32_e32 v230, v230
	v_mfma_f32_16x16x32_f16 v[218:221], v[18:21], v[158:161], v[218:221]
	v_fma_f32 v226, -v228, v230, v230
	v_fma_f32 v200, v200, v227, v226
	v_mfma_f32_16x16x32_f16 v[218:221], v[14:17], v[162:165], v[218:221]
	v_exp_f32_e32 v226, v200
	s_nop 0
	v_add_f32_e32 v227, 1.0, v226
	v_mfma_f32_16x16x32_f16 v[218:221], v[10:13], v[166:169], v[218:221]
	v_fma_f32 v227, v229, v227, v227
	v_rcp_f32_e32 v227, v227
	v_mfma_f32_16x16x32_f16 v[218:221], v[26:29], v[170:173], v[218:221]
	v_fma_f32 v226, -v226, v227, v227
	v_exp_f32_e32 v231, v214
	v_mfma_f32_16x16x32_f16 v[222:225], v[2:5], v[158:161], v[222:225]
	v_exp_f32_e32 v232, v215
	v_min_f32_e32 v233, s42, v216
	v_mfma_f32_16x16x32_f16 v[222:225], v[6:9], v[162:165], v[222:225]
	v_exp_f32_e32 v234, v217
	v_exp_f32_e32 v233, v233
	v_mfma_f32_16x16x32_f16 v[222:225], v[22:25], v[166:169], v[222:225]
	v_exp_f32_e32 v236, v218
	v_add_f32_e32 v232, 1.0, v232
	v_mfma_f32_16x16x32_f16 v[222:225], v[30:33], v[170:173], v[222:225]
	v_fma_f32 v235, v233, s41, s41
	v_exp_f32_e32 v227, v219
	v_rcp_f32_e32 v232, v232
	v_fma_f32 v235, v231, v235, v235
	v_min_f32_e32 v228, s42, v220
	v_rcp_f32_e32 v235, v235
	s_nop 0
	v_fma_f32 v231, -v233, v235, v235
	v_exp_f32_e32 v229, v221
	v_fma_f32 v201, v201, v232, v231
	v_exp_f32_e32 v231, v201
	v_exp_f32_e32 v228, v228
	v_add_f32_e32 v232, 1.0, v231
	v_fma_f32 v232, v234, v232, v232
	v_add_f32_e32 v227, 1.0, v227
	v_rcp_f32_e32 v232, v232
	v_mfma_f32_16x16x32_f16 v[146:149], v[122:125], v[158:161], v[146:149]
	v_fma_f32 v231, -v231, v232, v232
	v_fma_f32 v230, v228, s41, s41
	v_cvt_pk_f16_f32 v246, v226, v231
	v_mfma_f32_16x16x32_f16 v[146:149], v[126:129], v[162:165], v[146:149]
	v_exp_f32_e32 v231, v222
	v_rcp_f32_e32 v227, v227
	v_exp_f32_e32 v232, v223
	buffer_load_dwordx4 v[122:125], v189, s[16:19], s46 offen
	buffer_load_dwordx4 v[126:129], v208, s[16:19], s46 offen
	v_min_f32_e32 v233, s42, v224
	v_fma_f32 v230, v236, v230, v230
	v_exp_f32_e32 v234, v225
	s_waitcnt lgkmcnt(0)
	v_mfma_f32_16x16x32_f16 v[210:213], v[70:73], v[150:153], v[98:101]
	v_exp_f32_e32 v233, v233
	v_rcp_f32_e32 v230, v230
	v_add_f32_e32 v232, 1.0, v232
	v_mfma_f32_16x16x32_f16 v[214:217], v[74:77], v[150:153], v[102:105]
	v_fma_f32 v235, v233, s41, s41
	v_fma_f32 v236, -v228, v230, v230
	v_rcp_f32_e32 v232, v232
	v_fma_f32 v235, v231, v235, v235
	v_fma_f32 v198, v198, v227, v236
	v_rcp_f32_e32 v235, v235
	s_nop 0
	v_fma_f32 v231, -v233, v235, v235
	v_exp_f32_e32 v236, v198
	v_fma_f32 v199, v199, v232, v231
	v_exp_f32_e32 v231, v199
	v_add_f32_e32 v227, 1.0, v236
	v_add_f32_e32 v232, 1.0, v231
	v_add_u32_e32 v250, s43, v206
	v_fma_f32 v232, v234, v232, v232
	v_fma_f32 v227, v229, v227, v227
	v_add_u32_e32 v248, s43, v252
	v_rcp_f32_e32 v232, v232
	s_nop 0
	v_fma_f32 v231, -v231, v232, v232
	v_add_u32_e32 v249, s43, v253
	v_rcp_f32_e32 v227, v227
	s_nop 0
	v_fma_f32 v236, -v236, v227, v227
	v_cvt_pk_f16_f32 v247, v236, v231
	ds_write_b64 v250, v[246:247] offset:8192
	v_mfma_f32_16x16x32_f16 v[210:213], v[66:69], v[154:157], v[210:213]
	v_mfma_f32_16x16x32_f16 v[214:217], v[78:81], v[154:157], v[214:217]
	v_mov_b32_e32 v245, v246
	v_mov_b32_e32 v187, v247
	buffer_load_dwordx2 v[192:193], v209, s[20:23], s45 offen
	s_add_i32 s40, s40, 1
	s_add_i32 s44, s44, 0x1000
	s_waitcnt lgkmcnt(0)
	s_barrier
	ds_read_b128 v[158:161], v248 offset:0
	ds_read_b128 v[162:165], v248 offset:1024
	ds_read_b128 v[166:169], v249 offset:2048
	ds_read_b128 v[170:173], v249 offset:3072
	v_mfma_f32_16x16x32_f16 v[218:221], v[82:85], v[150:153], v[106:109]
	v_mfma_f32_16x16x32_f16 v[222:225], v[90:93], v[150:153], v[110:113]
	v_mfma_f32_16x16x32_f16 v[218:221], v[86:89], v[154:157], v[218:221]
	v_mfma_f32_16x16x32_f16 v[222:225], v[94:97], v[154:157], v[222:225]
	s_waitcnt lgkmcnt(2)
	v_mfma_f32_16x16x32_f16 v[210:213], v[54:57], v[158:161], v[210:213]
	v_mfma_f32_16x16x32_f16 v[210:213], v[58:61], v[162:165], v[210:213]
	s_waitcnt lgkmcnt(0)
	v_mfma_f32_16x16x32_f16 v[210:213], v[62:65], v[166:169], v[210:213]
	v_mfma_f32_16x16x32_f16 v[210:213], v[50:53], v[170:173], v[210:213]
	s_waitcnt vmcnt(9)
	v_cvt_pk_f16_f32 v251, v190, v191
	ds_write_b32 v1, v251 offset:2048
	ds_read_b128 v[150:153], v186 offset:0
	ds_read_b128 v[154:157], v186 offset:1024
	s_add_i32 s45, s45, 0x100000
	s_add_i32 s46, s46, 0x4000
	s_movk_i32 s47, 0x1000
	s_add_i32 s43, s40, -12
	s_lshl_b32 s43, s43, 12
	s_cmp_lt_u32 s40, 14
	s_cselect_b32 s43, s47, s43
	v_exp_f32_e32 v226, v210
	v_exp_f32_e32 v227, v211
	v_mfma_f32_16x16x32_f16 v[214:217], v[34:37], v[158:161], v[214:217]
	v_min_f32_e32 v228, s42, v212
	v_exp_f32_e32 v229, v213
	v_mfma_f32_16x16x32_f16 v[214:217], v[38:41], v[162:165], v[214:217]
	v_exp_f32_e32 v228, v228
	v_add_f32_e32 v227, 1.0, v227
	v_mfma_f32_16x16x32_f16 v[214:217], v[42:45], v[166:169], v[214:217]
	v_fma_f32 v230, v228, s41, s41
	v_rcp_f32_e32 v227, v227
	v_mfma_f32_16x16x32_f16 v[214:217], v[46:49], v[170:173], v[214:217]
	v_fma_f32 v230, v226, v230, v230
	v_rcp_f32_e32 v230, v230
	v_mfma_f32_16x16x32_f16 v[218:221], v[18:21], v[158:161], v[218:221]
	v_fma_f32 v226, -v228, v230, v230
	v_fma_f32 v200, v200, v227, v226
	v_mfma_f32_16x16x32_f16 v[218:221], v[14:17], v[162:165], v[218:221]
	v_exp_f32_e32 v226, v200
	s_nop 0
	v_add_f32_e32 v227, 1.0, v226
	v_mfma_f32_16x16x32_f16 v[218:221], v[10:13], v[166:169], v[218:221]
	v_fma_f32 v227, v229, v227, v227
	v_rcp_f32_e32 v227, v227
	v_mfma_f32_16x16x32_f16 v[218:221], v[26:29], v[170:173], v[218:221]
	v_fma_f32 v226, -v226, v227, v227
	v_exp_f32_e32 v231, v214
	v_mfma_f32_16x16x32_f16 v[222:225], v[2:5], v[158:161], v[222:225]
	v_exp_f32_e32 v232, v215
	v_min_f32_e32 v233, s42, v216
	v_mfma_f32_16x16x32_f16 v[222:225], v[6:9], v[162:165], v[222:225]
	v_exp_f32_e32 v234, v217
	v_exp_f32_e32 v233, v233
	v_mfma_f32_16x16x32_f16 v[222:225], v[22:25], v[166:169], v[222:225]
	v_exp_f32_e32 v236, v218
	v_add_f32_e32 v232, 1.0, v232
	v_mfma_f32_16x16x32_f16 v[222:225], v[30:33], v[170:173], v[222:225]
	v_fma_f32 v235, v233, s41, s41
	v_exp_f32_e32 v227, v219
	v_rcp_f32_e32 v232, v232
	v_fma_f32 v235, v231, v235, v235
	v_min_f32_e32 v228, s42, v220
	v_rcp_f32_e32 v235, v235
	s_nop 0
	v_fma_f32 v231, -v233, v235, v235
	v_exp_f32_e32 v229, v221
	v_fma_f32 v201, v201, v232, v231
	v_exp_f32_e32 v231, v201
	v_exp_f32_e32 v228, v228
	v_add_f32_e32 v232, 1.0, v231
	v_fma_f32 v232, v234, v232, v232
	v_add_f32_e32 v227, 1.0, v227
	v_rcp_f32_e32 v232, v232
	v_mfma_f32_16x16x32_f16 v[146:149], v[114:117], v[158:161], v[146:149]
	v_fma_f32 v231, -v231, v232, v232
	v_fma_f32 v230, v228, s41, s41
	v_cvt_pk_f16_f32 v246, v226, v231
	v_mfma_f32_16x16x32_f16 v[146:149], v[118:121], v[162:165], v[146:149]
	v_exp_f32_e32 v231, v222
	v_rcp_f32_e32 v227, v227
	v_exp_f32_e32 v232, v223
	buffer_load_dwordx4 v[114:117], v189, s[16:19], s46 offen
	buffer_load_dwordx4 v[118:121], v208, s[16:19], s46 offen
	v_min_f32_e32 v233, s42, v224
	v_fma_f32 v230, v236, v230, v230
	v_exp_f32_e32 v234, v225
	s_waitcnt lgkmcnt(0)
	v_mfma_f32_16x16x32_f16 v[210:213], v[70:73], v[150:153], v[98:101]
	v_exp_f32_e32 v233, v233
	v_rcp_f32_e32 v230, v230
	v_add_f32_e32 v232, 1.0, v232
	v_mfma_f32_16x16x32_f16 v[214:217], v[74:77], v[150:153], v[102:105]
	v_fma_f32 v235, v233, s41, s41
	v_fma_f32 v236, -v228, v230, v230
	v_rcp_f32_e32 v232, v232
	v_fma_f32 v235, v231, v235, v235
	v_fma_f32 v198, v198, v227, v236
	v_rcp_f32_e32 v235, v235
	s_nop 0
	v_fma_f32 v231, -v233, v235, v235
	v_exp_f32_e32 v236, v198
	v_fma_f32 v199, v199, v232, v231
	v_exp_f32_e32 v231, v199
	v_add_f32_e32 v227, 1.0, v236
	v_add_f32_e32 v232, 1.0, v231
	v_add_u32_e32 v250, s43, v206
	v_fma_f32 v232, v234, v232, v232
	v_fma_f32 v227, v229, v227, v227
	v_add_u32_e32 v248, s43, v252
	v_rcp_f32_e32 v232, v232
	s_nop 0
	v_fma_f32 v231, -v231, v232, v232
	v_add_u32_e32 v249, s43, v253
	v_rcp_f32_e32 v227, v227
	s_nop 0
	v_fma_f32 v236, -v236, v227, v227
	v_cvt_pk_f16_f32 v247, v236, v231
	ds_write_b64 v250, v[246:247] offset:8192
	v_mfma_f32_16x16x32_f16 v[210:213], v[66:69], v[154:157], v[210:213]
	v_mfma_f32_16x16x32_f16 v[214:217], v[78:81], v[154:157], v[214:217]
	v_mov_b32_e32 v188, v246
	v_mov_b32_e32 v202, v247
	buffer_load_dwordx2 v[190:191], v209, s[20:23], s45 offen
	s_add_i32 s40, s40, 1
	s_add_i32 s44, s44, 0x1000
	s_waitcnt lgkmcnt(0)
	s_barrier
	ds_read_b128 v[158:161], v248 offset:0
	ds_read_b128 v[162:165], v248 offset:1024
	ds_read_b128 v[166:169], v249 offset:2048
	ds_read_b128 v[170:173], v249 offset:3072
	v_mfma_f32_16x16x32_f16 v[218:221], v[82:85], v[150:153], v[106:109]
	v_mfma_f32_16x16x32_f16 v[222:225], v[90:93], v[150:153], v[110:113]
	v_mfma_f32_16x16x32_f16 v[218:221], v[86:89], v[154:157], v[218:221]
	v_mfma_f32_16x16x32_f16 v[222:225], v[94:97], v[154:157], v[222:225]
	s_waitcnt lgkmcnt(2)
	v_mfma_f32_16x16x32_f16 v[210:213], v[54:57], v[158:161], v[210:213]
	v_mfma_f32_16x16x32_f16 v[210:213], v[58:61], v[162:165], v[210:213]
	s_waitcnt lgkmcnt(0)
	v_mfma_f32_16x16x32_f16 v[210:213], v[62:65], v[166:169], v[210:213]
	v_mfma_f32_16x16x32_f16 v[210:213], v[50:53], v[170:173], v[210:213]
	s_waitcnt vmcnt(9)
	v_cvt_pk_f16_f32 v251, v196, v197
	ds_write_b32 v1, v251 offset:4096
	ds_read_b128 v[150:153], v186 offset:2048
	ds_read_b128 v[154:157], v186 offset:3072
	s_add_i32 s45, s45, 0x100000
	s_add_i32 s46, s46, 0x4000
	s_movk_i32 s47, 0x0
	s_add_i32 s43, s40, -12
	s_lshl_b32 s43, s43, 12
	s_cmp_lt_u32 s40, 14
	s_cselect_b32 s43, s47, s43
	v_exp_f32_e32 v226, v210
	v_exp_f32_e32 v227, v211
	v_mfma_f32_16x16x32_f16 v[214:217], v[34:37], v[158:161], v[214:217]
	v_min_f32_e32 v228, s42, v212
	v_exp_f32_e32 v229, v213
	v_mfma_f32_16x16x32_f16 v[214:217], v[38:41], v[162:165], v[214:217]
	v_exp_f32_e32 v228, v228
	v_add_f32_e32 v227, 1.0, v227
	v_mfma_f32_16x16x32_f16 v[214:217], v[42:45], v[166:169], v[214:217]
	v_fma_f32 v230, v228, s41, s41
	v_rcp_f32_e32 v227, v227
	v_mfma_f32_16x16x32_f16 v[214:217], v[46:49], v[170:173], v[214:217]
	v_fma_f32 v230, v226, v230, v230
	v_rcp_f32_e32 v230, v230
	v_mfma_f32_16x16x32_f16 v[218:221], v[18:21], v[158:161], v[218:221]
	v_fma_f32 v226, -v228, v230, v230
	v_fma_f32 v200, v200, v227, v226
	v_mfma_f32_16x16x32_f16 v[218:221], v[14:17], v[162:165], v[218:221]
	v_exp_f32_e32 v226, v200
	s_nop 0
	v_add_f32_e32 v227, 1.0, v226
	v_mfma_f32_16x16x32_f16 v[218:221], v[10:13], v[166:169], v[218:221]
	v_fma_f32 v227, v229, v227, v227
	v_rcp_f32_e32 v227, v227
	v_mfma_f32_16x16x32_f16 v[218:221], v[26:29], v[170:173], v[218:221]
	v_fma_f32 v226, -v226, v227, v227
	v_exp_f32_e32 v231, v214
	v_mfma_f32_16x16x32_f16 v[222:225], v[2:5], v[158:161], v[222:225]
	v_exp_f32_e32 v232, v215
	v_min_f32_e32 v233, s42, v216
	v_mfma_f32_16x16x32_f16 v[222:225], v[6:9], v[162:165], v[222:225]
	v_exp_f32_e32 v234, v217
	v_exp_f32_e32 v233, v233
	v_mfma_f32_16x16x32_f16 v[222:225], v[22:25], v[166:169], v[222:225]
	v_exp_f32_e32 v236, v218
	v_add_f32_e32 v232, 1.0, v232
	v_mfma_f32_16x16x32_f16 v[222:225], v[30:33], v[170:173], v[222:225]
	v_fma_f32 v235, v233, s41, s41
	v_exp_f32_e32 v227, v219
	v_rcp_f32_e32 v232, v232
	v_fma_f32 v235, v231, v235, v235
	v_min_f32_e32 v228, s42, v220
	v_rcp_f32_e32 v235, v235
	s_nop 0
	v_fma_f32 v231, -v233, v235, v235
	v_exp_f32_e32 v229, v221
	v_fma_f32 v201, v201, v232, v231
	v_exp_f32_e32 v231, v201
	v_exp_f32_e32 v228, v228
	v_add_f32_e32 v232, 1.0, v231
	v_fma_f32 v232, v234, v232, v232
	v_add_f32_e32 v227, 1.0, v227
	v_rcp_f32_e32 v232, v232
	v_mfma_f32_16x16x32_f16 v[146:149], v[138:141], v[158:161], v[146:149]
	v_fma_f32 v231, -v231, v232, v232
	v_fma_f32 v230, v228, s41, s41
	v_cvt_pk_f16_f32 v246, v226, v231
	v_mfma_f32_16x16x32_f16 v[146:149], v[142:145], v[162:165], v[146:149]
	v_exp_f32_e32 v231, v222
	v_rcp_f32_e32 v227, v227
	v_exp_f32_e32 v232, v223
	buffer_load_dwordx4 v[138:141], v189, s[16:19], s46 offen
	buffer_load_dwordx4 v[142:145], v208, s[16:19], s46 offen
	v_min_f32_e32 v233, s42, v224
	v_fma_f32 v230, v236, v230, v230
	v_exp_f32_e32 v234, v225
	s_waitcnt lgkmcnt(0)
	v_mfma_f32_16x16x32_f16 v[210:213], v[70:73], v[150:153], v[98:101]
	v_exp_f32_e32 v233, v233
	v_rcp_f32_e32 v230, v230
	v_add_f32_e32 v232, 1.0, v232
	v_mfma_f32_16x16x32_f16 v[214:217], v[74:77], v[150:153], v[102:105]
	v_fma_f32 v235, v233, s41, s41
	v_fma_f32 v236, -v228, v230, v230
	v_rcp_f32_e32 v232, v232
	v_fma_f32 v235, v231, v235, v235
	v_fma_f32 v198, v198, v227, v236
	v_rcp_f32_e32 v235, v235
	s_nop 0
	v_fma_f32 v231, -v233, v235, v235
	v_exp_f32_e32 v236, v198
	v_fma_f32 v199, v199, v232, v231
	v_exp_f32_e32 v231, v199
	v_add_f32_e32 v227, 1.0, v236
	v_add_f32_e32 v232, 1.0, v231
	v_add_u32_e32 v250, s43, v206
	v_fma_f32 v232, v234, v232, v232
	v_fma_f32 v227, v229, v227, v227
	v_add_u32_e32 v248, s43, v252
	v_rcp_f32_e32 v232, v232
	s_nop 0
	v_fma_f32 v231, -v231, v232, v232
	v_add_u32_e32 v249, s43, v253
	v_rcp_f32_e32 v227, v227
	s_nop 0
	v_fma_f32 v236, -v236, v227, v227
	v_cvt_pk_f16_f32 v247, v236, v231
	ds_write_b64 v250, v[246:247] offset:8192
	v_mfma_f32_16x16x32_f16 v[210:213], v[66:69], v[154:157], v[210:213]
	v_mfma_f32_16x16x32_f16 v[214:217], v[78:81], v[154:157], v[214:217]
	v_mov_b32_e32 v203, v246
	v_mov_b32_e32 v204, v247
	buffer_load_dwordx2 v[196:197], v209, s[20:23], s45 offen
	s_add_i32 s40, s40, 1
	s_add_i32 s44, s44, 0x1000
	s_waitcnt lgkmcnt(0)
	s_barrier
	ds_read_b128 v[158:161], v248 offset:0
	ds_read_b128 v[162:165], v248 offset:1024
	ds_read_b128 v[166:169], v249 offset:2048
	ds_read_b128 v[170:173], v249 offset:3072
	v_mfma_f32_16x16x32_f16 v[218:221], v[82:85], v[150:153], v[106:109]
	v_mfma_f32_16x16x32_f16 v[222:225], v[90:93], v[150:153], v[110:113]
	v_mfma_f32_16x16x32_f16 v[218:221], v[86:89], v[154:157], v[218:221]
	v_mfma_f32_16x16x32_f16 v[222:225], v[94:97], v[154:157], v[222:225]
	s_waitcnt lgkmcnt(2)
	v_mfma_f32_16x16x32_f16 v[210:213], v[54:57], v[158:161], v[210:213]
	v_mfma_f32_16x16x32_f16 v[210:213], v[58:61], v[162:165], v[210:213]
	s_waitcnt lgkmcnt(0)
	v_mfma_f32_16x16x32_f16 v[210:213], v[62:65], v[166:169], v[210:213]
	v_mfma_f32_16x16x32_f16 v[210:213], v[50:53], v[170:173], v[210:213]
	s_waitcnt vmcnt(9)
	v_cvt_pk_f16_f32 v251, v194, v195
	ds_write_b32 v1, v251 offset:6144
	ds_read_b128 v[150:153], v186 offset:4096
	ds_read_b128 v[154:157], v186 offset:5120
	s_add_i32 s45, s45, 0x100000
	s_add_i32 s46, s46, 0x4000
	s_movk_i32 s47, 0x1000
	s_add_i32 s43, s40, -12
	s_lshl_b32 s43, s43, 12
	s_cmp_lt_u32 s40, 14
	s_cselect_b32 s43, s47, s43
	v_exp_f32_e32 v226, v210
	v_exp_f32_e32 v227, v211
	v_mfma_f32_16x16x32_f16 v[214:217], v[34:37], v[158:161], v[214:217]
	v_min_f32_e32 v228, s42, v212
	v_exp_f32_e32 v229, v213
	v_mfma_f32_16x16x32_f16 v[214:217], v[38:41], v[162:165], v[214:217]
	v_exp_f32_e32 v228, v228
	v_add_f32_e32 v227, 1.0, v227
	v_mfma_f32_16x16x32_f16 v[214:217], v[42:45], v[166:169], v[214:217]
	v_fma_f32 v230, v228, s41, s41
	v_rcp_f32_e32 v227, v227
	v_mfma_f32_16x16x32_f16 v[214:217], v[46:49], v[170:173], v[214:217]
	v_fma_f32 v230, v226, v230, v230
	v_rcp_f32_e32 v230, v230
	v_mfma_f32_16x16x32_f16 v[218:221], v[18:21], v[158:161], v[218:221]
	v_fma_f32 v226, -v228, v230, v230
	v_fma_f32 v200, v200, v227, v226
	v_mfma_f32_16x16x32_f16 v[218:221], v[14:17], v[162:165], v[218:221]
	v_exp_f32_e32 v226, v200
	s_nop 0
	v_add_f32_e32 v227, 1.0, v226
	v_mfma_f32_16x16x32_f16 v[218:221], v[10:13], v[166:169], v[218:221]
	v_fma_f32 v227, v229, v227, v227
	v_rcp_f32_e32 v227, v227
	v_mfma_f32_16x16x32_f16 v[218:221], v[26:29], v[170:173], v[218:221]
	v_fma_f32 v226, -v226, v227, v227
	v_exp_f32_e32 v231, v214
	v_mfma_f32_16x16x32_f16 v[222:225], v[2:5], v[158:161], v[222:225]
	v_exp_f32_e32 v232, v215
	v_min_f32_e32 v233, s42, v216
	v_mfma_f32_16x16x32_f16 v[222:225], v[6:9], v[162:165], v[222:225]
	v_exp_f32_e32 v234, v217
	v_exp_f32_e32 v233, v233
	v_mfma_f32_16x16x32_f16 v[222:225], v[22:25], v[166:169], v[222:225]
	v_exp_f32_e32 v236, v218
	v_add_f32_e32 v232, 1.0, v232
	v_mfma_f32_16x16x32_f16 v[222:225], v[30:33], v[170:173], v[222:225]
	v_fma_f32 v235, v233, s41, s41
	v_exp_f32_e32 v227, v219
	v_rcp_f32_e32 v232, v232
	v_fma_f32 v235, v231, v235, v235
	v_min_f32_e32 v228, s42, v220
	v_rcp_f32_e32 v235, v235
	s_nop 0
	v_fma_f32 v231, -v233, v235, v235
	v_exp_f32_e32 v229, v221
	v_fma_f32 v201, v201, v232, v231
	v_exp_f32_e32 v231, v201
	v_exp_f32_e32 v228, v228
	v_add_f32_e32 v232, 1.0, v231
	v_fma_f32 v232, v234, v232, v232
	v_add_f32_e32 v227, 1.0, v227
	v_rcp_f32_e32 v232, v232
	v_mfma_f32_16x16x32_f16 v[146:149], v[130:133], v[158:161], v[146:149]
	v_fma_f32 v231, -v231, v232, v232
	v_fma_f32 v230, v228, s41, s41
	v_cvt_pk_f16_f32 v246, v226, v231
	v_mfma_f32_16x16x32_f16 v[146:149], v[134:137], v[162:165], v[146:149]
	v_exp_f32_e32 v231, v222
	v_rcp_f32_e32 v227, v227
	v_exp_f32_e32 v232, v223
	buffer_load_dwordx4 v[130:133], v189, s[16:19], s46 offen
	buffer_load_dwordx4 v[134:137], v208, s[16:19], s46 offen
	v_min_f32_e32 v233, s42, v224
	v_fma_f32 v230, v236, v230, v230
	v_exp_f32_e32 v234, v225
	s_waitcnt lgkmcnt(0)
	v_mfma_f32_16x16x32_f16 v[210:213], v[70:73], v[150:153], v[98:101]
	v_exp_f32_e32 v233, v233
	v_rcp_f32_e32 v230, v230
	v_add_f32_e32 v232, 1.0, v232
	v_mfma_f32_16x16x32_f16 v[214:217], v[74:77], v[150:153], v[102:105]
	v_fma_f32 v235, v233, s41, s41
	v_fma_f32 v236, -v228, v230, v230
	v_rcp_f32_e32 v232, v232
	v_fma_f32 v235, v231, v235, v235
	v_fma_f32 v198, v198, v227, v236
	v_rcp_f32_e32 v235, v235
	s_nop 0
	v_fma_f32 v231, -v233, v235, v235
	v_exp_f32_e32 v236, v198
	v_fma_f32 v199, v199, v232, v231
	v_exp_f32_e32 v231, v199
	v_add_f32_e32 v227, 1.0, v236
	v_add_f32_e32 v232, 1.0, v231
	v_add_u32_e32 v250, s43, v206
	v_fma_f32 v232, v234, v232, v232
	v_fma_f32 v227, v229, v227, v227
	v_add_u32_e32 v248, s43, v252
	v_rcp_f32_e32 v232, v232
	s_nop 0
	v_fma_f32 v231, -v231, v232, v232
	v_add_u32_e32 v249, s43, v253
	v_rcp_f32_e32 v227, v227
	s_nop 0
	v_fma_f32 v236, -v236, v227, v227
	v_cvt_pk_f16_f32 v247, v236, v231
	ds_write_b64 v250, v[246:247] offset:8192
	v_mfma_f32_16x16x32_f16 v[210:213], v[66:69], v[154:157], v[210:213]
	v_mfma_f32_16x16x32_f16 v[214:217], v[78:81], v[154:157], v[214:217]
	v_mov_b32_e32 v205, v246
	v_mov_b32_e32 v207, v247
	buffer_load_dwordx2 v[194:195], v209, s[20:23], s45 offen
	s_add_i32 s40, s40, 1
	s_add_i32 s44, s44, 0x1000
	s_waitcnt lgkmcnt(0)
	s_barrier
	s_mov_b32 s45, 0xc00000
	s_mov_b32 s46, 0x30000
.Lmy_loopb:
	ds_read_b128 v[158:161], v248 offset:0
	ds_read_b128 v[162:165], v248 offset:1024
	ds_read_b128 v[166:169], v249 offset:2048
	ds_read_b128 v[170:173], v249 offset:3072
	v_mfma_f32_16x16x32_f16 v[218:221], v[82:85], v[150:153], v[106:109]
	v_mfma_f32_16x16x32_f16 v[222:225], v[90:93], v[150:153], v[110:113]
	v_mfma_f32_16x16x32_f16 v[218:221], v[86:89], v[154:157], v[218:221]
	v_mfma_f32_16x16x32_f16 v[222:225], v[94:97], v[154:157], v[222:225]
	s_waitcnt lgkmcnt(2)
	v_mfma_f32_16x16x32_f16 v[210:213], v[54:57], v[158:161], v[210:213]
	v_mfma_f32_16x16x32_f16 v[210:213], v[58:61], v[162:165], v[210:213]
	s_waitcnt lgkmcnt(0)
	v_mfma_f32_16x16x32_f16 v[210:213], v[62:65], v[166:169], v[210:213]
	v_mfma_f32_16x16x32_f16 v[210:213], v[50:53], v[170:173], v[210:213]
	s_waitcnt vmcnt(9)
	v_cvt_pk_f16_f32 v251, v192, v193
	ds_write_b32 v1, v251 offset:0
	ds_read_b128 v[150:153], v186 offset:6144
	ds_read_b128 v[154:157], v186 offset:7168
	v_add_u32_e32 v250, 0x1000, v250
	v_add_u32_e32 v248, 0x1000, v248
	v_add_u32_e32 v249, 0x1000, v249
	v_exp_f32_e32 v226, v210
	v_exp_f32_e32 v227, v211
	v_mfma_f32_16x16x32_f16 v[214:217], v[34:37], v[158:161], v[214:217]
	v_min_f32_e32 v228, s42, v212
	v_exp_f32_e32 v229, v213
	v_mfma_f32_16x16x32_f16 v[214:217], v[38:41], v[162:165], v[214:217]
	v_exp_f32_e32 v228, v228
	v_add_f32_e32 v227, 1.0, v227
	v_mfma_f32_16x16x32_f16 v[214:217], v[42:45], v[166:169], v[214:217]
	v_fma_f32 v230, v228, s41, s41
	v_rcp_f32_e32 v227, v227
	v_mfma_f32_16x16x32_f16 v[214:217], v[46:49], v[170:173], v[214:217]
	v_fma_f32 v230, v226, v230, v230
	v_rcp_f32_e32 v230, v230
	v_mfma_f32_16x16x32_f16 v[218:221], v[18:21], v[158:161], v[218:221]
	v_fma_f32 v226, -v228, v230, v230
	v_fma_f32 v200, v200, v227, v226
	v_mfma_f32_16x16x32_f16 v[218:221], v[14:17], v[162:165], v[218:221]
	v_exp_f32_e32 v226, v200
	s_nop 0
	v_add_f32_e32 v227, 1.0, v226
	v_mfma_f32_16x16x32_f16 v[218:221], v[10:13], v[166:169], v[218:221]
	v_fma_f32 v227, v229, v227, v227
	v_rcp_f32_e32 v227, v227
	v_mfma_f32_16x16x32_f16 v[218:221], v[26:29], v[170:173], v[218:221]
	v_fma_f32 v226, -v226, v227, v227
	v_exp_f32_e32 v231, v214
	v_mfma_f32_16x16x32_f16 v[222:225], v[2:5], v[158:161], v[222:225]
	v_exp_f32_e32 v232, v215
	v_min_f32_e32 v233, s42, v216
	v_mfma_f32_16x16x32_f16 v[222:225], v[6:9], v[162:165], v[222:225]
	v_exp_f32_e32 v234, v217
	v_exp_f32_e32 v233, v233
	v_mfma_f32_16x16x32_f16 v[222:225], v[22:25], v[166:169], v[222:225]
	v_exp_f32_e32 v236, v218
	v_add_f32_e32 v232, 1.0, v232
	v_mfma_f32_16x16x32_f16 v[222:225], v[30:33], v[170:173], v[222:225]
	v_fma_f32 v235, v233, s41, s41
	v_exp_f32_e32 v227, v219
	v_rcp_f32_e32 v232, v232
	v_fma_f32 v235, v231, v235, v235
	v_min_f32_e32 v228, s42, v220
	v_rcp_f32_e32 v235, v235
	s_nop 0
	v_fma_f32 v231, -v233, v235, v235
	v_exp_f32_e32 v229, v221
	v_fma_f32 v201, v201, v232, v231
	v_exp_f32_e32 v231, v201
	v_exp_f32_e32 v228, v228
	v_add_f32_e32 v232, 1.0, v231
	v_fma_f32 v232, v234, v232, v232
	v_add_f32_e32 v227, 1.0, v227
	v_rcp_f32_e32 v232, v232
	v_mfma_f32_16x16x32_f16 v[146:149], v[122:125], v[158:161], v[146:149]
	v_fma_f32 v231, -v231, v232, v232
	v_fma_f32 v230, v228, s41, s41
	v_cvt_pk_f16_f32 v246, v226, v231
	v_mfma_f32_16x16x32_f16 v[146:149], v[126:129], v[162:165], v[146:149]
	v_exp_f32_e32 v231, v222
	v_rcp_f32_e32 v227, v227
	v_exp_f32_e32 v232, v223
	buffer_load_dwordx4 v[122:125], v189, s[76:79], s46 offen
	buffer_load_dwordx4 v[126:129], v208, s[76:79], s46 offen
	v_min_f32_e32 v233, s42, v224
	v_fma_f32 v230, v236, v230, v230
	v_exp_f32_e32 v234, v225
	s_waitcnt lgkmcnt(0)
	v_mfma_f32_16x16x32_f16 v[210:213], v[70:73], v[150:153], v[98:101]
	v_exp_f32_e32 v233, v233
	v_rcp_f32_e32 v230, v230
	v_add_f32_e32 v232, 1.0, v232
	v_mfma_f32_16x16x32_f16 v[214:217], v[74:77], v[150:153], v[102:105]
	v_fma_f32 v235, v233, s41, s41
	v_fma_f32 v236, -v228, v230, v230
	v_rcp_f32_e32 v232, v232
	v_fma_f32 v235, v231, v235, v235
	v_fma_f32 v198, v198, v227, v236
	v_rcp_f32_e32 v235, v235
	s_nop 0
	v_fma_f32 v231, -v233, v235, v235
	v_exp_f32_e32 v236, v198
	v_fma_f32 v199, v199, v232, v231
	v_exp_f32_e32 v231, v199
	v_add_f32_e32 v227, 1.0, v236
	v_add_f32_e32 v232, 1.0, v231
	v_fma_f32 v232, v234, v232, v232
	v_fma_f32 v227, v229, v227, v227
	v_rcp_f32_e32 v232, v232
	s_nop 0
	v_fma_f32 v231, -v231, v232, v232
	v_rcp_f32_e32 v227, v227
	s_nop 0
	v_fma_f32 v236, -v236, v227, v227
	v_cvt_pk_f16_f32 v247, v236, v231
	ds_write_b64 v250, v[246:247] offset:8192
	v_mfma_f32_16x16x32_f16 v[210:213], v[66:69], v[154:157], v[210:213]
	v_mfma_f32_16x16x32_f16 v[214:217], v[78:81], v[154:157], v[214:217]
	buffer_load_dwordx2 v[192:193], v209, s[56:59], s45 offen
	s_waitcnt lgkmcnt(0)
	s_barrier
	ds_read_b128 v[158:161], v248 offset:0
	ds_read_b128 v[162:165], v248 offset:1024
	ds_read_b128 v[166:169], v249 offset:2048
	ds_read_b128 v[170:173], v249 offset:3072
	v_mfma_f32_16x16x32_f16 v[218:221], v[82:85], v[150:153], v[106:109]
	v_mfma_f32_16x16x32_f16 v[222:225], v[90:93], v[150:153], v[110:113]
	v_mfma_f32_16x16x32_f16 v[218:221], v[86:89], v[154:157], v[218:221]
	v_mfma_f32_16x16x32_f16 v[222:225], v[94:97], v[154:157], v[222:225]
	s_waitcnt lgkmcnt(2)
	v_mfma_f32_16x16x32_f16 v[210:213], v[54:57], v[158:161], v[210:213]
	v_mfma_f32_16x16x32_f16 v[210:213], v[58:61], v[162:165], v[210:213]
	s_waitcnt lgkmcnt(0)
	v_mfma_f32_16x16x32_f16 v[210:213], v[62:65], v[166:169], v[210:213]
	v_mfma_f32_16x16x32_f16 v[210:213], v[50:53], v[170:173], v[210:213]
	s_waitcnt vmcnt(9)
	v_cvt_pk_f16_f32 v251, v190, v191
	ds_write_b32 v1, v251 offset:2048
	ds_read_b128 v[150:153], v186 offset:0
	ds_read_b128 v[154:157], v186 offset:1024
	v_add_u32_e32 v250, 0x1000, v250
	v_add_u32_e32 v248, 0x1000, v248
	v_add_u32_e32 v249, 0x1000, v249
	v_exp_f32_e32 v226, v210
	v_exp_f32_e32 v227, v211
	v_mfma_f32_16x16x32_f16 v[214:217], v[34:37], v[158:161], v[214:217]
	v_min_f32_e32 v228, s42, v212
	v_exp_f32_e32 v229, v213
	v_mfma_f32_16x16x32_f16 v[214:217], v[38:41], v[162:165], v[214:217]
	v_exp_f32_e32 v228, v228
	v_add_f32_e32 v227, 1.0, v227
	v_mfma_f32_16x16x32_f16 v[214:217], v[42:45], v[166:169], v[214:217]
	v_fma_f32 v230, v228, s41, s41
	v_rcp_f32_e32 v227, v227
	v_mfma_f32_16x16x32_f16 v[214:217], v[46:49], v[170:173], v[214:217]
	v_fma_f32 v230, v226, v230, v230
	v_rcp_f32_e32 v230, v230
	v_mfma_f32_16x16x32_f16 v[218:221], v[18:21], v[158:161], v[218:221]
	v_fma_f32 v226, -v228, v230, v230
	v_fma_f32 v200, v200, v227, v226
	v_mfma_f32_16x16x32_f16 v[218:221], v[14:17], v[162:165], v[218:221]
	v_exp_f32_e32 v226, v200
	s_nop 0
	v_add_f32_e32 v227, 1.0, v226
	v_mfma_f32_16x16x32_f16 v[218:221], v[10:13], v[166:169], v[218:221]
	v_fma_f32 v227, v229, v227, v227
	v_rcp_f32_e32 v227, v227
	v_mfma_f32_16x16x32_f16 v[218:221], v[26:29], v[170:173], v[218:221]
	v_fma_f32 v226, -v226, v227, v227
	v_exp_f32_e32 v231, v214
	v_mfma_f32_16x16x32_f16 v[222:225], v[2:5], v[158:161], v[222:225]
	v_exp_f32_e32 v232, v215
	v_min_f32_e32 v233, s42, v216
	v_mfma_f32_16x16x32_f16 v[222:225], v[6:9], v[162:165], v[222:225]
	v_exp_f32_e32 v234, v217
	v_exp_f32_e32 v233, v233
	v_mfma_f32_16x16x32_f16 v[222:225], v[22:25], v[166:169], v[222:225]
	v_exp_f32_e32 v236, v218
	v_add_f32_e32 v232, 1.0, v232
	v_mfma_f32_16x16x32_f16 v[222:225], v[30:33], v[170:173], v[222:225]
	v_fma_f32 v235, v233, s41, s41
	v_exp_f32_e32 v227, v219
	v_rcp_f32_e32 v232, v232
	v_fma_f32 v235, v231, v235, v235
	v_min_f32_e32 v228, s42, v220
	v_rcp_f32_e32 v235, v235
	s_nop 0
	v_fma_f32 v231, -v233, v235, v235
	v_exp_f32_e32 v229, v221
	v_fma_f32 v201, v201, v232, v231
	v_exp_f32_e32 v231, v201
	v_exp_f32_e32 v228, v228
	v_add_f32_e32 v232, 1.0, v231
	v_fma_f32 v232, v234, v232, v232
	v_add_f32_e32 v227, 1.0, v227
	v_rcp_f32_e32 v232, v232
	v_mfma_f32_16x16x32_f16 v[146:149], v[114:117], v[158:161], v[146:149]
	v_fma_f32 v231, -v231, v232, v232
	v_fma_f32 v230, v228, s41, s41
	v_cvt_pk_f16_f32 v246, v226, v231
	v_mfma_f32_16x16x32_f16 v[146:149], v[118:121], v[162:165], v[146:149]
	v_exp_f32_e32 v231, v222
	v_rcp_f32_e32 v227, v227
	v_exp_f32_e32 v232, v223
	buffer_load_dwordx4 v[114:117], v189, s[80:83], s46 offen
	buffer_load_dwordx4 v[118:121], v208, s[80:83], s46 offen
	v_min_f32_e32 v233, s42, v224
	v_fma_f32 v230, v236, v230, v230
	v_exp_f32_e32 v234, v225
	s_waitcnt lgkmcnt(0)
	v_mfma_f32_16x16x32_f16 v[210:213], v[70:73], v[150:153], v[98:101]
	v_exp_f32_e32 v233, v233
	v_rcp_f32_e32 v230, v230
	v_add_f32_e32 v232, 1.0, v232
	v_mfma_f32_16x16x32_f16 v[214:217], v[74:77], v[150:153], v[102:105]
	v_fma_f32 v235, v233, s41, s41
	v_fma_f32 v236, -v228, v230, v230
	v_rcp_f32_e32 v232, v232
	v_fma_f32 v235, v231, v235, v235
	v_fma_f32 v198, v198, v227, v236
	v_rcp_f32_e32 v235, v235
	s_nop 0
	v_fma_f32 v231, -v233, v235, v235
	v_exp_f32_e32 v236, v198
	v_fma_f32 v199, v199, v232, v231
	v_exp_f32_e32 v231, v199
	v_add_f32_e32 v227, 1.0, v236
	v_add_f32_e32 v232, 1.0, v231
	v_fma_f32 v232, v234, v232, v232
	v_fma_f32 v227, v229, v227, v227
	v_rcp_f32_e32 v232, v232
	s_nop 0
	v_fma_f32 v231, -v231, v232, v232
	v_rcp_f32_e32 v227, v227
	s_nop 0
	v_fma_f32 v236, -v236, v227, v227
	v_cvt_pk_f16_f32 v247, v236, v231
	ds_write_b64 v250, v[246:247] offset:8192
	v_mfma_f32_16x16x32_f16 v[210:213], v[66:69], v[154:157], v[210:213]
	v_mfma_f32_16x16x32_f16 v[214:217], v[78:81], v[154:157], v[214:217]
	buffer_load_dwordx2 v[190:191], v209, s[60:63], s45 offen
	s_add_i32 s45, s45, 0x400000
	s_add_i32 s46, s46, 0x10000
	s_waitcnt lgkmcnt(0)
	s_barrier
	ds_read_b128 v[158:161], v248 offset:0
	ds_read_b128 v[162:165], v248 offset:1024
	ds_read_b128 v[166:169], v249 offset:2048
	ds_read_b128 v[170:173], v249 offset:3072
	v_mfma_f32_16x16x32_f16 v[218:221], v[82:85], v[150:153], v[106:109]
	v_mfma_f32_16x16x32_f16 v[222:225], v[90:93], v[150:153], v[110:113]
	v_mfma_f32_16x16x32_f16 v[218:221], v[86:89], v[154:157], v[218:221]
	v_mfma_f32_16x16x32_f16 v[222:225], v[94:97], v[154:157], v[222:225]
	s_waitcnt lgkmcnt(2)
	v_mfma_f32_16x16x32_f16 v[210:213], v[54:57], v[158:161], v[210:213]
	v_mfma_f32_16x16x32_f16 v[210:213], v[58:61], v[162:165], v[210:213]
	s_waitcnt lgkmcnt(0)
	v_mfma_f32_16x16x32_f16 v[210:213], v[62:65], v[166:169], v[210:213]
	v_mfma_f32_16x16x32_f16 v[210:213], v[50:53], v[170:173], v[210:213]
	s_waitcnt vmcnt(9)
	v_cvt_pk_f16_f32 v251, v196, v197
	ds_write_b32 v1, v251 offset:4096
	ds_read_b128 v[150:153], v186 offset:2048
	ds_read_b128 v[154:157], v186 offset:3072
	v_add_u32_e32 v250, 0x1000, v250
	v_add_u32_e32 v248, 0x1000, v248
	v_add_u32_e32 v249, 0x1000, v249
	v_exp_f32_e32 v226, v210
	v_exp_f32_e32 v227, v211
	v_mfma_f32_16x16x32_f16 v[214:217], v[34:37], v[158:161], v[214:217]
	v_min_f32_e32 v228, s42, v212
	v_exp_f32_e32 v229, v213
	v_mfma_f32_16x16x32_f16 v[214:217], v[38:41], v[162:165], v[214:217]
	v_exp_f32_e32 v228, v228
	v_add_f32_e32 v227, 1.0, v227
	v_mfma_f32_16x16x32_f16 v[214:217], v[42:45], v[166:169], v[214:217]
	v_fma_f32 v230, v228, s41, s41
	v_rcp_f32_e32 v227, v227
	v_mfma_f32_16x16x32_f16 v[214:217], v[46:49], v[170:173], v[214:217]
	v_fma_f32 v230, v226, v230, v230
	v_rcp_f32_e32 v230, v230
	v_mfma_f32_16x16x32_f16 v[218:221], v[18:21], v[158:161], v[218:221]
	v_fma_f32 v226, -v228, v230, v230
	v_fma_f32 v200, v200, v227, v226
	v_mfma_f32_16x16x32_f16 v[218:221], v[14:17], v[162:165], v[218:221]
	v_exp_f32_e32 v226, v200
	s_nop 0
	v_add_f32_e32 v227, 1.0, v226
	v_mfma_f32_16x16x32_f16 v[218:221], v[10:13], v[166:169], v[218:221]
	v_fma_f32 v227, v229, v227, v227
	v_rcp_f32_e32 v227, v227
	v_mfma_f32_16x16x32_f16 v[218:221], v[26:29], v[170:173], v[218:221]
	v_fma_f32 v226, -v226, v227, v227
	v_exp_f32_e32 v231, v214
	v_mfma_f32_16x16x32_f16 v[222:225], v[2:5], v[158:161], v[222:225]
	v_exp_f32_e32 v232, v215
	v_min_f32_e32 v233, s42, v216
	v_mfma_f32_16x16x32_f16 v[222:225], v[6:9], v[162:165], v[222:225]
	v_exp_f32_e32 v234, v217
	v_exp_f32_e32 v233, v233
	v_mfma_f32_16x16x32_f16 v[222:225], v[22:25], v[166:169], v[222:225]
	v_exp_f32_e32 v236, v218
	v_add_f32_e32 v232, 1.0, v232
	v_mfma_f32_16x16x32_f16 v[222:225], v[30:33], v[170:173], v[222:225]
	v_fma_f32 v235, v233, s41, s41
	v_exp_f32_e32 v227, v219
	v_rcp_f32_e32 v232, v232
	v_fma_f32 v235, v231, v235, v235
	v_min_f32_e32 v228, s42, v220
	v_rcp_f32_e32 v235, v235
	s_nop 0
	v_fma_f32 v231, -v233, v235, v235
	v_exp_f32_e32 v229, v221
	v_fma_f32 v201, v201, v232, v231
	v_exp_f32_e32 v231, v201
	v_exp_f32_e32 v228, v228
	v_add_f32_e32 v232, 1.0, v231
	v_fma_f32 v232, v234, v232, v232
	v_add_f32_e32 v227, 1.0, v227
	v_rcp_f32_e32 v232, v232
	v_mfma_f32_16x16x32_f16 v[146:149], v[138:141], v[158:161], v[146:149]
	v_fma_f32 v231, -v231, v232, v232
	v_fma_f32 v230, v228, s41, s41
	v_cvt_pk_f16_f32 v246, v226, v231
	v_mfma_f32_16x16x32_f16 v[146:149], v[142:145], v[162:165], v[146:149]
	v_exp_f32_e32 v231, v222
	v_rcp_f32_e32 v227, v227
	v_exp_f32_e32 v232, v223
	buffer_load_dwordx4 v[138:141], v189, s[68:71], s46 offen
	buffer_load_dwordx4 v[142:145], v208, s[68:71], s46 offen
	v_min_f32_e32 v233, s42, v224
	v_fma_f32 v230, v236, v230, v230
	v_exp_f32_e32 v234, v225
	s_waitcnt lgkmcnt(0)
	v_mfma_f32_16x16x32_f16 v[210:213], v[70:73], v[150:153], v[98:101]
	v_exp_f32_e32 v233, v233
	v_rcp_f32_e32 v230, v230
	v_add_f32_e32 v232, 1.0, v232
	v_mfma_f32_16x16x32_f16 v[214:217], v[74:77], v[150:153], v[102:105]
	v_fma_f32 v235, v233, s41, s41
	v_fma_f32 v236, -v228, v230, v230
	v_rcp_f32_e32 v232, v232
	v_fma_f32 v235, v231, v235, v235
	v_fma_f32 v198, v198, v227, v236
	v_rcp_f32_e32 v235, v235
	s_nop 0
	v_fma_f32 v231, -v233, v235, v235
	v_exp_f32_e32 v236, v198
	v_fma_f32 v199, v199, v232, v231
	v_exp_f32_e32 v231, v199
	v_add_f32_e32 v227, 1.0, v236
	v_add_f32_e32 v232, 1.0, v231
	v_fma_f32 v232, v234, v232, v232
	v_fma_f32 v227, v229, v227, v227
	v_rcp_f32_e32 v232, v232
	s_nop 0
	v_fma_f32 v231, -v231, v232, v232
	v_rcp_f32_e32 v227, v227
	s_nop 0
	v_fma_f32 v236, -v236, v227, v227
	v_cvt_pk_f16_f32 v247, v236, v231
	ds_write_b64 v250, v[246:247] offset:8192
	v_mfma_f32_16x16x32_f16 v[210:213], v[66:69], v[154:157], v[210:213]
	v_mfma_f32_16x16x32_f16 v[214:217], v[78:81], v[154:157], v[214:217]
	buffer_load_dwordx2 v[196:197], v209, s[48:51], s45 offen
	s_waitcnt lgkmcnt(0)
	s_barrier
	ds_read_b128 v[158:161], v248 offset:0
	ds_read_b128 v[162:165], v248 offset:1024
	ds_read_b128 v[166:169], v249 offset:2048
	ds_read_b128 v[170:173], v249 offset:3072
	v_mfma_f32_16x16x32_f16 v[218:221], v[82:85], v[150:153], v[106:109]
	v_mfma_f32_16x16x32_f16 v[222:225], v[90:93], v[150:153], v[110:113]
	v_mfma_f32_16x16x32_f16 v[218:221], v[86:89], v[154:157], v[218:221]
	v_mfma_f32_16x16x32_f16 v[222:225], v[94:97], v[154:157], v[222:225]
	s_waitcnt lgkmcnt(2)
	v_mfma_f32_16x16x32_f16 v[210:213], v[54:57], v[158:161], v[210:213]
	v_mfma_f32_16x16x32_f16 v[210:213], v[58:61], v[162:165], v[210:213]
	s_waitcnt lgkmcnt(0)
	v_mfma_f32_16x16x32_f16 v[210:213], v[62:65], v[166:169], v[210:213]
	v_mfma_f32_16x16x32_f16 v[210:213], v[50:53], v[170:173], v[210:213]
	s_waitcnt vmcnt(9)
	v_cvt_pk_f16_f32 v251, v194, v195
	ds_write_b32 v1, v251 offset:6144
	ds_read_b128 v[150:153], v186 offset:4096
	ds_read_b128 v[154:157], v186 offset:5120
	v_add_u32_e32 v250, 0x1000, v250
	v_add_u32_e32 v248, 0x1000, v248
	v_add_u32_e32 v249, 0x1000, v249
	v_exp_f32_e32 v226, v210
	v_exp_f32_e32 v227, v211
	v_mfma_f32_16x16x32_f16 v[214:217], v[34:37], v[158:161], v[214:217]
	v_min_f32_e32 v228, s42, v212
	v_exp_f32_e32 v229, v213
	v_mfma_f32_16x16x32_f16 v[214:217], v[38:41], v[162:165], v[214:217]
	v_exp_f32_e32 v228, v228
	v_add_f32_e32 v227, 1.0, v227
	v_mfma_f32_16x16x32_f16 v[214:217], v[42:45], v[166:169], v[214:217]
	v_fma_f32 v230, v228, s41, s41
	v_rcp_f32_e32 v227, v227
	v_mfma_f32_16x16x32_f16 v[214:217], v[46:49], v[170:173], v[214:217]
	v_fma_f32 v230, v226, v230, v230
	v_rcp_f32_e32 v230, v230
	v_mfma_f32_16x16x32_f16 v[218:221], v[18:21], v[158:161], v[218:221]
	v_fma_f32 v226, -v228, v230, v230
	v_fma_f32 v200, v200, v227, v226
	v_mfma_f32_16x16x32_f16 v[218:221], v[14:17], v[162:165], v[218:221]
	v_exp_f32_e32 v226, v200
	s_nop 0
	v_add_f32_e32 v227, 1.0, v226
	v_mfma_f32_16x16x32_f16 v[218:221], v[10:13], v[166:169], v[218:221]
	v_fma_f32 v227, v229, v227, v227
	v_rcp_f32_e32 v227, v227
	v_mfma_f32_16x16x32_f16 v[218:221], v[26:29], v[170:173], v[218:221]
	v_fma_f32 v226, -v226, v227, v227
	v_exp_f32_e32 v231, v214
	v_mfma_f32_16x16x32_f16 v[222:225], v[2:5], v[158:161], v[222:225]
	v_exp_f32_e32 v232, v215
	v_min_f32_e32 v233, s42, v216
	v_mfma_f32_16x16x32_f16 v[222:225], v[6:9], v[162:165], v[222:225]
	v_exp_f32_e32 v234, v217
	v_exp_f32_e32 v233, v233
	v_mfma_f32_16x16x32_f16 v[222:225], v[22:25], v[166:169], v[222:225]
	v_exp_f32_e32 v236, v218
	v_add_f32_e32 v232, 1.0, v232
	v_mfma_f32_16x16x32_f16 v[222:225], v[30:33], v[170:173], v[222:225]
	v_fma_f32 v235, v233, s41, s41
	v_exp_f32_e32 v227, v219
	v_rcp_f32_e32 v232, v232
	v_fma_f32 v235, v231, v235, v235
	v_min_f32_e32 v228, s42, v220
	v_rcp_f32_e32 v235, v235
	s_nop 0
	v_fma_f32 v231, -v233, v235, v235
	v_exp_f32_e32 v229, v221
	v_fma_f32 v201, v201, v232, v231
	v_exp_f32_e32 v231, v201
	v_exp_f32_e32 v228, v228
	v_add_f32_e32 v232, 1.0, v231
	v_fma_f32 v232, v234, v232, v232
	v_add_f32_e32 v227, 1.0, v227
	v_rcp_f32_e32 v232, v232
	v_mfma_f32_16x16x32_f16 v[146:149], v[130:133], v[158:161], v[146:149]
	v_fma_f32 v231, -v231, v232, v232
	v_fma_f32 v230, v228, s41, s41
	v_cvt_pk_f16_f32 v246, v226, v231
	v_mfma_f32_16x16x32_f16 v[146:149], v[134:137], v[162:165], v[146:149]
	v_exp_f32_e32 v231, v222
	v_rcp_f32_e32 v227, v227
	v_exp_f32_e32 v232, v223
	buffer_load_dwordx4 v[130:133], v189, s[72:75], s46 offen
	buffer_load_dwordx4 v[134:137], v208, s[72:75], s46 offen
	v_min_f32_e32 v233, s42, v224
	v_fma_f32 v230, v236, v230, v230
	v_exp_f32_e32 v234, v225
	s_waitcnt lgkmcnt(0)
	v_mfma_f32_16x16x32_f16 v[210:213], v[70:73], v[150:153], v[98:101]
	v_exp_f32_e32 v233, v233
	v_rcp_f32_e32 v230, v230
	v_add_f32_e32 v232, 1.0, v232
	v_mfma_f32_16x16x32_f16 v[214:217], v[74:77], v[150:153], v[102:105]
	v_fma_f32 v235, v233, s41, s41
	v_fma_f32 v236, -v228, v230, v230
	v_rcp_f32_e32 v232, v232
	v_fma_f32 v235, v231, v235, v235
	v_fma_f32 v198, v198, v227, v236
	v_rcp_f32_e32 v235, v235
	s_nop 0
	v_fma_f32 v231, -v233, v235, v235
	v_exp_f32_e32 v236, v198
	v_fma_f32 v199, v199, v232, v231
	v_exp_f32_e32 v231, v199
	v_add_f32_e32 v227, 1.0, v236
	v_add_f32_e32 v232, 1.0, v231
	v_fma_f32 v232, v234, v232, v232
	v_fma_f32 v227, v229, v227, v227
	v_rcp_f32_e32 v232, v232
	s_nop 0
	v_fma_f32 v231, -v231, v232, v232
	v_rcp_f32_e32 v227, v227
	s_nop 0
	v_fma_f32 v236, -v236, v227, v227
	v_cvt_pk_f16_f32 v247, v236, v231
	ds_write_b64 v250, v[246:247] offset:8192
	v_mfma_f32_16x16x32_f16 v[210:213], v[66:69], v[154:157], v[210:213]
	v_mfma_f32_16x16x32_f16 v[214:217], v[78:81], v[154:157], v[214:217]
	buffer_load_dwordx2 v[194:195], v209, s[52:55], s45 offen
	s_waitcnt lgkmcnt(0)
	s_barrier
	s_cmp_lt_u32 s46, 0xa0000
	s_cbranch_scc1 .Lmy_loopb
	ds_read_b128 v[158:161], v248 offset:0
	ds_read_b128 v[162:165], v248 offset:1024
	ds_read_b128 v[166:169], v249 offset:2048
	ds_read_b128 v[170:173], v249 offset:3072
	v_mfma_f32_16x16x32_f16 v[218:221], v[82:85], v[150:153], v[106:109]
	v_mfma_f32_16x16x32_f16 v[222:225], v[90:93], v[150:153], v[110:113]
	v_mfma_f32_16x16x32_f16 v[218:221], v[86:89], v[154:157], v[218:221]
	v_mfma_f32_16x16x32_f16 v[222:225], v[94:97], v[154:157], v[222:225]
	s_waitcnt lgkmcnt(2)
	v_mfma_f32_16x16x32_f16 v[210:213], v[54:57], v[158:161], v[210:213]
	v_mfma_f32_16x16x32_f16 v[210:213], v[58:61], v[162:165], v[210:213]
	s_waitcnt lgkmcnt(0)
	v_mfma_f32_16x16x32_f16 v[210:213], v[62:65], v[166:169], v[210:213]
	v_mfma_f32_16x16x32_f16 v[210:213], v[50:53], v[170:173], v[210:213]
	s_waitcnt vmcnt(9)
	v_cvt_pk_f16_f32 v251, v192, v193
	ds_write_b32 v1, v251 offset:0
	ds_read_b128 v[150:153], v186 offset:6144
	ds_read_b128 v[154:157], v186 offset:7168
	v_add_u32_e32 v250, 0x1000, v250
	v_add_u32_e32 v248, 0x1000, v248
	v_add_u32_e32 v249, 0x1000, v249
	v_exp_f32_e32 v226, v210
	v_exp_f32_e32 v227, v211
	v_mfma_f32_16x16x32_f16 v[214:217], v[34:37], v[158:161], v[214:217]
	v_min_f32_e32 v228, s42, v212
	v_exp_f32_e32 v229, v213
	v_mfma_f32_16x16x32_f16 v[214:217], v[38:41], v[162:165], v[214:217]
	v_exp_f32_e32 v228, v228
	v_add_f32_e32 v227, 1.0, v227
	v_mfma_f32_16x16x32_f16 v[214:217], v[42:45], v[166:169], v[214:217]
	v_fma_f32 v230, v228, s41, s41
	v_rcp_f32_e32 v227, v227
	v_mfma_f32_16x16x32_f16 v[214:217], v[46:49], v[170:173], v[214:217]
	v_fma_f32 v230, v226, v230, v230
	v_rcp_f32_e32 v230, v230
	v_mfma_f32_16x16x32_f16 v[218:221], v[18:21], v[158:161], v[218:221]
	v_fma_f32 v226, -v228, v230, v230
	v_fma_f32 v200, v200, v227, v226
	v_mfma_f32_16x16x32_f16 v[218:221], v[14:17], v[162:165], v[218:221]
	v_min_f32_e32 v226, s42, v200
	v_exp_f32_e32 v226, v226
	v_mfma_f32_16x16x32_f16 v[218:221], v[10:13], v[166:169], v[218:221]
	v_add_f32_e32 v227, 1.0, v226
	v_fma_f32 v227, v229, v227, v227
	v_mfma_f32_16x16x32_f16 v[218:221], v[26:29], v[170:173], v[218:221]
	v_rcp_f32_e32 v227, v227
	v_exp_f32_e32 v231, v214
	v_mfma_f32_16x16x32_f16 v[222:225], v[2:5], v[158:161], v[222:225]
	v_exp_f32_e32 v232, v215
	v_fma_f32 v226, -v226, v227, v227
	v_mfma_f32_16x16x32_f16 v[222:225], v[6:9], v[162:165], v[222:225]
	v_min_f32_e32 v233, s42, v216
	v_exp_f32_e32 v234, v217
	v_mfma_f32_16x16x32_f16 v[222:225], v[22:25], v[166:169], v[222:225]
	v_exp_f32_e32 v236, v218
	v_exp_f32_e32 v233, v233
	v_mfma_f32_16x16x32_f16 v[222:225], v[30:33], v[170:173], v[222:225]
	v_add_f32_e32 v232, 1.0, v232
	v_exp_f32_e32 v227, v219
	v_fma_f32 v235, v233, s41, s41
	v_rcp_f32_e32 v232, v232
	v_min_f32_e32 v228, s42, v220
	v_fma_f32 v235, v231, v235, v235
	v_rcp_f32_e32 v235, v235
	v_exp_f32_e32 v229, v221
	v_fma_f32 v231, -v233, v235, v235
	v_fma_f32 v201, v201, v232, v231
	v_exp_f32_e32 v228, v228
	v_min_f32_e32 v231, s42, v201
	v_exp_f32_e32 v231, v231
	v_add_f32_e32 v227, 1.0, v227
	v_add_f32_e32 v232, 1.0, v231
	v_mfma_f32_16x16x32_f16 v[146:149], v[122:125], v[158:161], v[146:149]
	v_fma_f32 v232, v234, v232, v232
	v_fma_f32 v230, v228, s41, s41
	v_rcp_f32_e32 v232, v232
	v_mfma_f32_16x16x32_f16 v[146:149], v[126:129], v[162:165], v[146:149]
	v_fma_f32 v231, -v231, v232, v232
	v_rcp_f32_e32 v227, v227
	v_cvt_pk_f16_f32 v246, v226, v231
	buffer_load_dwordx4 v[122:125], v189, s[76:79], s46 offen
	buffer_load_dwordx4 v[126:129], v208, s[76:79], s46 offen
	v_exp_f32_e32 v231, v222
	v_fma_f32 v230, v236, v230, v230
	v_exp_f32_e32 v232, v223
	s_waitcnt lgkmcnt(0)
	v_mfma_f32_16x16x32_f16 v[210:213], v[70:73], v[150:153], v[98:101]
	v_min_f32_e32 v233, s42, v224
	v_rcp_f32_e32 v230, v230
	v_exp_f32_e32 v234, v225
	v_mfma_f32_16x16x32_f16 v[214:217], v[74:77], v[150:153], v[102:105]
	v_exp_f32_e32 v233, v233
	v_fma_f32 v236, -v228, v230, v230
	v_add_f32_e32 v232, 1.0, v232
	v_fma_f32 v235, v233, s41, s41
	v_fma_f32 v198, v198, v227, v236
	v_rcp_f32_e32 v232, v232
	v_fma_f32 v235, v231, v235, v235
	v_min_f32_e32 v236, s42, v198
	v_rcp_f32_e32 v235, v235
	s_nop 0
	v_fma_f32 v231, -v233, v235, v235
	v_exp_f32_e32 v236, v236
	v_fma_f32 v199, v199, v232, v231
	v_min_f32_e32 v231, s42, v199
	v_add_f32_e32 v227, 1.0, v236
	v_exp_f32_e32 v231, v231
	v_fma_f32 v227, v229, v227, v227
	v_add_f32_e32 v232, 1.0, v231
	v_rcp_f32_e32 v227, v227
	v_fma_f32 v232, v234, v232, v232
	v_fma_f32 v236, -v236, v227, v227
	v_rcp_f32_e32 v232, v232
	s_nop 0
	v_fma_f32 v231, -v231, v232, v232
	v_cvt_pk_f16_f32 v247, v236, v231
	ds_write_b64 v250, v[246:247] offset:8192
	v_mfma_f32_16x16x32_f16 v[210:213], v[66:69], v[154:157], v[210:213]
	v_mfma_f32_16x16x32_f16 v[214:217], v[78:81], v[154:157], v[214:217]
	buffer_load_dwordx2 v[192:193], v209, s[56:59], s45 offen
	s_waitcnt lgkmcnt(0)
	s_barrier
	ds_read_b128 v[158:161], v248 offset:0
	ds_read_b128 v[162:165], v248 offset:1024
	ds_read_b128 v[166:169], v249 offset:2048
	ds_read_b128 v[170:173], v249 offset:3072
	v_mfma_f32_16x16x32_f16 v[218:221], v[82:85], v[150:153], v[106:109]
	v_mfma_f32_16x16x32_f16 v[222:225], v[90:93], v[150:153], v[110:113]
	v_mfma_f32_16x16x32_f16 v[218:221], v[86:89], v[154:157], v[218:221]
	v_mfma_f32_16x16x32_f16 v[222:225], v[94:97], v[154:157], v[222:225]
	s_waitcnt lgkmcnt(2)
	v_mfma_f32_16x16x32_f16 v[210:213], v[54:57], v[158:161], v[210:213]
	v_mfma_f32_16x16x32_f16 v[210:213], v[58:61], v[162:165], v[210:213]
	s_waitcnt lgkmcnt(0)
	v_mfma_f32_16x16x32_f16 v[210:213], v[62:65], v[166:169], v[210:213]
	v_mfma_f32_16x16x32_f16 v[210:213], v[50:53], v[170:173], v[210:213]
	s_waitcnt vmcnt(9)
	v_cvt_pk_f16_f32 v251, v190, v191
	ds_write_b32 v1, v251 offset:2048
	ds_read_b128 v[150:153], v186 offset:0
	ds_read_b128 v[154:157], v186 offset:1024
	v_add_u32_e32 v250, 0x1000, v250
	v_add_u32_e32 v248, 0x1000, v248
	v_add_u32_e32 v249, 0x1000, v249
	v_exp_f32_e32 v226, v210
	v_exp_f32_e32 v227, v211
	v_mfma_f32_16x16x32_f16 v[214:217], v[34:37], v[158:161], v[214:217]
	v_min_f32_e32 v228, s42, v212
	v_exp_f32_e32 v229, v213
	v_mfma_f32_16x16x32_f16 v[214:217], v[38:41], v[162:165], v[214:217]
	v_exp_f32_e32 v228, v228
	v_add_f32_e32 v227, 1.0, v227
	v_mfma_f32_16x16x32_f16 v[214:217], v[42:45], v[166:169], v[214:217]
	v_fma_f32 v230, v228, s41, s41
	v_rcp_f32_e32 v227, v227
	v_mfma_f32_16x16x32_f16 v[214:217], v[46:49], v[170:173], v[214:217]
	v_fma_f32 v230, v226, v230, v230
	v_rcp_f32_e32 v230, v230
	v_mfma_f32_16x16x32_f16 v[218:221], v[18:21], v[158:161], v[218:221]
	v_fma_f32 v226, -v228, v230, v230
	v_fma_f32 v200, v200, v227, v226
	v_mfma_f32_16x16x32_f16 v[218:221], v[14:17], v[162:165], v[218:221]
	v_min_f32_e32 v226, s42, v200
	v_exp_f32_e32 v226, v226
	v_mfma_f32_16x16x32_f16 v[218:221], v[10:13], v[166:169], v[218:221]
	v_add_f32_e32 v227, 1.0, v226
	v_fma_f32 v227, v229, v227, v227
	v_mfma_f32_16x16x32_f16 v[218:221], v[26:29], v[170:173], v[218:221]
	v_rcp_f32_e32 v227, v227
	v_exp_f32_e32 v231, v214
	v_mfma_f32_16x16x32_f16 v[222:225], v[2:5], v[158:161], v[222:225]
	v_exp_f32_e32 v232, v215
	v_fma_f32 v226, -v226, v227, v227
	v_mfma_f32_16x16x32_f16 v[222:225], v[6:9], v[162:165], v[222:225]
	v_min_f32_e32 v233, s42, v216
	v_exp_f32_e32 v234, v217
	v_mfma_f32_16x16x32_f16 v[222:225], v[22:25], v[166:169], v[222:225]
	v_exp_f32_e32 v236, v218
	v_exp_f32_e32 v233, v233
	v_mfma_f32_16x16x32_f16 v[222:225], v[30:33], v[170:173], v[222:225]
	v_add_f32_e32 v232, 1.0, v232
	v_exp_f32_e32 v227, v219
	v_fma_f32 v235, v233, s41, s41
	v_rcp_f32_e32 v232, v232
	v_min_f32_e32 v228, s42, v220
	v_fma_f32 v235, v231, v235, v235
	v_rcp_f32_e32 v235, v235
	v_exp_f32_e32 v229, v221
	v_fma_f32 v231, -v233, v235, v235
	v_fma_f32 v201, v201, v232, v231
	v_exp_f32_e32 v228, v228
	v_min_f32_e32 v231, s42, v201
	v_exp_f32_e32 v231, v231
	v_add_f32_e32 v227, 1.0, v227
	v_add_f32_e32 v232, 1.0, v231
	v_mfma_f32_16x16x32_f16 v[146:149], v[114:117], v[158:161], v[146:149]
	v_fma_f32 v232, v234, v232, v232
	v_fma_f32 v230, v228, s41, s41
	v_rcp_f32_e32 v232, v232
	v_mfma_f32_16x16x32_f16 v[146:149], v[118:121], v[162:165], v[146:149]
	v_fma_f32 v231, -v231, v232, v232
	v_rcp_f32_e32 v227, v227
	v_cvt_pk_f16_f32 v246, v226, v231
	buffer_load_dwordx4 v[114:117], v189, s[80:83], s46 offen
	buffer_load_dwordx4 v[118:121], v208, s[80:83], s46 offen
	v_exp_f32_e32 v231, v222
	v_fma_f32 v230, v236, v230, v230
	v_exp_f32_e32 v232, v223
	s_waitcnt lgkmcnt(0)
	v_mfma_f32_16x16x32_f16 v[210:213], v[70:73], v[150:153], v[98:101]
	v_min_f32_e32 v233, s42, v224
	v_rcp_f32_e32 v230, v230
	v_exp_f32_e32 v234, v225
	v_mfma_f32_16x16x32_f16 v[214:217], v[74:77], v[150:153], v[102:105]
	v_exp_f32_e32 v233, v233
	v_fma_f32 v236, -v228, v230, v230
	v_add_f32_e32 v232, 1.0, v232
	v_fma_f32 v235, v233, s41, s41
	v_fma_f32 v198, v198, v227, v236
	v_rcp_f32_e32 v232, v232
	v_fma_f32 v235, v231, v235, v235
	v_min_f32_e32 v236, s42, v198
	v_rcp_f32_e32 v235, v235
	s_nop 0
	v_fma_f32 v231, -v233, v235, v235
	v_exp_f32_e32 v236, v236
	v_fma_f32 v199, v199, v232, v231
	v_min_f32_e32 v231, s42, v199
	v_add_f32_e32 v227, 1.0, v236
	v_exp_f32_e32 v231, v231
	v_fma_f32 v227, v229, v227, v227
	v_add_f32_e32 v232, 1.0, v231
	v_rcp_f32_e32 v227, v227
	v_fma_f32 v232, v234, v232, v232
	v_fma_f32 v236, -v236, v227, v227
	v_rcp_f32_e32 v232, v232
	s_nop 0
	v_fma_f32 v231, -v231, v232, v232
	v_cvt_pk_f16_f32 v247, v236, v231
	ds_write_b64 v250, v[246:247] offset:8192
	v_mfma_f32_16x16x32_f16 v[210:213], v[66:69], v[154:157], v[210:213]
	v_mfma_f32_16x16x32_f16 v[214:217], v[78:81], v[154:157], v[214:217]
	buffer_load_dwordx2 v[190:191], v209, s[60:63], s45 offen
	s_add_i32 s45, s45, 0x400000
	s_add_i32 s46, s46, 0x10000
	s_waitcnt lgkmcnt(0)
	s_barrier
	ds_read_b128 v[158:161], v248 offset:0
	ds_read_b128 v[162:165], v248 offset:1024
	ds_read_b128 v[166:169], v249 offset:2048
	ds_read_b128 v[170:173], v249 offset:3072
	v_mfma_f32_16x16x32_f16 v[218:221], v[82:85], v[150:153], v[106:109]
	v_mfma_f32_16x16x32_f16 v[222:225], v[90:93], v[150:153], v[110:113]
	v_mfma_f32_16x16x32_f16 v[218:221], v[86:89], v[154:157], v[218:221]
	v_mfma_f32_16x16x32_f16 v[222:225], v[94:97], v[154:157], v[222:225]
	s_waitcnt lgkmcnt(2)
	v_mfma_f32_16x16x32_f16 v[210:213], v[54:57], v[158:161], v[210:213]
	v_mfma_f32_16x16x32_f16 v[210:213], v[58:61], v[162:165], v[210:213]
	s_waitcnt lgkmcnt(0)
	v_mfma_f32_16x16x32_f16 v[210:213], v[62:65], v[166:169], v[210:213]
	v_mfma_f32_16x16x32_f16 v[210:213], v[50:53], v[170:173], v[210:213]
	s_waitcnt vmcnt(9)
	v_cvt_pk_f16_f32 v251, v196, v197
	ds_write_b32 v1, v251 offset:4096
	ds_read_b128 v[150:153], v186 offset:2048
	ds_read_b128 v[154:157], v186 offset:3072
	v_add_u32_e32 v250, 0x1000, v250
	v_add_u32_e32 v248, 0x1000, v248
	v_add_u32_e32 v249, 0x1000, v249
	v_exp_f32_e32 v226, v210
	v_exp_f32_e32 v227, v211
	v_mfma_f32_16x16x32_f16 v[214:217], v[34:37], v[158:161], v[214:217]
	v_min_f32_e32 v228, s42, v212
	v_exp_f32_e32 v229, v213
	v_mfma_f32_16x16x32_f16 v[214:217], v[38:41], v[162:165], v[214:217]
	v_exp_f32_e32 v228, v228
	v_add_f32_e32 v227, 1.0, v227
	v_mfma_f32_16x16x32_f16 v[214:217], v[42:45], v[166:169], v[214:217]
	v_fma_f32 v230, v228, s41, s41
	v_rcp_f32_e32 v227, v227
	v_mfma_f32_16x16x32_f16 v[214:217], v[46:49], v[170:173], v[214:217]
	v_fma_f32 v230, v226, v230, v230
	v_rcp_f32_e32 v230, v230
	v_mfma_f32_16x16x32_f16 v[218:221], v[18:21], v[158:161], v[218:221]
	v_fma_f32 v226, -v228, v230, v230
	v_fma_f32 v200, v200, v227, v226
	v_mfma_f32_16x16x32_f16 v[218:221], v[14:17], v[162:165], v[218:221]
	v_min_f32_e32 v226, s42, v200
	v_exp_f32_e32 v226, v226
	v_mfma_f32_16x16x32_f16 v[218:221], v[10:13], v[166:169], v[218:221]
	v_add_f32_e32 v227, 1.0, v226
	v_fma_f32 v227, v229, v227, v227
	v_mfma_f32_16x16x32_f16 v[218:221], v[26:29], v[170:173], v[218:221]
	v_rcp_f32_e32 v227, v227
	v_exp_f32_e32 v231, v214
	v_mfma_f32_16x16x32_f16 v[222:225], v[2:5], v[158:161], v[222:225]
	v_exp_f32_e32 v232, v215
	v_fma_f32 v226, -v226, v227, v227
	v_mfma_f32_16x16x32_f16 v[222:225], v[6:9], v[162:165], v[222:225]
	v_min_f32_e32 v233, s42, v216
	v_exp_f32_e32 v234, v217
	v_mfma_f32_16x16x32_f16 v[222:225], v[22:25], v[166:169], v[222:225]
	v_exp_f32_e32 v236, v218
	v_exp_f32_e32 v233, v233
	v_mfma_f32_16x16x32_f16 v[222:225], v[30:33], v[170:173], v[222:225]
	v_add_f32_e32 v232, 1.0, v232
	v_exp_f32_e32 v227, v219
	v_fma_f32 v235, v233, s41, s41
	v_rcp_f32_e32 v232, v232
	v_min_f32_e32 v228, s42, v220
	v_fma_f32 v235, v231, v235, v235
	v_rcp_f32_e32 v235, v235
	v_exp_f32_e32 v229, v221
	v_fma_f32 v231, -v233, v235, v235
	v_fma_f32 v201, v201, v232, v231
	v_exp_f32_e32 v228, v228
	v_min_f32_e32 v231, s42, v201
	v_exp_f32_e32 v231, v231
	v_add_f32_e32 v227, 1.0, v227
	v_add_f32_e32 v232, 1.0, v231
	v_mfma_f32_16x16x32_f16 v[146:149], v[138:141], v[158:161], v[146:149]
	v_fma_f32 v232, v234, v232, v232
	v_fma_f32 v230, v228, s41, s41
	v_rcp_f32_e32 v232, v232
	v_mfma_f32_16x16x32_f16 v[146:149], v[142:145], v[162:165], v[146:149]
	v_fma_f32 v231, -v231, v232, v232
	v_rcp_f32_e32 v227, v227
	v_cvt_pk_f16_f32 v246, v226, v231
	buffer_load_dwordx4 v[138:141], v189, s[68:71], s46 offen
	buffer_load_dwordx4 v[142:145], v208, s[68:71], s46 offen
	v_exp_f32_e32 v231, v222
	v_fma_f32 v230, v236, v230, v230
	v_exp_f32_e32 v232, v223
	s_waitcnt lgkmcnt(0)
	v_mfma_f32_16x16x32_f16 v[210:213], v[70:73], v[150:153], v[98:101]
	v_min_f32_e32 v233, s42, v224
	v_rcp_f32_e32 v230, v230
	v_exp_f32_e32 v234, v225
	v_mfma_f32_16x16x32_f16 v[214:217], v[74:77], v[150:153], v[102:105]
	v_exp_f32_e32 v233, v233
	v_fma_f32 v236, -v228, v230, v230
	v_add_f32_e32 v232, 1.0, v232
	v_fma_f32 v235, v233, s41, s41
	v_fma_f32 v198, v198, v227, v236
	v_rcp_f32_e32 v232, v232
	v_fma_f32 v235, v231, v235, v235
	v_min_f32_e32 v236, s42, v198
	v_rcp_f32_e32 v235, v235
	s_nop 0
	v_fma_f32 v231, -v233, v235, v235
	v_exp_f32_e32 v236, v236
	v_fma_f32 v199, v199, v232, v231
	v_min_f32_e32 v231, s42, v199
	v_add_f32_e32 v227, 1.0, v236
	v_exp_f32_e32 v231, v231
	v_fma_f32 v227, v229, v227, v227
	v_add_f32_e32 v232, 1.0, v231
	v_rcp_f32_e32 v227, v227
	v_fma_f32 v232, v234, v232, v232
	v_fma_f32 v236, -v236, v227, v227
	v_rcp_f32_e32 v232, v232
	s_nop 0
	v_fma_f32 v231, -v231, v232, v232
	v_cvt_pk_f16_f32 v247, v236, v231
	ds_write_b64 v250, v[246:247] offset:8192
	v_mfma_f32_16x16x32_f16 v[210:213], v[66:69], v[154:157], v[210:213]
	v_mfma_f32_16x16x32_f16 v[214:217], v[78:81], v[154:157], v[214:217]
	buffer_load_dwordx2 v[196:197], v209, s[48:51], s45 offen
	s_waitcnt lgkmcnt(0)
	s_barrier
	ds_read_b128 v[158:161], v248 offset:0
	ds_read_b128 v[162:165], v248 offset:1024
	ds_read_b128 v[166:169], v249 offset:2048
	ds_read_b128 v[170:173], v249 offset:3072
	v_mfma_f32_16x16x32_f16 v[218:221], v[82:85], v[150:153], v[106:109]
	v_mfma_f32_16x16x32_f16 v[222:225], v[90:93], v[150:153], v[110:113]
	v_mfma_f32_16x16x32_f16 v[218:221], v[86:89], v[154:157], v[218:221]
	v_mfma_f32_16x16x32_f16 v[222:225], v[94:97], v[154:157], v[222:225]
	s_waitcnt lgkmcnt(2)
	v_mfma_f32_16x16x32_f16 v[210:213], v[54:57], v[158:161], v[210:213]
	v_mfma_f32_16x16x32_f16 v[210:213], v[58:61], v[162:165], v[210:213]
	s_waitcnt lgkmcnt(0)
	v_mfma_f32_16x16x32_f16 v[210:213], v[62:65], v[166:169], v[210:213]
	v_mfma_f32_16x16x32_f16 v[210:213], v[50:53], v[170:173], v[210:213]
	s_waitcnt vmcnt(9)
	v_cvt_pk_f16_f32 v251, v194, v195
	ds_write_b32 v1, v251 offset:6144
	ds_read_b128 v[150:153], v186 offset:4096
	ds_read_b128 v[154:157], v186 offset:5120
	v_add_u32_e32 v250, 0x1000, v250
	v_add_u32_e32 v248, 0x1000, v248
	v_add_u32_e32 v249, 0x1000, v249
	v_exp_f32_e32 v226, v210
	v_exp_f32_e32 v227, v211
	v_mfma_f32_16x16x32_f16 v[214:217], v[34:37], v[158:161], v[214:217]
	v_min_f32_e32 v228, s42, v212
	v_exp_f32_e32 v229, v213
	v_mfma_f32_16x16x32_f16 v[214:217], v[38:41], v[162:165], v[214:217]
	v_exp_f32_e32 v228, v228
	v_add_f32_e32 v227, 1.0, v227
	v_mfma_f32_16x16x32_f16 v[214:217], v[42:45], v[166:169], v[214:217]
	v_fma_f32 v230, v228, s41, s41
	v_rcp_f32_e32 v227, v227
	v_mfma_f32_16x16x32_f16 v[214:217], v[46:49], v[170:173], v[214:217]
	v_fma_f32 v230, v226, v230, v230
	v_rcp_f32_e32 v230, v230
	v_mfma_f32_16x16x32_f16 v[218:221], v[18:21], v[158:161], v[218:221]
	v_fma_f32 v226, -v228, v230, v230
	v_fma_f32 v200, v200, v227, v226
	v_mfma_f32_16x16x32_f16 v[218:221], v[14:17], v[162:165], v[218:221]
	v_min_f32_e32 v226, s42, v200
	v_exp_f32_e32 v226, v226
	v_mfma_f32_16x16x32_f16 v[218:221], v[10:13], v[166:169], v[218:221]
	v_add_f32_e32 v227, 1.0, v226
	v_fma_f32 v227, v229, v227, v227
	v_mfma_f32_16x16x32_f16 v[218:221], v[26:29], v[170:173], v[218:221]
	v_rcp_f32_e32 v227, v227
	v_exp_f32_e32 v231, v214
	v_mfma_f32_16x16x32_f16 v[222:225], v[2:5], v[158:161], v[222:225]
	v_exp_f32_e32 v232, v215
	v_fma_f32 v226, -v226, v227, v227
	v_mfma_f32_16x16x32_f16 v[222:225], v[6:9], v[162:165], v[222:225]
	v_min_f32_e32 v233, s42, v216
	v_exp_f32_e32 v234, v217
	v_mfma_f32_16x16x32_f16 v[222:225], v[22:25], v[166:169], v[222:225]
	v_exp_f32_e32 v236, v218
	v_exp_f32_e32 v233, v233
	v_mfma_f32_16x16x32_f16 v[222:225], v[30:33], v[170:173], v[222:225]
	v_add_f32_e32 v232, 1.0, v232
	v_exp_f32_e32 v227, v219
	v_fma_f32 v235, v233, s41, s41
	v_rcp_f32_e32 v232, v232
	v_min_f32_e32 v228, s42, v220
	v_fma_f32 v235, v231, v235, v235
	v_rcp_f32_e32 v235, v235
	v_exp_f32_e32 v229, v221
	v_fma_f32 v231, -v233, v235, v235
	v_fma_f32 v201, v201, v232, v231
	v_exp_f32_e32 v228, v228
	v_min_f32_e32 v231, s42, v201
	v_exp_f32_e32 v231, v231
	v_add_f32_e32 v227, 1.0, v227
	v_add_f32_e32 v232, 1.0, v231
	v_mfma_f32_16x16x32_f16 v[146:149], v[130:133], v[158:161], v[146:149]
	v_fma_f32 v232, v234, v232, v232
	v_fma_f32 v230, v228, s41, s41
	v_rcp_f32_e32 v232, v232
	v_mfma_f32_16x16x32_f16 v[146:149], v[134:137], v[162:165], v[146:149]
	v_fma_f32 v231, -v231, v232, v232
	v_rcp_f32_e32 v227, v227
	v_cvt_pk_f16_f32 v246, v226, v231
	buffer_load_dwordx4 v[130:133], v189, s[72:75], s46 offen
	buffer_load_dwordx4 v[134:137], v208, s[72:75], s46 offen
	v_exp_f32_e32 v231, v222
	v_fma_f32 v230, v236, v230, v230
	v_exp_f32_e32 v232, v223
	s_waitcnt lgkmcnt(0)
	v_mfma_f32_16x16x32_f16 v[210:213], v[70:73], v[150:153], v[98:101]
	v_min_f32_e32 v233, s42, v224
	v_rcp_f32_e32 v230, v230
	v_exp_f32_e32 v234, v225
	v_mfma_f32_16x16x32_f16 v[214:217], v[74:77], v[150:153], v[102:105]
	v_exp_f32_e32 v233, v233
	v_fma_f32 v236, -v228, v230, v230
	v_add_f32_e32 v232, 1.0, v232
	v_fma_f32 v235, v233, s41, s41
	v_fma_f32 v198, v198, v227, v236
	v_rcp_f32_e32 v232, v232
	v_fma_f32 v235, v231, v235, v235
	v_min_f32_e32 v236, s42, v198
	v_rcp_f32_e32 v235, v235
	s_nop 0
	v_fma_f32 v231, -v233, v235, v235
	v_exp_f32_e32 v236, v236
	v_fma_f32 v199, v199, v232, v231
	v_min_f32_e32 v231, s42, v199
	v_add_f32_e32 v227, 1.0, v236
	v_exp_f32_e32 v231, v231
	v_fma_f32 v227, v229, v227, v227
	v_add_f32_e32 v232, 1.0, v231
	v_rcp_f32_e32 v227, v227
	v_fma_f32 v232, v234, v232, v232
	v_fma_f32 v236, -v236, v227, v227
	v_rcp_f32_e32 v232, v232
	s_nop 0
	v_fma_f32 v231, -v231, v232, v232
	v_cvt_pk_f16_f32 v247, v236, v231
	ds_write_b64 v250, v[246:247] offset:8192
	v_mfma_f32_16x16x32_f16 v[210:213], v[66:69], v[154:157], v[210:213]
	v_mfma_f32_16x16x32_f16 v[214:217], v[78:81], v[154:157], v[214:217]
	buffer_load_dwordx2 v[194:195], v209, s[52:55], s45 offen
	s_waitcnt lgkmcnt(0)
	s_barrier
	ds_read_b128 v[158:161], v248 offset:0
	ds_read_b128 v[162:165], v248 offset:1024
	ds_read_b128 v[166:169], v249 offset:2048
	ds_read_b128 v[170:173], v249 offset:3072
	v_mfma_f32_16x16x32_f16 v[218:221], v[82:85], v[150:153], v[106:109]
	v_mfma_f32_16x16x32_f16 v[222:225], v[90:93], v[150:153], v[110:113]
	v_mfma_f32_16x16x32_f16 v[218:221], v[86:89], v[154:157], v[218:221]
	v_mfma_f32_16x16x32_f16 v[222:225], v[94:97], v[154:157], v[222:225]
	s_waitcnt lgkmcnt(2)
	v_mfma_f32_16x16x32_f16 v[210:213], v[54:57], v[158:161], v[210:213]
	v_mfma_f32_16x16x32_f16 v[210:213], v[58:61], v[162:165], v[210:213]
	s_waitcnt lgkmcnt(0)
	v_mfma_f32_16x16x32_f16 v[210:213], v[62:65], v[166:169], v[210:213]
	v_mfma_f32_16x16x32_f16 v[210:213], v[50:53], v[170:173], v[210:213]
	s_waitcnt vmcnt(9)
	v_cvt_pk_f16_f32 v251, v192, v193
	ds_write_b32 v1, v251 offset:0
	ds_read_b128 v[150:153], v186 offset:6144
	ds_read_b128 v[154:157], v186 offset:7168
	v_add_u32_e32 v250, 0x1000, v250
	v_add_u32_e32 v248, 0x1000, v248
	v_add_u32_e32 v249, 0x1000, v249
	v_exp_f32_e32 v226, v210
	v_exp_f32_e32 v227, v211
	v_mfma_f32_16x16x32_f16 v[214:217], v[34:37], v[158:161], v[214:217]
	v_min_f32_e32 v228, s42, v212
	v_exp_f32_e32 v229, v213
	v_mfma_f32_16x16x32_f16 v[214:217], v[38:41], v[162:165], v[214:217]
	v_exp_f32_e32 v228, v228
	v_add_f32_e32 v227, 1.0, v227
	v_mfma_f32_16x16x32_f16 v[214:217], v[42:45], v[166:169], v[214:217]
	v_fma_f32 v230, v228, s41, s41
	v_rcp_f32_e32 v227, v227
	v_mfma_f32_16x16x32_f16 v[214:217], v[46:49], v[170:173], v[214:217]
	v_fma_f32 v230, v226, v230, v230
	v_rcp_f32_e32 v230, v230
	v_mfma_f32_16x16x32_f16 v[218:221], v[18:21], v[158:161], v[218:221]
	v_fma_f32 v226, -v228, v230, v230
	v_fma_f32 v200, v200, v227, v226
	v_mfma_f32_16x16x32_f16 v[218:221], v[14:17], v[162:165], v[218:221]
	v_min_f32_e32 v226, s42, v200
	v_exp_f32_e32 v226, v226
	v_mfma_f32_16x16x32_f16 v[218:221], v[10:13], v[166:169], v[218:221]
	v_add_f32_e32 v227, 1.0, v226
	v_fma_f32 v227, v229, v227, v227
	v_mfma_f32_16x16x32_f16 v[218:221], v[26:29], v[170:173], v[218:221]
	v_rcp_f32_e32 v227, v227
	v_exp_f32_e32 v231, v214
	v_mfma_f32_16x16x32_f16 v[222:225], v[2:5], v[158:161], v[222:225]
	v_exp_f32_e32 v232, v215
	v_fma_f32 v226, -v226, v227, v227
	v_mfma_f32_16x16x32_f16 v[222:225], v[6:9], v[162:165], v[222:225]
	v_min_f32_e32 v233, s42, v216
	v_exp_f32_e32 v234, v217
	v_mfma_f32_16x16x32_f16 v[222:225], v[22:25], v[166:169], v[222:225]
	v_exp_f32_e32 v236, v218
	v_exp_f32_e32 v233, v233
	v_mfma_f32_16x16x32_f16 v[222:225], v[30:33], v[170:173], v[222:225]
	v_add_f32_e32 v232, 1.0, v232
	v_exp_f32_e32 v227, v219
	v_fma_f32 v235, v233, s41, s41
	v_rcp_f32_e32 v232, v232
	v_min_f32_e32 v228, s42, v220
	v_fma_f32 v235, v231, v235, v235
	v_rcp_f32_e32 v235, v235
	v_exp_f32_e32 v229, v221
	v_fma_f32 v231, -v233, v235, v235
	v_fma_f32 v201, v201, v232, v231
	v_exp_f32_e32 v228, v228
	v_min_f32_e32 v231, s42, v201
	v_exp_f32_e32 v231, v231
	v_add_f32_e32 v227, 1.0, v227
	v_add_f32_e32 v232, 1.0, v231
	v_mfma_f32_16x16x32_f16 v[146:149], v[122:125], v[158:161], v[146:149]
	v_fma_f32 v232, v234, v232, v232
	v_fma_f32 v230, v228, s41, s41
	v_rcp_f32_e32 v232, v232
	v_mfma_f32_16x16x32_f16 v[146:149], v[126:129], v[162:165], v[146:149]
	v_fma_f32 v231, -v231, v232, v232
	v_rcp_f32_e32 v227, v227
	v_cvt_pk_f16_f32 v246, v226, v231
	buffer_load_dwordx4 v[122:125], v189, s[76:79], s46 offen
	buffer_load_dwordx4 v[126:129], v208, s[76:79], s46 offen
	v_exp_f32_e32 v231, v222
	v_fma_f32 v230, v236, v230, v230
	v_exp_f32_e32 v232, v223
	s_waitcnt lgkmcnt(0)
	v_mfma_f32_16x16x32_f16 v[210:213], v[70:73], v[150:153], v[98:101]
	v_min_f32_e32 v233, s42, v224
	v_rcp_f32_e32 v230, v230
	v_exp_f32_e32 v234, v225
	v_mfma_f32_16x16x32_f16 v[214:217], v[74:77], v[150:153], v[102:105]
	v_exp_f32_e32 v233, v233
	v_fma_f32 v236, -v228, v230, v230
	v_add_f32_e32 v232, 1.0, v232
	v_fma_f32 v235, v233, s41, s41
	v_fma_f32 v198, v198, v227, v236
	v_rcp_f32_e32 v232, v232
	v_fma_f32 v235, v231, v235, v235
	v_min_f32_e32 v236, s42, v198
	v_rcp_f32_e32 v235, v235
	s_nop 0
	v_fma_f32 v231, -v233, v235, v235
	v_exp_f32_e32 v236, v236
	v_fma_f32 v199, v199, v232, v231
	v_min_f32_e32 v231, s42, v199
	v_add_f32_e32 v227, 1.0, v236
	v_exp_f32_e32 v231, v231
	v_fma_f32 v227, v229, v227, v227
	v_add_f32_e32 v232, 1.0, v231
	v_rcp_f32_e32 v227, v227
	v_fma_f32 v232, v234, v232, v232
	v_fma_f32 v236, -v236, v227, v227
	v_rcp_f32_e32 v232, v232
	s_nop 0
	v_fma_f32 v231, -v231, v232, v232
	v_cvt_pk_f16_f32 v247, v236, v231
	ds_write_b64 v250, v[246:247] offset:8192
	v_mfma_f32_16x16x32_f16 v[210:213], v[66:69], v[154:157], v[210:213]
	v_mfma_f32_16x16x32_f16 v[214:217], v[78:81], v[154:157], v[214:217]
	buffer_load_dwordx2 v[192:193], v209, s[56:59], s45 offen
	s_waitcnt lgkmcnt(0)
	s_barrier
	ds_read_b128 v[158:161], v248 offset:0
	ds_read_b128 v[162:165], v248 offset:1024
	ds_read_b128 v[166:169], v249 offset:2048
	ds_read_b128 v[170:173], v249 offset:3072
	v_mfma_f32_16x16x32_f16 v[218:221], v[82:85], v[150:153], v[106:109]
	v_mfma_f32_16x16x32_f16 v[222:225], v[90:93], v[150:153], v[110:113]
	v_mfma_f32_16x16x32_f16 v[218:221], v[86:89], v[154:157], v[218:221]
	v_mfma_f32_16x16x32_f16 v[222:225], v[94:97], v[154:157], v[222:225]
	s_waitcnt lgkmcnt(2)
	v_mfma_f32_16x16x32_f16 v[210:213], v[54:57], v[158:161], v[210:213]
	v_mfma_f32_16x16x32_f16 v[210:213], v[58:61], v[162:165], v[210:213]
	s_waitcnt lgkmcnt(0)
	v_mfma_f32_16x16x32_f16 v[210:213], v[62:65], v[166:169], v[210:213]
	v_mfma_f32_16x16x32_f16 v[210:213], v[50:53], v[170:173], v[210:213]
	s_waitcnt vmcnt(9)
	v_cvt_pk_f16_f32 v251, v190, v191
	ds_write_b32 v1, v251 offset:2048
	ds_read_b128 v[150:153], v186 offset:0
	ds_read_b128 v[154:157], v186 offset:1024
	v_add_u32_e32 v250, 0x1000, v250
	v_add_u32_e32 v248, 0x1000, v248
	v_add_u32_e32 v249, 0x1000, v249
	v_exp_f32_e32 v226, v210
	v_exp_f32_e32 v227, v211
	v_mfma_f32_16x16x32_f16 v[214:217], v[34:37], v[158:161], v[214:217]
	v_min_f32_e32 v228, s42, v212
	v_exp_f32_e32 v229, v213
	v_mfma_f32_16x16x32_f16 v[214:217], v[38:41], v[162:165], v[214:217]
	v_exp_f32_e32 v228, v228
	v_add_f32_e32 v227, 1.0, v227
	v_mfma_f32_16x16x32_f16 v[214:217], v[42:45], v[166:169], v[214:217]
	v_fma_f32 v230, v228, s41, s41
	v_rcp_f32_e32 v227, v227
	v_mfma_f32_16x16x32_f16 v[214:217], v[46:49], v[170:173], v[214:217]
	v_fma_f32 v230, v226, v230, v230
	v_rcp_f32_e32 v230, v230
	v_mfma_f32_16x16x32_f16 v[218:221], v[18:21], v[158:161], v[218:221]
	v_fma_f32 v226, -v228, v230, v230
	v_fma_f32 v200, v200, v227, v226
	v_mfma_f32_16x16x32_f16 v[218:221], v[14:17], v[162:165], v[218:221]
	v_min_f32_e32 v226, s42, v200
	v_exp_f32_e32 v226, v226
	v_mfma_f32_16x16x32_f16 v[218:221], v[10:13], v[166:169], v[218:221]
	v_add_f32_e32 v227, 1.0, v226
	v_fma_f32 v227, v229, v227, v227
	v_mfma_f32_16x16x32_f16 v[218:221], v[26:29], v[170:173], v[218:221]
	v_rcp_f32_e32 v227, v227
	v_exp_f32_e32 v231, v214
	v_mfma_f32_16x16x32_f16 v[222:225], v[2:5], v[158:161], v[222:225]
	v_exp_f32_e32 v232, v215
	v_fma_f32 v226, -v226, v227, v227
	v_mfma_f32_16x16x32_f16 v[222:225], v[6:9], v[162:165], v[222:225]
	v_min_f32_e32 v233, s42, v216
	v_exp_f32_e32 v234, v217
	v_mfma_f32_16x16x32_f16 v[222:225], v[22:25], v[166:169], v[222:225]
	v_exp_f32_e32 v236, v218
	v_exp_f32_e32 v233, v233
	v_mfma_f32_16x16x32_f16 v[222:225], v[30:33], v[170:173], v[222:225]
	v_add_f32_e32 v232, 1.0, v232
	v_exp_f32_e32 v227, v219
	v_fma_f32 v235, v233, s41, s41
	v_rcp_f32_e32 v232, v232
	v_min_f32_e32 v228, s42, v220
	v_fma_f32 v235, v231, v235, v235
	v_rcp_f32_e32 v235, v235
	v_exp_f32_e32 v229, v221
	v_fma_f32 v231, -v233, v235, v235
	v_fma_f32 v201, v201, v232, v231
	v_exp_f32_e32 v228, v228
	v_min_f32_e32 v231, s42, v201
	v_exp_f32_e32 v231, v231
	v_add_f32_e32 v227, 1.0, v227
	v_add_f32_e32 v232, 1.0, v231
	v_mfma_f32_16x16x32_f16 v[146:149], v[114:117], v[158:161], v[146:149]
	v_fma_f32 v232, v234, v232, v232
	v_fma_f32 v230, v228, s41, s41
	v_rcp_f32_e32 v232, v232
	v_mfma_f32_16x16x32_f16 v[146:149], v[118:121], v[162:165], v[146:149]
	v_fma_f32 v231, -v231, v232, v232
	v_rcp_f32_e32 v227, v227
	v_cvt_pk_f16_f32 v246, v226, v231
	buffer_load_dwordx4 v[114:117], v189, s[80:83], s46 offen
	buffer_load_dwordx4 v[118:121], v208, s[80:83], s46 offen
	v_exp_f32_e32 v231, v222
	v_fma_f32 v230, v236, v230, v230
	v_exp_f32_e32 v232, v223
	s_waitcnt lgkmcnt(0)
	v_mfma_f32_16x16x32_f16 v[210:213], v[70:73], v[150:153], v[98:101]
	v_min_f32_e32 v233, s42, v224
	v_rcp_f32_e32 v230, v230
	v_exp_f32_e32 v234, v225
	v_mfma_f32_16x16x32_f16 v[214:217], v[74:77], v[150:153], v[102:105]
	v_exp_f32_e32 v233, v233
	v_fma_f32 v236, -v228, v230, v230
	v_add_f32_e32 v232, 1.0, v232
	v_fma_f32 v235, v233, s41, s41
	v_fma_f32 v198, v198, v227, v236
	v_rcp_f32_e32 v232, v232
	v_fma_f32 v235, v231, v235, v235
	v_min_f32_e32 v236, s42, v198
	v_rcp_f32_e32 v235, v235
	s_nop 0
	v_fma_f32 v231, -v233, v235, v235
	v_exp_f32_e32 v236, v236
	v_fma_f32 v199, v199, v232, v231
	v_min_f32_e32 v231, s42, v199
	v_add_f32_e32 v227, 1.0, v236
	v_exp_f32_e32 v231, v231
	v_fma_f32 v227, v229, v227, v227
	v_add_f32_e32 v232, 1.0, v231
	v_rcp_f32_e32 v227, v227
	v_fma_f32 v232, v234, v232, v232
	v_fma_f32 v236, -v236, v227, v227
	v_rcp_f32_e32 v232, v232
	s_nop 0
	v_fma_f32 v231, -v231, v232, v232
	v_cvt_pk_f16_f32 v247, v236, v231
	ds_write_b64 v250, v[246:247] offset:8192
	v_mfma_f32_16x16x32_f16 v[210:213], v[66:69], v[154:157], v[210:213]
	v_mfma_f32_16x16x32_f16 v[214:217], v[78:81], v[154:157], v[214:217]
	buffer_load_dwordx2 v[190:191], v209, s[60:63], s45 offen
	s_add_i32 s45, s45, 0x400000
	s_add_i32 s46, s46, 0x10000
	s_waitcnt lgkmcnt(0)
	s_barrier
	ds_read_b128 v[158:161], v248 offset:0
	ds_read_b128 v[162:165], v248 offset:1024
	ds_read_b128 v[166:169], v249 offset:2048
	ds_read_b128 v[170:173], v249 offset:3072
	v_mfma_f32_16x16x32_f16 v[218:221], v[82:85], v[150:153], v[106:109]
	v_mfma_f32_16x16x32_f16 v[222:225], v[90:93], v[150:153], v[110:113]
	v_mfma_f32_16x16x32_f16 v[218:221], v[86:89], v[154:157], v[218:221]
	v_mfma_f32_16x16x32_f16 v[222:225], v[94:97], v[154:157], v[222:225]
	s_waitcnt lgkmcnt(2)
	v_mfma_f32_16x16x32_f16 v[210:213], v[54:57], v[158:161], v[210:213]
	v_mfma_f32_16x16x32_f16 v[210:213], v[58:61], v[162:165], v[210:213]
	s_waitcnt lgkmcnt(0)
	v_mfma_f32_16x16x32_f16 v[210:213], v[62:65], v[166:169], v[210:213]
	v_mfma_f32_16x16x32_f16 v[210:213], v[50:53], v[170:173], v[210:213]
	s_waitcnt vmcnt(9)
	v_cvt_pk_f16_f32 v251, v196, v197
	ds_write_b32 v1, v251 offset:4096
	ds_read_b128 v[150:153], v186 offset:2048
	ds_read_b128 v[154:157], v186 offset:3072
	v_add_u32_e32 v250, 0x1000, v250
	v_add_u32_e32 v248, 0x1000, v248
	v_add_u32_e32 v249, 0x1000, v249
	v_exp_f32_e32 v226, v210
	v_exp_f32_e32 v227, v211
	v_mfma_f32_16x16x32_f16 v[214:217], v[34:37], v[158:161], v[214:217]
	v_min_f32_e32 v228, s42, v212
	v_exp_f32_e32 v229, v213
	v_mfma_f32_16x16x32_f16 v[214:217], v[38:41], v[162:165], v[214:217]
	v_exp_f32_e32 v228, v228
	v_add_f32_e32 v227, 1.0, v227
	v_mfma_f32_16x16x32_f16 v[214:217], v[42:45], v[166:169], v[214:217]
	v_fma_f32 v230, v228, s41, s41
	v_rcp_f32_e32 v227, v227
	v_mfma_f32_16x16x32_f16 v[214:217], v[46:49], v[170:173], v[214:217]
	v_fma_f32 v230, v226, v230, v230
	v_rcp_f32_e32 v230, v230
	v_mfma_f32_16x16x32_f16 v[218:221], v[18:21], v[158:161], v[218:221]
	v_fma_f32 v226, -v228, v230, v230
	v_fma_f32 v200, v200, v227, v226
	v_mfma_f32_16x16x32_f16 v[218:221], v[14:17], v[162:165], v[218:221]
	v_min_f32_e32 v226, s42, v200
	v_exp_f32_e32 v226, v226
	v_mfma_f32_16x16x32_f16 v[218:221], v[10:13], v[166:169], v[218:221]
	v_add_f32_e32 v227, 1.0, v226
	v_fma_f32 v227, v229, v227, v227
	v_mfma_f32_16x16x32_f16 v[218:221], v[26:29], v[170:173], v[218:221]
	v_rcp_f32_e32 v227, v227
	v_exp_f32_e32 v231, v214
	v_mfma_f32_16x16x32_f16 v[222:225], v[2:5], v[158:161], v[222:225]
	v_exp_f32_e32 v232, v215
	v_fma_f32 v226, -v226, v227, v227
	v_mfma_f32_16x16x32_f16 v[222:225], v[6:9], v[162:165], v[222:225]
	v_min_f32_e32 v233, s42, v216
	v_exp_f32_e32 v234, v217
	v_mfma_f32_16x16x32_f16 v[222:225], v[22:25], v[166:169], v[222:225]
	v_exp_f32_e32 v236, v218
	v_exp_f32_e32 v233, v233
	v_mfma_f32_16x16x32_f16 v[222:225], v[30:33], v[170:173], v[222:225]
	v_add_f32_e32 v232, 1.0, v232
	v_exp_f32_e32 v227, v219
	v_fma_f32 v235, v233, s41, s41
	v_rcp_f32_e32 v232, v232
	v_min_f32_e32 v228, s42, v220
	v_fma_f32 v235, v231, v235, v235
	v_rcp_f32_e32 v235, v235
	v_exp_f32_e32 v229, v221
	v_fma_f32 v231, -v233, v235, v235
	v_fma_f32 v201, v201, v232, v231
	v_exp_f32_e32 v228, v228
	v_min_f32_e32 v231, s42, v201
	v_exp_f32_e32 v231, v231
	v_add_f32_e32 v227, 1.0, v227
	v_add_f32_e32 v232, 1.0, v231
	v_mfma_f32_16x16x32_f16 v[146:149], v[138:141], v[158:161], v[146:149]
	v_fma_f32 v232, v234, v232, v232
	v_fma_f32 v230, v228, s41, s41
	v_rcp_f32_e32 v232, v232
	v_mfma_f32_16x16x32_f16 v[146:149], v[142:145], v[162:165], v[146:149]
	v_fma_f32 v231, -v231, v232, v232
	v_rcp_f32_e32 v227, v227
	v_cvt_pk_f16_f32 v246, v226, v231
	buffer_load_dwordx4 v[138:141], v189, s[68:71], s46 offen
	buffer_load_dwordx4 v[142:145], v208, s[68:71], s46 offen
	v_exp_f32_e32 v231, v222
	v_fma_f32 v230, v236, v230, v230
	v_exp_f32_e32 v232, v223
	s_waitcnt lgkmcnt(0)
	v_mfma_f32_16x16x32_f16 v[210:213], v[70:73], v[150:153], v[98:101]
	v_min_f32_e32 v233, s42, v224
	v_rcp_f32_e32 v230, v230
	v_exp_f32_e32 v234, v225
	v_mfma_f32_16x16x32_f16 v[214:217], v[74:77], v[150:153], v[102:105]
	v_exp_f32_e32 v233, v233
	v_fma_f32 v236, -v228, v230, v230
	v_add_f32_e32 v232, 1.0, v232
	v_fma_f32 v235, v233, s41, s41
	v_fma_f32 v198, v198, v227, v236
	v_rcp_f32_e32 v232, v232
	v_fma_f32 v235, v231, v235, v235
	v_min_f32_e32 v236, s42, v198
	v_rcp_f32_e32 v235, v235
	s_nop 0
	v_fma_f32 v231, -v233, v235, v235
	v_exp_f32_e32 v236, v236
	v_fma_f32 v199, v199, v232, v231
	v_min_f32_e32 v231, s42, v199
	v_add_f32_e32 v227, 1.0, v236
	v_exp_f32_e32 v231, v231
	v_fma_f32 v227, v229, v227, v227
	v_add_f32_e32 v232, 1.0, v231
	v_rcp_f32_e32 v227, v227
	v_fma_f32 v232, v234, v232, v232
	v_fma_f32 v236, -v236, v227, v227
	v_rcp_f32_e32 v232, v232
	s_nop 0
	v_fma_f32 v231, -v231, v232, v232
	v_cvt_pk_f16_f32 v247, v236, v231
	ds_write_b64 v250, v[246:247] offset:8192
	v_mfma_f32_16x16x32_f16 v[210:213], v[66:69], v[154:157], v[210:213]
	v_mfma_f32_16x16x32_f16 v[214:217], v[78:81], v[154:157], v[214:217]
	buffer_load_dwordx2 v[196:197], v209, s[48:51], s45 offen
	s_waitcnt lgkmcnt(0)
	s_barrier
	ds_read_b128 v[158:161], v248 offset:0
	ds_read_b128 v[162:165], v248 offset:1024
	ds_read_b128 v[166:169], v249 offset:2048
	ds_read_b128 v[170:173], v249 offset:3072
	v_mfma_f32_16x16x32_f16 v[218:221], v[82:85], v[150:153], v[106:109]
	v_mfma_f32_16x16x32_f16 v[222:225], v[90:93], v[150:153], v[110:113]
	v_mfma_f32_16x16x32_f16 v[218:221], v[86:89], v[154:157], v[218:221]
	v_mfma_f32_16x16x32_f16 v[222:225], v[94:97], v[154:157], v[222:225]
	s_waitcnt lgkmcnt(2)
	v_mfma_f32_16x16x32_f16 v[210:213], v[54:57], v[158:161], v[210:213]
	v_mfma_f32_16x16x32_f16 v[210:213], v[58:61], v[162:165], v[210:213]
	s_waitcnt lgkmcnt(0)
	v_mfma_f32_16x16x32_f16 v[210:213], v[62:65], v[166:169], v[210:213]
	v_mfma_f32_16x16x32_f16 v[210:213], v[50:53], v[170:173], v[210:213]
	s_waitcnt vmcnt(9)
	v_cvt_pk_f16_f32 v251, v194, v195
	ds_write_b32 v1, v251 offset:6144
	ds_read_b128 v[150:153], v186 offset:4096
	ds_read_b128 v[154:157], v186 offset:5120
	v_add_u32_e32 v250, 0x1000, v250
	v_add_u32_e32 v248, 0x1000, v248
	v_add_u32_e32 v249, 0x1000, v249
	v_exp_f32_e32 v226, v210
	v_exp_f32_e32 v227, v211
	v_mfma_f32_16x16x32_f16 v[214:217], v[34:37], v[158:161], v[214:217]
	v_min_f32_e32 v228, s42, v212
	v_exp_f32_e32 v229, v213
	v_mfma_f32_16x16x32_f16 v[214:217], v[38:41], v[162:165], v[214:217]
	v_exp_f32_e32 v228, v228
	v_add_f32_e32 v227, 1.0, v227
	v_mfma_f32_16x16x32_f16 v[214:217], v[42:45], v[166:169], v[214:217]
	v_fma_f32 v230, v228, s41, s41
	v_rcp_f32_e32 v227, v227
	v_mfma_f32_16x16x32_f16 v[214:217], v[46:49], v[170:173], v[214:217]
	v_fma_f32 v230, v226, v230, v230
	v_rcp_f32_e32 v230, v230
	v_mfma_f32_16x16x32_f16 v[218:221], v[18:21], v[158:161], v[218:221]
	v_fma_f32 v226, -v228, v230, v230
	v_fma_f32 v200, v200, v227, v226
	v_mfma_f32_16x16x32_f16 v[218:221], v[14:17], v[162:165], v[218:221]
	v_min_f32_e32 v226, s42, v200
	v_exp_f32_e32 v226, v226
	v_mfma_f32_16x16x32_f16 v[218:221], v[10:13], v[166:169], v[218:221]
	v_add_f32_e32 v227, 1.0, v226
	v_fma_f32 v227, v229, v227, v227
	v_mfma_f32_16x16x32_f16 v[218:221], v[26:29], v[170:173], v[218:221]
	v_rcp_f32_e32 v227, v227
	v_exp_f32_e32 v231, v214
	v_mfma_f32_16x16x32_f16 v[222:225], v[2:5], v[158:161], v[222:225]
	v_exp_f32_e32 v232, v215
	v_fma_f32 v226, -v226, v227, v227
	v_mfma_f32_16x16x32_f16 v[222:225], v[6:9], v[162:165], v[222:225]
	v_min_f32_e32 v233, s42, v216
	v_exp_f32_e32 v234, v217
	v_mfma_f32_16x16x32_f16 v[222:225], v[22:25], v[166:169], v[222:225]
	v_exp_f32_e32 v236, v218
	v_exp_f32_e32 v233, v233
	v_mfma_f32_16x16x32_f16 v[222:225], v[30:33], v[170:173], v[222:225]
	v_add_f32_e32 v232, 1.0, v232
	v_exp_f32_e32 v227, v219
	v_fma_f32 v235, v233, s41, s41
	v_rcp_f32_e32 v232, v232
	v_min_f32_e32 v228, s42, v220
	v_fma_f32 v235, v231, v235, v235
	v_rcp_f32_e32 v235, v235
	v_exp_f32_e32 v229, v221
	v_fma_f32 v231, -v233, v235, v235
	v_fma_f32 v201, v201, v232, v231
	v_exp_f32_e32 v228, v228
	v_min_f32_e32 v231, s42, v201
	v_exp_f32_e32 v231, v231
	v_add_f32_e32 v227, 1.0, v227
	v_add_f32_e32 v232, 1.0, v231
	v_mfma_f32_16x16x32_f16 v[146:149], v[130:133], v[158:161], v[146:149]
	v_fma_f32 v232, v234, v232, v232
	v_fma_f32 v230, v228, s41, s41
	v_rcp_f32_e32 v232, v232
	v_mfma_f32_16x16x32_f16 v[146:149], v[134:137], v[162:165], v[146:149]
	v_fma_f32 v231, -v231, v232, v232
	v_rcp_f32_e32 v227, v227
	v_cvt_pk_f16_f32 v246, v226, v231
	buffer_load_dwordx4 v[130:133], v189, s[72:75], s46 offen
	buffer_load_dwordx4 v[134:137], v208, s[72:75], s46 offen
	v_exp_f32_e32 v231, v222
	v_fma_f32 v230, v236, v230, v230
	v_exp_f32_e32 v232, v223
	s_waitcnt lgkmcnt(0)
	v_mfma_f32_16x16x32_f16 v[210:213], v[70:73], v[150:153], v[98:101]
	v_min_f32_e32 v233, s42, v224
	v_rcp_f32_e32 v230, v230
	v_exp_f32_e32 v234, v225
	v_mfma_f32_16x16x32_f16 v[214:217], v[74:77], v[150:153], v[102:105]
	v_exp_f32_e32 v233, v233
	v_fma_f32 v236, -v228, v230, v230
	v_add_f32_e32 v232, 1.0, v232
	v_fma_f32 v235, v233, s41, s41
	v_fma_f32 v198, v198, v227, v236
	v_rcp_f32_e32 v232, v232
	v_fma_f32 v235, v231, v235, v235
	v_min_f32_e32 v236, s42, v198
	v_rcp_f32_e32 v235, v235
	s_nop 0
	v_fma_f32 v231, -v233, v235, v235
	v_exp_f32_e32 v236, v236
	v_fma_f32 v199, v199, v232, v231
	v_min_f32_e32 v231, s42, v199
	v_add_f32_e32 v227, 1.0, v236
	v_exp_f32_e32 v231, v231
	v_fma_f32 v227, v229, v227, v227
	v_add_f32_e32 v232, 1.0, v231
	v_rcp_f32_e32 v227, v227
	v_fma_f32 v232, v234, v232, v232
	v_fma_f32 v236, -v236, v227, v227
	v_rcp_f32_e32 v232, v232
	s_nop 0
	v_fma_f32 v231, -v231, v232, v232
	v_cvt_pk_f16_f32 v247, v236, v231
	ds_write_b64 v250, v[246:247] offset:8192
	v_mfma_f32_16x16x32_f16 v[210:213], v[66:69], v[154:157], v[210:213]
	v_mfma_f32_16x16x32_f16 v[214:217], v[78:81], v[154:157], v[214:217]
	buffer_load_dwordx2 v[194:195], v209, s[52:55], s45 offen
	s_waitcnt lgkmcnt(0)
	s_barrier
	s_nop 7
	ds_read_b128 v[158:161], v248 offset:0
	ds_read_b128 v[162:165], v248 offset:1024
	s_lshr_b32 s48, s35, 5
	v_and_b32_e32 v211, 15, v0
	v_bfe_u32 v212, v0, 4, 2
	v_and_b32_e32 v213, 31, v0
	v_bfe_u32 v214, v0, 5, 1
	v_add_u32_e32 v214, s48, v214
	s_lshl_b32 s49, s35, 4
	s_addk_i32 s49, 0x2000
	v_lshl_add_u32 v215, v212, 8, s49
	v_lshl_add_u32 v215, v211, 2, v215
	v_lshlrev_b32_e32 v216, 6, v213
	v_lshl_add_u32 v216, v214, 2, v216
	v_mul_u32_u24_e32 v217, 0x110, v214
	v_lshl_add_u32 v217, v213, 2, v217
	v_mul_u32_u24_e32 v218, 0x110, v211
	v_add_u32_e32 v219, 0x4000, v206
	v_add_u32_e32 v220, 0x14000, v206
	v_add_u32_e32 v221, 0x24000, v206
	v_add_u32_e32 v222, s34, v211
	v_lshlrev_b32_e32 v222, 9, v222
	v_add_u32_e32 v222, s35, v222
	v_lshl_add_u32 v222, v212, 4, v222
	s_waitcnt vmcnt(10) lgkmcnt(0)
	v_mfma_f32_16x16x32_f16 v[146:149], v[122:125], v[158:161], v[146:149]
	v_mfma_f32_16x16x32_f16 v[146:149], v[126:129], v[162:165], v[146:149]
	ds_read_b64 v[30:31], v219 offset:0
	ds_read_b64 v[32:33], v219 offset:4096
	ds_read_b64 v[34:35], v219 offset:8192
	ds_read_b64 v[36:37], v219 offset:12288
	ds_read_b64 v[38:39], v219 offset:16384
	ds_read_b64 v[40:41], v219 offset:20480
	ds_read_b64 v[42:43], v219 offset:24576
	ds_read_b64 v[44:45], v219 offset:28672
	s_waitcnt lgkmcnt(4)
	ds_read_b64 v[46:47], v219 offset:32768
	ds_read_b64 v[48:49], v219 offset:36864
	ds_read_b64 v[50:51], v219 offset:40960
	ds_read_b64 v[52:53], v219 offset:45056
	ds_read_b64 v[54:55], v219 offset:49152
	ds_read_b64 v[56:57], v219 offset:53248
	ds_read_b64 v[58:59], v219 offset:57344
	ds_read_b64 v[60:61], v219 offset:61440
	s_waitcnt lgkmcnt(4)
	ds_read_b64 v[62:63], v220 offset:0
	ds_read_b64 v[64:65], v220 offset:4096
	ds_read_b64 v[66:67], v220 offset:8192
	ds_read_b64 v[68:69], v220 offset:12288
	ds_read_b64 v[70:71], v220 offset:16384
	ds_read_b64 v[72:73], v220 offset:20480
	ds_read_b64 v[74:75], v220 offset:24576
	ds_read_b64 v[76:77], v220 offset:28672
	s_waitcnt lgkmcnt(4)
	ds_read_b64 v[78:79], v220 offset:32768
	ds_read_b64 v[80:81], v220 offset:36864
	ds_read_b64 v[82:83], v220 offset:40960
	ds_read_b64 v[84:85], v220 offset:45056
	ds_read_b64 v[86:87], v220 offset:49152
	ds_read_b64 v[88:89], v220 offset:53248
	ds_read_b64 v[90:91], v220 offset:57344
	ds_read_b64 v[92:93], v220 offset:61440
	s_waitcnt lgkmcnt(4)
	ds_read_b64 v[94:95], v221 offset:0
	ds_read_b64 v[96:97], v221 offset:4096
	ds_read_b64 v[98:99], v221 offset:8192
	ds_read_b64 v[100:101], v221 offset:12288
	ds_write2_b32 v215, v146, v147 offset1:16
	ds_write2_b32 v215, v148, v149 offset0:32 offset1:48
	s_waitcnt lgkmcnt(0)
	s_barrier
	ds_read2st64_b32 v[230:231], v216 offset0:32 offset1:48
	ds_read2st64_b32 v[232:233], v216 offset0:40 offset1:56
	v_cmp_gt_u32_e32 vcc, 18, v213
	s_waitcnt vmcnt(0) lgkmcnt(0)
	v_add_f32_e32 v223, v230, v231
	v_add_f32_e32 v224, v232, v233
	v_add_f32_e32 v223, v223, v254
	v_add_f32_e32 v224, v224, v255
	v_max_f32_e32 v223, 0, v223
	v_max_f32_e32 v224, 0, v224
	v_mov_b32_e32 v226, 0xf149f2ca
	v_cndmask_b32_e32 v224, v226, v224, vcc
	v_max_f32_e32 v225, v223, v224
	s_nop 1
	v_max_f32_dpp v226, v225, v225 quad_perm:[1,0,3,2] row_mask:0xf bank_mask:0xf
	s_nop 1
	v_max_f32_dpp v225, v226, v226 quad_perm:[2,3,0,1] row_mask:0xf bank_mask:0xf
	s_nop 1
	v_max_f32_dpp v226, v225, v225 row_half_mirror row_mask:0xf bank_mask:0xf
	s_nop 1
	v_max_f32_dpp v225, v226, v226 row_mirror row_mask:0xf bank_mask:0xf
	ds_swizzle_b32 v226, v225 offset:swizzle(SWAP,16)
	s_waitcnt lgkmcnt(0)
	v_max_f32_e32 v225, v225, v226
	v_sub_f32_e32 v223, v223, v225
	v_sub_f32_e32 v224, v224, v225
	v_mul_f32_e32 v223, 0x3fb8aa3b, v223
	v_mul_f32_e32 v224, 0x3fb8aa3b, v224
	v_exp_f32_e32 v227, v223
	v_exp_f32_e32 v228, v224
	s_nop 0
	v_add_f32_e32 v229, v227, v228
	s_nop 1
	v_add_f32_dpp v226, v229, v229 quad_perm:[1,0,3,2] row_mask:0xf bank_mask:0xf
	s_nop 1
	v_add_f32_dpp v229, v226, v226 quad_perm:[2,3,0,1] row_mask:0xf bank_mask:0xf
	s_nop 1
	v_add_f32_dpp v226, v229, v229 row_half_mirror row_mask:0xf bank_mask:0xf
	s_nop 1
	v_add_f32_dpp v229, v226, v226 row_mirror row_mask:0xf bank_mask:0xf
	ds_swizzle_b32 v226, v229 offset:swizzle(SWAP,16)
	s_waitcnt lgkmcnt(0)
	v_add_f32_e32 v229, v229, v226
	v_rcp_f32_e32 v234, v229
	s_nop 0
	v_mul_f32_e32 v227, v227, v234
	v_mul_f32_e32 v228, v228, v234
	ds_write_b32 v217, v227
	ds_write_b32 v217, v228 offset:128
	s_waitcnt lgkmcnt(0)
	s_barrier
	ds_read_b128 v[102:105], v218 offset:0
	ds_read_b128 v[106:109], v218 offset:16
	ds_read_b128 v[110:113], v218 offset:32
	ds_read_b128 v[114:117], v218 offset:48
	ds_read_b128 v[118:121], v218 offset:64
	ds_read_b128 v[122:125], v218 offset:80
	ds_read_b128 v[126:129], v218 offset:96
	ds_read_b128 v[130:133], v218 offset:112
	ds_read_b128 v[134:137], v218 offset:128
	ds_read_b128 v[138:141], v218 offset:144
	ds_read_b128 v[142:145], v218 offset:160
	ds_read_b128 v[146:149], v218 offset:176
	ds_read_b128 v[150:153], v218 offset:192
	v_mov_b32_e32 v154, 0
	v_mov_b32_e32 v155, 0
	v_mov_b32_e32 v156, 0
	v_mov_b32_e32 v157, 0
	s_waitcnt vmcnt(0) lgkmcnt(0)
	v_fma_mix_f32 v154, v174, v102, v154 op_sel_hi:[1,0,0]
	v_fma_mix_f32 v155, v174, v102, v155 op_sel:[1,0,0] op_sel_hi:[1,0,0]
	v_fma_mix_f32 v156, v175, v102, v156 op_sel_hi:[1,0,0]
	v_fma_mix_f32 v157, v175, v102, v157 op_sel:[1,0,0] op_sel_hi:[1,0,0]
	v_fma_mix_f32 v154, v176, v103, v154 op_sel_hi:[1,0,0]
	v_fma_mix_f32 v155, v176, v103, v155 op_sel:[1,0,0] op_sel_hi:[1,0,0]
	v_fma_mix_f32 v156, v177, v103, v156 op_sel_hi:[1,0,0]
	v_fma_mix_f32 v157, v177, v103, v157 op_sel:[1,0,0] op_sel_hi:[1,0,0]
	v_fma_mix_f32 v154, v178, v104, v154 op_sel_hi:[1,0,0]
	v_fma_mix_f32 v155, v178, v104, v155 op_sel:[1,0,0] op_sel_hi:[1,0,0]
	v_fma_mix_f32 v156, v179, v104, v156 op_sel_hi:[1,0,0]
	v_fma_mix_f32 v157, v179, v104, v157 op_sel:[1,0,0] op_sel_hi:[1,0,0]
	v_fma_mix_f32 v154, v180, v105, v154 op_sel_hi:[1,0,0]
	v_fma_mix_f32 v155, v180, v105, v155 op_sel:[1,0,0] op_sel_hi:[1,0,0]
	v_fma_mix_f32 v156, v181, v105, v156 op_sel_hi:[1,0,0]
	v_fma_mix_f32 v157, v181, v105, v157 op_sel:[1,0,0] op_sel_hi:[1,0,0]
	v_fma_mix_f32 v154, v182, v106, v154 op_sel_hi:[1,0,0]
	v_fma_mix_f32 v155, v182, v106, v155 op_sel:[1,0,0] op_sel_hi:[1,0,0]
	v_fma_mix_f32 v156, v183, v106, v156 op_sel_hi:[1,0,0]
	v_fma_mix_f32 v157, v183, v106, v157 op_sel:[1,0,0] op_sel_hi:[1,0,0]
	v_fma_mix_f32 v154, v184, v107, v154 op_sel_hi:[1,0,0]
	v_fma_mix_f32 v155, v184, v107, v155 op_sel:[1,0,0] op_sel_hi:[1,0,0]
	v_fma_mix_f32 v156, v185, v107, v156 op_sel_hi:[1,0,0]
	v_fma_mix_f32 v157, v185, v107, v157 op_sel:[1,0,0] op_sel_hi:[1,0,0]
	v_fma_mix_f32 v154, v237, v108, v154 op_sel_hi:[1,0,0]
	v_fma_mix_f32 v155, v237, v108, v155 op_sel:[1,0,0] op_sel_hi:[1,0,0]
	v_fma_mix_f32 v156, v238, v108, v156 op_sel_hi:[1,0,0]
	v_fma_mix_f32 v157, v238, v108, v157 op_sel:[1,0,0] op_sel_hi:[1,0,0]
	v_fma_mix_f32 v154, v239, v109, v154 op_sel_hi:[1,0,0]
	v_fma_mix_f32 v155, v239, v109, v155 op_sel:[1,0,0] op_sel_hi:[1,0,0]
	v_fma_mix_f32 v156, v240, v109, v156 op_sel_hi:[1,0,0]
	v_fma_mix_f32 v157, v240, v109, v157 op_sel:[1,0,0] op_sel_hi:[1,0,0]
	v_fma_mix_f32 v154, v241, v110, v154 op_sel_hi:[1,0,0]
	v_fma_mix_f32 v155, v241, v110, v155 op_sel:[1,0,0] op_sel_hi:[1,0,0]
	v_fma_mix_f32 v156, v242, v110, v156 op_sel_hi:[1,0,0]
	v_fma_mix_f32 v157, v242, v110, v157 op_sel:[1,0,0] op_sel_hi:[1,0,0]
	v_fma_mix_f32 v154, v243, v111, v154 op_sel_hi:[1,0,0]
	v_fma_mix_f32 v155, v243, v111, v155 op_sel:[1,0,0] op_sel_hi:[1,0,0]
	v_fma_mix_f32 v156, v244, v111, v156 op_sel_hi:[1,0,0]
	v_fma_mix_f32 v157, v244, v111, v157 op_sel:[1,0,0] op_sel_hi:[1,0,0]
	v_fma_mix_f32 v154, v245, v112, v154 op_sel_hi:[1,0,0]
	v_fma_mix_f32 v155, v245, v112, v155 op_sel:[1,0,0] op_sel_hi:[1,0,0]
	v_fma_mix_f32 v156, v187, v112, v156 op_sel_hi:[1,0,0]
	v_fma_mix_f32 v157, v187, v112, v157 op_sel:[1,0,0] op_sel_hi:[1,0,0]
	v_fma_mix_f32 v154, v188, v113, v154 op_sel_hi:[1,0,0]
	v_fma_mix_f32 v155, v188, v113, v155 op_sel:[1,0,0] op_sel_hi:[1,0,0]
	v_fma_mix_f32 v156, v202, v113, v156 op_sel_hi:[1,0,0]
	v_fma_mix_f32 v157, v202, v113, v157 op_sel:[1,0,0] op_sel_hi:[1,0,0]
	v_fma_mix_f32 v154, v203, v114, v154 op_sel_hi:[1,0,0]
	v_fma_mix_f32 v155, v203, v114, v155 op_sel:[1,0,0] op_sel_hi:[1,0,0]
	v_fma_mix_f32 v156, v204, v114, v156 op_sel_hi:[1,0,0]
	v_fma_mix_f32 v157, v204, v114, v157 op_sel:[1,0,0] op_sel_hi:[1,0,0]
	v_fma_mix_f32 v154, v205, v115, v154 op_sel_hi:[1,0,0]
	v_fma_mix_f32 v155, v205, v115, v155 op_sel:[1,0,0] op_sel_hi:[1,0,0]
	v_fma_mix_f32 v156, v207, v115, v156 op_sel_hi:[1,0,0]
	v_fma_mix_f32 v157, v207, v115, v157 op_sel:[1,0,0] op_sel_hi:[1,0,0]
	v_fma_mix_f32 v154, v30, v116, v154 op_sel_hi:[1,0,0]
	v_fma_mix_f32 v155, v30, v116, v155 op_sel:[1,0,0] op_sel_hi:[1,0,0]
	v_fma_mix_f32 v156, v31, v116, v156 op_sel_hi:[1,0,0]
	v_fma_mix_f32 v157, v31, v116, v157 op_sel:[1,0,0] op_sel_hi:[1,0,0]
	v_fma_mix_f32 v154, v32, v117, v154 op_sel_hi:[1,0,0]
	v_fma_mix_f32 v155, v32, v117, v155 op_sel:[1,0,0] op_sel_hi:[1,0,0]
	v_fma_mix_f32 v156, v33, v117, v156 op_sel_hi:[1,0,0]
	v_fma_mix_f32 v157, v33, v117, v157 op_sel:[1,0,0] op_sel_hi:[1,0,0]
	v_fma_mix_f32 v154, v34, v118, v154 op_sel_hi:[1,0,0]
	v_fma_mix_f32 v155, v34, v118, v155 op_sel:[1,0,0] op_sel_hi:[1,0,0]
	v_fma_mix_f32 v156, v35, v118, v156 op_sel_hi:[1,0,0]
	v_fma_mix_f32 v157, v35, v118, v157 op_sel:[1,0,0] op_sel_hi:[1,0,0]
	v_fma_mix_f32 v154, v36, v119, v154 op_sel_hi:[1,0,0]
	v_fma_mix_f32 v155, v36, v119, v155 op_sel:[1,0,0] op_sel_hi:[1,0,0]
	v_fma_mix_f32 v156, v37, v119, v156 op_sel_hi:[1,0,0]
	v_fma_mix_f32 v157, v37, v119, v157 op_sel:[1,0,0] op_sel_hi:[1,0,0]
	v_fma_mix_f32 v154, v38, v120, v154 op_sel_hi:[1,0,0]
	v_fma_mix_f32 v155, v38, v120, v155 op_sel:[1,0,0] op_sel_hi:[1,0,0]
	v_fma_mix_f32 v156, v39, v120, v156 op_sel_hi:[1,0,0]
	v_fma_mix_f32 v157, v39, v120, v157 op_sel:[1,0,0] op_sel_hi:[1,0,0]
	v_fma_mix_f32 v154, v40, v121, v154 op_sel_hi:[1,0,0]
	v_fma_mix_f32 v155, v40, v121, v155 op_sel:[1,0,0] op_sel_hi:[1,0,0]
	v_fma_mix_f32 v156, v41, v121, v156 op_sel_hi:[1,0,0]
	v_fma_mix_f32 v157, v41, v121, v157 op_sel:[1,0,0] op_sel_hi:[1,0,0]
	v_fma_mix_f32 v154, v42, v122, v154 op_sel_hi:[1,0,0]
	v_fma_mix_f32 v155, v42, v122, v155 op_sel:[1,0,0] op_sel_hi:[1,0,0]
	v_fma_mix_f32 v156, v43, v122, v156 op_sel_hi:[1,0,0]
	v_fma_mix_f32 v157, v43, v122, v157 op_sel:[1,0,0] op_sel_hi:[1,0,0]
	v_fma_mix_f32 v154, v44, v123, v154 op_sel_hi:[1,0,0]
	v_fma_mix_f32 v155, v44, v123, v155 op_sel:[1,0,0] op_sel_hi:[1,0,0]
	v_fma_mix_f32 v156, v45, v123, v156 op_sel_hi:[1,0,0]
	v_fma_mix_f32 v157, v45, v123, v157 op_sel:[1,0,0] op_sel_hi:[1,0,0]
	v_fma_mix_f32 v154, v46, v124, v154 op_sel_hi:[1,0,0]
	v_fma_mix_f32 v155, v46, v124, v155 op_sel:[1,0,0] op_sel_hi:[1,0,0]
	v_fma_mix_f32 v156, v47, v124, v156 op_sel_hi:[1,0,0]
	v_fma_mix_f32 v157, v47, v124, v157 op_sel:[1,0,0] op_sel_hi:[1,0,0]
	v_fma_mix_f32 v154, v48, v125, v154 op_sel_hi:[1,0,0]
	v_fma_mix_f32 v155, v48, v125, v155 op_sel:[1,0,0] op_sel_hi:[1,0,0]
	v_fma_mix_f32 v156, v49, v125, v156 op_sel_hi:[1,0,0]
	v_fma_mix_f32 v157, v49, v125, v157 op_sel:[1,0,0] op_sel_hi:[1,0,0]
	v_fma_mix_f32 v154, v50, v126, v154 op_sel_hi:[1,0,0]
	v_fma_mix_f32 v155, v50, v126, v155 op_sel:[1,0,0] op_sel_hi:[1,0,0]
	v_fma_mix_f32 v156, v51, v126, v156 op_sel_hi:[1,0,0]
	v_fma_mix_f32 v157, v51, v126, v157 op_sel:[1,0,0] op_sel_hi:[1,0,0]
	v_fma_mix_f32 v154, v52, v127, v154 op_sel_hi:[1,0,0]
	v_fma_mix_f32 v155, v52, v127, v155 op_sel:[1,0,0] op_sel_hi:[1,0,0]
	v_fma_mix_f32 v156, v53, v127, v156 op_sel_hi:[1,0,0]
	v_fma_mix_f32 v157, v53, v127, v157 op_sel:[1,0,0] op_sel_hi:[1,0,0]
	v_fma_mix_f32 v154, v54, v128, v154 op_sel_hi:[1,0,0]
	v_fma_mix_f32 v155, v54, v128, v155 op_sel:[1,0,0] op_sel_hi:[1,0,0]
	v_fma_mix_f32 v156, v55, v128, v156 op_sel_hi:[1,0,0]
	v_fma_mix_f32 v157, v55, v128, v157 op_sel:[1,0,0] op_sel_hi:[1,0,0]
	v_fma_mix_f32 v154, v56, v129, v154 op_sel_hi:[1,0,0]
	v_fma_mix_f32 v155, v56, v129, v155 op_sel:[1,0,0] op_sel_hi:[1,0,0]
	v_fma_mix_f32 v156, v57, v129, v156 op_sel_hi:[1,0,0]
	v_fma_mix_f32 v157, v57, v129, v157 op_sel:[1,0,0] op_sel_hi:[1,0,0]
	v_fma_mix_f32 v154, v58, v130, v154 op_sel_hi:[1,0,0]
	v_fma_mix_f32 v155, v58, v130, v155 op_sel:[1,0,0] op_sel_hi:[1,0,0]
	v_fma_mix_f32 v156, v59, v130, v156 op_sel_hi:[1,0,0]
	v_fma_mix_f32 v157, v59, v130, v157 op_sel:[1,0,0] op_sel_hi:[1,0,0]
	v_fma_mix_f32 v154, v60, v131, v154 op_sel_hi:[1,0,0]
	v_fma_mix_f32 v155, v60, v131, v155 op_sel:[1,0,0] op_sel_hi:[1,0,0]
	v_fma_mix_f32 v156, v61, v131, v156 op_sel_hi:[1,0,0]
	v_fma_mix_f32 v157, v61, v131, v157 op_sel:[1,0,0] op_sel_hi:[1,0,0]
	v_fma_mix_f32 v154, v62, v132, v154 op_sel_hi:[1,0,0]
	v_fma_mix_f32 v155, v62, v132, v155 op_sel:[1,0,0] op_sel_hi:[1,0,0]
	v_fma_mix_f32 v156, v63, v132, v156 op_sel_hi:[1,0,0]
	v_fma_mix_f32 v157, v63, v132, v157 op_sel:[1,0,0] op_sel_hi:[1,0,0]
	v_fma_mix_f32 v154, v64, v133, v154 op_sel_hi:[1,0,0]
	v_fma_mix_f32 v155, v64, v133, v155 op_sel:[1,0,0] op_sel_hi:[1,0,0]
	v_fma_mix_f32 v156, v65, v133, v156 op_sel_hi:[1,0,0]
	v_fma_mix_f32 v157, v65, v133, v157 op_sel:[1,0,0] op_sel_hi:[1,0,0]
	v_fma_mix_f32 v154, v66, v134, v154 op_sel_hi:[1,0,0]
	v_fma_mix_f32 v155, v66, v134, v155 op_sel:[1,0,0] op_sel_hi:[1,0,0]
	v_fma_mix_f32 v156, v67, v134, v156 op_sel_hi:[1,0,0]
	v_fma_mix_f32 v157, v67, v134, v157 op_sel:[1,0,0] op_sel_hi:[1,0,0]
	v_fma_mix_f32 v154, v68, v135, v154 op_sel_hi:[1,0,0]
	v_fma_mix_f32 v155, v68, v135, v155 op_sel:[1,0,0] op_sel_hi:[1,0,0]
	v_fma_mix_f32 v156, v69, v135, v156 op_sel_hi:[1,0,0]
	v_fma_mix_f32 v157, v69, v135, v157 op_sel:[1,0,0] op_sel_hi:[1,0,0]
	v_fma_mix_f32 v154, v70, v136, v154 op_sel_hi:[1,0,0]
	v_fma_mix_f32 v155, v70, v136, v155 op_sel:[1,0,0] op_sel_hi:[1,0,0]
	v_fma_mix_f32 v156, v71, v136, v156 op_sel_hi:[1,0,0]
	v_fma_mix_f32 v157, v71, v136, v157 op_sel:[1,0,0] op_sel_hi:[1,0,0]
	v_fma_mix_f32 v154, v72, v137, v154 op_sel_hi:[1,0,0]
	v_fma_mix_f32 v155, v72, v137, v155 op_sel:[1,0,0] op_sel_hi:[1,0,0]
	v_fma_mix_f32 v156, v73, v137, v156 op_sel_hi:[1,0,0]
	v_fma_mix_f32 v157, v73, v137, v157 op_sel:[1,0,0] op_sel_hi:[1,0,0]
	v_fma_mix_f32 v154, v74, v138, v154 op_sel_hi:[1,0,0]
	v_fma_mix_f32 v155, v74, v138, v155 op_sel:[1,0,0] op_sel_hi:[1,0,0]
	v_fma_mix_f32 v156, v75, v138, v156 op_sel_hi:[1,0,0]
	v_fma_mix_f32 v157, v75, v138, v157 op_sel:[1,0,0] op_sel_hi:[1,0,0]
	v_fma_mix_f32 v154, v76, v139, v154 op_sel_hi:[1,0,0]
	v_fma_mix_f32 v155, v76, v139, v155 op_sel:[1,0,0] op_sel_hi:[1,0,0]
	v_fma_mix_f32 v156, v77, v139, v156 op_sel_hi:[1,0,0]
	v_fma_mix_f32 v157, v77, v139, v157 op_sel:[1,0,0] op_sel_hi:[1,0,0]
	v_fma_mix_f32 v154, v78, v140, v154 op_sel_hi:[1,0,0]
	v_fma_mix_f32 v155, v78, v140, v155 op_sel:[1,0,0] op_sel_hi:[1,0,0]
	v_fma_mix_f32 v156, v79, v140, v156 op_sel_hi:[1,0,0]
	v_fma_mix_f32 v157, v79, v140, v157 op_sel:[1,0,0] op_sel_hi:[1,0,0]
	v_fma_mix_f32 v154, v80, v141, v154 op_sel_hi:[1,0,0]
	v_fma_mix_f32 v155, v80, v141, v155 op_sel:[1,0,0] op_sel_hi:[1,0,0]
	v_fma_mix_f32 v156, v81, v141, v156 op_sel_hi:[1,0,0]
	v_fma_mix_f32 v157, v81, v141, v157 op_sel:[1,0,0] op_sel_hi:[1,0,0]
	v_fma_mix_f32 v154, v82, v142, v154 op_sel_hi:[1,0,0]
	v_fma_mix_f32 v155, v82, v142, v155 op_sel:[1,0,0] op_sel_hi:[1,0,0]
	v_fma_mix_f32 v156, v83, v142, v156 op_sel_hi:[1,0,0]
	v_fma_mix_f32 v157, v83, v142, v157 op_sel:[1,0,0] op_sel_hi:[1,0,0]
	v_fma_mix_f32 v154, v84, v143, v154 op_sel_hi:[1,0,0]
	v_fma_mix_f32 v155, v84, v143, v155 op_sel:[1,0,0] op_sel_hi:[1,0,0]
	v_fma_mix_f32 v156, v85, v143, v156 op_sel_hi:[1,0,0]
	v_fma_mix_f32 v157, v85, v143, v157 op_sel:[1,0,0] op_sel_hi:[1,0,0]
	v_fma_mix_f32 v154, v86, v144, v154 op_sel_hi:[1,0,0]
	v_fma_mix_f32 v155, v86, v144, v155 op_sel:[1,0,0] op_sel_hi:[1,0,0]
	v_fma_mix_f32 v156, v87, v144, v156 op_sel_hi:[1,0,0]
	v_fma_mix_f32 v157, v87, v144, v157 op_sel:[1,0,0] op_sel_hi:[1,0,0]
	v_fma_mix_f32 v154, v88, v145, v154 op_sel_hi:[1,0,0]
	v_fma_mix_f32 v155, v88, v145, v155 op_sel:[1,0,0] op_sel_hi:[1,0,0]
	v_fma_mix_f32 v156, v89, v145, v156 op_sel_hi:[1,0,0]
	v_fma_mix_f32 v157, v89, v145, v157 op_sel:[1,0,0] op_sel_hi:[1,0,0]
	v_fma_mix_f32 v154, v90, v146, v154 op_sel_hi:[1,0,0]
	v_fma_mix_f32 v155, v90, v146, v155 op_sel:[1,0,0] op_sel_hi:[1,0,0]
	v_fma_mix_f32 v156, v91, v146, v156 op_sel_hi:[1,0,0]
	v_fma_mix_f32 v157, v91, v146, v157 op_sel:[1,0,0] op_sel_hi:[1,0,0]
	v_fma_mix_f32 v154, v92, v147, v154 op_sel_hi:[1,0,0]
	v_fma_mix_f32 v155, v92, v147, v155 op_sel:[1,0,0] op_sel_hi:[1,0,0]
	v_fma_mix_f32 v156, v93, v147, v156 op_sel_hi:[1,0,0]
	v_fma_mix_f32 v157, v93, v147, v157 op_sel:[1,0,0] op_sel_hi:[1,0,0]
	v_fma_mix_f32 v154, v94, v148, v154 op_sel_hi:[1,0,0]
	v_fma_mix_f32 v155, v94, v148, v155 op_sel:[1,0,0] op_sel_hi:[1,0,0]
	v_fma_mix_f32 v156, v95, v148, v156 op_sel_hi:[1,0,0]
	v_fma_mix_f32 v157, v95, v148, v157 op_sel:[1,0,0] op_sel_hi:[1,0,0]
	v_fma_mix_f32 v154, v96, v149, v154 op_sel_hi:[1,0,0]
	v_fma_mix_f32 v155, v96, v149, v155 op_sel:[1,0,0] op_sel_hi:[1,0,0]
	v_fma_mix_f32 v156, v97, v149, v156 op_sel_hi:[1,0,0]
	v_fma_mix_f32 v157, v97, v149, v157 op_sel:[1,0,0] op_sel_hi:[1,0,0]
	v_fma_mix_f32 v154, v98, v150, v154 op_sel_hi:[1,0,0]
	v_fma_mix_f32 v155, v98, v150, v155 op_sel:[1,0,0] op_sel_hi:[1,0,0]
	v_fma_mix_f32 v156, v99, v150, v156 op_sel_hi:[1,0,0]
	v_fma_mix_f32 v157, v99, v150, v157 op_sel:[1,0,0] op_sel_hi:[1,0,0]
	v_fma_mix_f32 v154, v100, v151, v154 op_sel_hi:[1,0,0]
	v_fma_mix_f32 v155, v100, v151, v155 op_sel:[1,0,0] op_sel_hi:[1,0,0]
	v_fma_mix_f32 v156, v101, v151, v156 op_sel_hi:[1,0,0]
	v_fma_mix_f32 v157, v101, v151, v157 op_sel:[1,0,0] op_sel_hi:[1,0,0]
	global_store_dwordx4 v222, v[154:157], s[8:9]
	s_endpgm
